# mid-segment s_setprio 0/1 flip pairs removed from the MMA segments (one raise at segment start, one drop at its end)
# speedup vs baseline: 1.0016x; 1.0016x over previous
.LBB0_216:
	s_waitcnt lgkmcnt(0)
	s_add_i32 s33, s92, 0x100
	s_add_i32 s66, s93, 0x100
	s_barrier
	s_setprio 1
	s_waitcnt lgkmcnt(7)
	v_mfma_f32_16x16x32_bf16 v[124:127], v[156:159], v[188:191], 0
	s_waitcnt lgkmcnt(6)
	v_mfma_f32_16x16x32_bf16 v[124:127], v[152:155], v[184:187], v[124:127]
	v_mfma_f32_16x16x32_bf16 v[120:123], v[148:151], v[188:191], 0
	s_nop 0
	v_mfma_f32_16x16x32_bf16 v[120:123], v[144:147], v[184:187], v[120:123]
	s_waitcnt lgkmcnt(5)
	v_mfma_f32_16x16x32_bf16 v[116:119], v[156:159], v[180:183], 0
	s_waitcnt lgkmcnt(4)
	v_mfma_f32_16x16x32_bf16 v[116:119], v[152:155], v[176:179], v[116:119]
	v_mfma_f32_16x16x32_bf16 v[112:115], v[148:151], v[180:183], 0
	s_nop 0
	v_mfma_f32_16x16x32_bf16 v[112:115], v[144:147], v[176:179], v[112:115]
	s_waitcnt lgkmcnt(3)
	v_mfma_f32_16x16x32_bf16 v[108:111], v[156:159], v[172:175], 0
	s_waitcnt lgkmcnt(2)
	v_mfma_f32_16x16x32_bf16 v[108:111], v[152:155], v[168:171], v[108:111]
	v_mfma_f32_16x16x32_bf16 v[104:107], v[148:151], v[172:175], 0
	s_nop 0
	v_mfma_f32_16x16x32_bf16 v[104:107], v[144:147], v[168:171], v[104:107]
	s_waitcnt lgkmcnt(1)
	v_mfma_f32_16x16x32_bf16 v[100:103], v[156:159], v[164:167], 0
	s_waitcnt lgkmcnt(0)
	v_mfma_f32_16x16x32_bf16 v[100:103], v[152:155], v[160:163], v[100:103]
	v_mfma_f32_16x16x32_bf16 v[96:99], v[148:151], v[164:167], 0
	s_nop 0
	v_mfma_f32_16x16x32_bf16 v[96:99], v[144:147], v[160:163], v[96:99]
	v_mfma_f32_16x16x32_bf16 v[92:95], v[140:143], v[188:191], 0
	s_nop 0
	v_mfma_f32_16x16x32_bf16 v[92:95], v[136:139], v[184:187], v[92:95]
	v_mfma_f32_16x16x32_bf16 v[88:91], v[132:135], v[188:191], 0
	s_nop 0
	v_mfma_f32_16x16x32_bf16 v[88:91], v[128:131], v[184:187], v[88:91]
	v_mfma_f32_16x16x32_bf16 v[84:87], v[140:143], v[180:183], 0
	s_nop 0
	v_mfma_f32_16x16x32_bf16 v[84:87], v[136:139], v[176:179], v[84:87]
	v_mfma_f32_16x16x32_bf16 v[80:83], v[132:135], v[180:183], 0
	s_nop 0
	v_mfma_f32_16x16x32_bf16 v[80:83], v[128:131], v[176:179], v[80:83]
	v_mfma_f32_16x16x32_bf16 v[76:79], v[140:143], v[172:175], 0
	s_nop 0
	v_mfma_f32_16x16x32_bf16 v[76:79], v[136:139], v[168:171], v[76:79]
	v_mfma_f32_16x16x32_bf16 v[72:75], v[132:135], v[172:175], 0
	s_nop 0
	v_mfma_f32_16x16x32_bf16 v[72:75], v[128:131], v[168:171], v[72:75]
	v_mfma_f32_16x16x32_bf16 v[68:71], v[140:143], v[164:167], 0
	s_nop 0
	v_mfma_f32_16x16x32_bf16 v[68:71], v[136:139], v[160:163], v[68:71]
	v_mfma_f32_16x16x32_bf16 v[64:67], v[132:135], v[164:167], 0
	s_nop 0
	v_mfma_f32_16x16x32_bf16 v[64:67], v[128:131], v[160:163], v[64:67]
	s_setprio 0
	s_barrier
	s_mov_b32 m0, s62
	s_mov_b32 s14, s10
	s_mov_b32 s15, s11
	buffer_load_dwordx4 v202, s[12:15], s66 offen lds
	s_add_i32 s66, s93, 0x80100
	s_mov_b32 m0, s63
	s_and_b64 vcc, exec, s[4:5]
	buffer_load_dwordx4 v202, s[12:15], s66 offen lds
	s_add_i32 s66, s93, 0x8100
	s_mov_b32 m0, s64
	s_nop 0
	buffer_load_dwordx4 v202, s[12:15], s66 offen lds
	s_add_i32 s66, s93, 0x88100
	s_mov_b32 m0, s65
	s_nop 0
	buffer_load_dwordx4 v202, s[12:15], s66 offen lds
	s_mov_b32 m0, s45
	s_add_i32 s14, s92, 0x10100
	buffer_load_dwordx4 v196, s[8:11], s33 offen lds
	s_mov_b32 m0, s68
	s_nop 0
	buffer_load_dwordx4 v196, s[8:11], s14 offen lds
	ds_read_b128 v[188:191], v219 offset:16384
	ds_read_b128 v[184:187], v219 offset:17408
	ds_read_b128 v[180:183], v219 offset:18432
	ds_read_b128 v[176:179], v219 offset:19456
	ds_read_b128 v[172:175], v219 offset:20480
	ds_read_b128 v[168:171], v219 offset:21504
	ds_read_b128 v[164:167], v219 offset:22528
	ds_read_b128 v[160:163], v219 offset:23552
	s_cbranch_vccz .LBB0_227
	s_waitcnt vmcnt(24)
	s_cbranch_execnz .LBB0_219

.LBB0_219:
	s_waitcnt lgkmcnt(0)
	s_add_i32 s4, s92, 0x180
	s_add_i32 s5, s93, 0x180
	s_barrier
	s_setprio 1
	s_waitcnt lgkmcnt(7)
	v_mfma_f32_16x16x32_bf16 v[60:63], v[156:159], v[188:191], 0
	s_waitcnt lgkmcnt(6)
	v_mfma_f32_16x16x32_bf16 v[60:63], v[152:155], v[184:187], v[60:63]
	v_mfma_f32_16x16x32_bf16 v[56:59], v[148:151], v[188:191], 0
	s_nop 0
	v_mfma_f32_16x16x32_bf16 v[56:59], v[144:147], v[184:187], v[56:59]
	s_waitcnt lgkmcnt(5)
	v_mfma_f32_16x16x32_bf16 v[52:55], v[156:159], v[180:183], 0
	s_waitcnt lgkmcnt(4)
	v_mfma_f32_16x16x32_bf16 v[52:55], v[152:155], v[176:179], v[52:55]
	v_mfma_f32_16x16x32_bf16 v[48:51], v[148:151], v[180:183], 0
	s_nop 0
	v_mfma_f32_16x16x32_bf16 v[48:51], v[144:147], v[176:179], v[48:51]
	s_waitcnt lgkmcnt(3)
	v_mfma_f32_16x16x32_bf16 v[44:47], v[156:159], v[172:175], 0
	s_waitcnt lgkmcnt(2)
	v_mfma_f32_16x16x32_bf16 v[44:47], v[152:155], v[168:171], v[44:47]
	v_mfma_f32_16x16x32_bf16 v[40:43], v[148:151], v[172:175], 0
	s_nop 0
	v_mfma_f32_16x16x32_bf16 v[40:43], v[144:147], v[168:171], v[40:43]
	s_waitcnt lgkmcnt(1)
	v_mfma_f32_16x16x32_bf16 v[36:39], v[156:159], v[164:167], 0
	s_waitcnt lgkmcnt(0)
	v_mfma_f32_16x16x32_bf16 v[36:39], v[152:155], v[160:163], v[36:39]
	v_mfma_f32_16x16x32_bf16 v[32:35], v[148:151], v[164:167], 0
	s_nop 0
	v_mfma_f32_16x16x32_bf16 v[32:35], v[144:147], v[160:163], v[32:35]
	v_mfma_f32_16x16x32_bf16 v[28:31], v[140:143], v[188:191], 0
	s_nop 0
	v_mfma_f32_16x16x32_bf16 v[28:31], v[136:139], v[184:187], v[28:31]
	v_mfma_f32_16x16x32_bf16 v[24:27], v[132:135], v[188:191], 0
	s_nop 0
	v_mfma_f32_16x16x32_bf16 v[24:27], v[128:131], v[184:187], v[24:27]
	v_mfma_f32_16x16x32_bf16 v[20:23], v[140:143], v[180:183], 0
	s_nop 0
	v_mfma_f32_16x16x32_bf16 v[20:23], v[136:139], v[176:179], v[20:23]
	v_mfma_f32_16x16x32_bf16 v[16:19], v[132:135], v[180:183], 0
	s_nop 0
	v_mfma_f32_16x16x32_bf16 v[16:19], v[128:131], v[176:179], v[16:19]
	v_mfma_f32_16x16x32_bf16 v[12:15], v[140:143], v[172:175], 0
	s_nop 0
	v_mfma_f32_16x16x32_bf16 v[12:15], v[136:139], v[168:171], v[12:15]
	v_mfma_f32_16x16x32_bf16 v[8:11], v[132:135], v[172:175], 0
	s_nop 0
	v_mfma_f32_16x16x32_bf16 v[8:11], v[128:131], v[168:171], v[8:11]
	v_mfma_f32_16x16x32_bf16 v[4:7], v[140:143], v[164:167], 0
	s_nop 0
	v_mfma_f32_16x16x32_bf16 v[4:7], v[136:139], v[160:163], v[4:7]
	v_mfma_f32_16x16x32_bf16 v[0:3], v[132:135], v[164:167], 0
	s_nop 0
	v_mfma_f32_16x16x32_bf16 v[0:3], v[128:131], v[160:163], v[0:3]
	s_setprio 0
	s_barrier
	ds_read_b128 v[156:159], v211
	ds_read_b128 v[152:155], v212
	ds_read_b128 v[148:151], v213
	ds_read_b128 v[144:147], v214
	ds_read_b128 v[140:143], v215
	ds_read_b128 v[136:139], v216
	ds_read_b128 v[132:135], v217
	ds_read_b128 v[128:131], v218
	ds_read_b128 v[160:163], v219 offset:32768
	ds_read_b128 v[164:167], v219 offset:33792
	ds_read_b128 v[168:171], v219 offset:34816
	ds_read_b128 v[172:175], v219 offset:35840
	ds_read_b128 v[176:179], v219 offset:36864
	ds_read_b128 v[180:183], v219 offset:37888
	ds_read_b128 v[184:187], v219 offset:38912
	ds_read_b128 v[188:191], v219 offset:39936
	s_mov_b32 m0, s69
	s_add_i32 s14, s92, 0x20100
	buffer_load_dwordx4 v196, s[8:11], s14 offen lds
	s_add_i32 s14, s92, 0x30100
	s_mov_b32 m0, s70
	s_nop 0
	buffer_load_dwordx4 v196, s[8:11], s14 offen lds
	s_waitcnt vmcnt(8)
	s_waitcnt lgkmcnt(8)
	s_barrier
	s_setprio 1
	s_waitcnt lgkmcnt(7)
	v_mfma_f32_16x16x32_bf16 v[124:127], v[156:159], v[160:163], v[124:127]
	s_waitcnt lgkmcnt(6)
	v_mfma_f32_16x16x32_bf16 v[124:127], v[152:155], v[164:167], v[124:127]
	v_mfma_f32_16x16x32_bf16 v[120:123], v[148:151], v[160:163], v[120:123]
	s_nop 0
	v_mfma_f32_16x16x32_bf16 v[120:123], v[144:147], v[164:167], v[120:123]
	s_waitcnt lgkmcnt(5)
	v_mfma_f32_16x16x32_bf16 v[116:119], v[156:159], v[168:171], v[116:119]
	s_waitcnt lgkmcnt(4)
	v_mfma_f32_16x16x32_bf16 v[116:119], v[152:155], v[172:175], v[116:119]
	v_mfma_f32_16x16x32_bf16 v[112:115], v[148:151], v[168:171], v[112:115]
	s_nop 0
	v_mfma_f32_16x16x32_bf16 v[112:115], v[144:147], v[172:175], v[112:115]
	s_waitcnt lgkmcnt(3)
	v_mfma_f32_16x16x32_bf16 v[108:111], v[156:159], v[176:179], v[108:111]
	s_waitcnt lgkmcnt(2)
	v_mfma_f32_16x16x32_bf16 v[108:111], v[152:155], v[180:183], v[108:111]
	v_mfma_f32_16x16x32_bf16 v[104:107], v[148:151], v[176:179], v[104:107]
	s_nop 0
	v_mfma_f32_16x16x32_bf16 v[104:107], v[144:147], v[180:183], v[104:107]
	s_waitcnt lgkmcnt(1)
	v_mfma_f32_16x16x32_bf16 v[100:103], v[156:159], v[184:187], v[100:103]
	s_waitcnt lgkmcnt(0)
	v_mfma_f32_16x16x32_bf16 v[100:103], v[152:155], v[188:191], v[100:103]
	v_mfma_f32_16x16x32_bf16 v[96:99], v[148:151], v[184:187], v[96:99]
	s_nop 0
	v_mfma_f32_16x16x32_bf16 v[96:99], v[144:147], v[188:191], v[96:99]
	v_mfma_f32_16x16x32_bf16 v[92:95], v[140:143], v[160:163], v[92:95]
	s_nop 0
	v_mfma_f32_16x16x32_bf16 v[92:95], v[136:139], v[164:167], v[92:95]
	v_mfma_f32_16x16x32_bf16 v[88:91], v[132:135], v[160:163], v[88:91]
	s_nop 0
	v_mfma_f32_16x16x32_bf16 v[88:91], v[128:131], v[164:167], v[88:91]
	v_mfma_f32_16x16x32_bf16 v[84:87], v[140:143], v[168:171], v[84:87]
	s_nop 0
	v_mfma_f32_16x16x32_bf16 v[84:87], v[136:139], v[172:175], v[84:87]
	v_mfma_f32_16x16x32_bf16 v[80:83], v[132:135], v[168:171], v[80:83]
	s_nop 0
	v_mfma_f32_16x16x32_bf16 v[80:83], v[128:131], v[172:175], v[80:83]
	v_mfma_f32_16x16x32_bf16 v[76:79], v[140:143], v[176:179], v[76:79]
	s_nop 0
	v_mfma_f32_16x16x32_bf16 v[76:79], v[136:139], v[180:183], v[76:79]
	v_mfma_f32_16x16x32_bf16 v[72:75], v[132:135], v[176:179], v[72:75]
	s_nop 0
	v_mfma_f32_16x16x32_bf16 v[72:75], v[128:131], v[180:183], v[72:75]
	v_mfma_f32_16x16x32_bf16 v[68:71], v[140:143], v[184:187], v[68:71]
	s_nop 0
	v_mfma_f32_16x16x32_bf16 v[68:71], v[136:139], v[188:191], v[68:71]
	v_mfma_f32_16x16x32_bf16 v[64:67], v[132:135], v[184:187], v[64:67]
	s_nop 0
	v_mfma_f32_16x16x32_bf16 v[64:67], v[128:131], v[188:191], v[64:67]
	s_setprio 0
	s_barrier
	ds_read_b128 v[160:163], v219 offset:49152
	ds_read_b128 v[164:167], v219 offset:50176
	ds_read_b128 v[168:171], v219 offset:51200
	ds_read_b128 v[172:175], v219 offset:52224
	ds_read_b128 v[176:179], v219 offset:53248
	ds_read_b128 v[180:183], v219 offset:54272
	ds_read_b128 v[184:187], v219 offset:55296
	ds_read_b128 v[188:191], v219 offset:56320
	s_mov_b32 m0, s73
	s_mov_b32 s14, s10
	s_mov_b32 s15, s11
	buffer_load_dwordx4 v202, s[12:15], s5 offen lds
	s_add_i32 s5, s93, 0x80180
	s_mov_b32 m0, s74
	s_nop 0
	buffer_load_dwordx4 v202, s[12:15], s5 offen lds
	s_add_i32 s5, s93, 0x8180
	s_mov_b32 m0, s77
	s_nop 0
	buffer_load_dwordx4 v202, s[12:15], s5 offen lds
	s_add_i32 s5, s93, 0x88180
	s_mov_b32 m0, s78
	s_nop 0
	buffer_load_dwordx4 v202, s[12:15], s5 offen lds
	s_mov_b32 m0, s75
	s_nop 0
	buffer_load_dwordx4 v196, s[8:11], s4 offen lds
	s_add_i32 s4, s92, 0x10180
	s_mov_b32 m0, s76
	s_nop 0
	buffer_load_dwordx4 v196, s[8:11], s4 offen lds
	s_waitcnt vmcnt(8)
	s_waitcnt lgkmcnt(6)
	s_barrier
	s_setprio 1
	s_waitcnt lgkmcnt(7)
	v_mfma_f32_16x16x32_bf16 v[60:63], v[156:159], v[160:163], v[60:63]
	s_waitcnt lgkmcnt(6)
	v_mfma_f32_16x16x32_bf16 v[60:63], v[152:155], v[164:167], v[60:63]
	v_mfma_f32_16x16x32_bf16 v[56:59], v[148:151], v[160:163], v[56:59]
	s_nop 0
	v_mfma_f32_16x16x32_bf16 v[56:59], v[144:147], v[164:167], v[56:59]
	s_waitcnt lgkmcnt(5)
	v_mfma_f32_16x16x32_bf16 v[52:55], v[156:159], v[168:171], v[52:55]
	s_waitcnt lgkmcnt(4)
	v_mfma_f32_16x16x32_bf16 v[52:55], v[152:155], v[172:175], v[52:55]
	v_mfma_f32_16x16x32_bf16 v[48:51], v[148:151], v[168:171], v[48:51]
	s_nop 0
	v_mfma_f32_16x16x32_bf16 v[48:51], v[144:147], v[172:175], v[48:51]
	s_waitcnt lgkmcnt(3)
	v_mfma_f32_16x16x32_bf16 v[44:47], v[156:159], v[176:179], v[44:47]
	s_waitcnt lgkmcnt(2)
	v_mfma_f32_16x16x32_bf16 v[44:47], v[152:155], v[180:183], v[44:47]
	v_mfma_f32_16x16x32_bf16 v[40:43], v[148:151], v[176:179], v[40:43]
	s_nop 0
	v_mfma_f32_16x16x32_bf16 v[40:43], v[144:147], v[180:183], v[40:43]
	s_waitcnt lgkmcnt(1)
	v_mfma_f32_16x16x32_bf16 v[36:39], v[156:159], v[184:187], v[36:39]
	s_waitcnt lgkmcnt(0)
	v_mfma_f32_16x16x32_bf16 v[36:39], v[152:155], v[188:191], v[36:39]
	v_mfma_f32_16x16x32_bf16 v[32:35], v[148:151], v[184:187], v[32:35]
	s_nop 0
	v_mfma_f32_16x16x32_bf16 v[32:35], v[144:147], v[188:191], v[32:35]
	v_mfma_f32_16x16x32_bf16 v[28:31], v[140:143], v[160:163], v[28:31]
	s_nop 0
	v_mfma_f32_16x16x32_bf16 v[28:31], v[136:139], v[164:167], v[28:31]
	v_mfma_f32_16x16x32_bf16 v[24:27], v[132:135], v[160:163], v[24:27]
	s_nop 0
	v_mfma_f32_16x16x32_bf16 v[24:27], v[128:131], v[164:167], v[24:27]
	v_mfma_f32_16x16x32_bf16 v[20:23], v[140:143], v[168:171], v[20:23]
	s_nop 0
	v_mfma_f32_16x16x32_bf16 v[20:23], v[136:139], v[172:175], v[20:23]
	v_mfma_f32_16x16x32_bf16 v[16:19], v[132:135], v[168:171], v[16:19]
	s_nop 0
	v_mfma_f32_16x16x32_bf16 v[16:19], v[128:131], v[172:175], v[16:19]
	v_mfma_f32_16x16x32_bf16 v[12:15], v[140:143], v[176:179], v[12:15]
	s_nop 0
	v_mfma_f32_16x16x32_bf16 v[12:15], v[136:139], v[180:183], v[12:15]
	v_mfma_f32_16x16x32_bf16 v[8:11], v[132:135], v[176:179], v[8:11]
	s_nop 0
	v_mfma_f32_16x16x32_bf16 v[8:11], v[128:131], v[180:183], v[8:11]
	v_mfma_f32_16x16x32_bf16 v[4:7], v[140:143], v[184:187], v[4:7]
	s_nop 0
	v_mfma_f32_16x16x32_bf16 v[4:7], v[136:139], v[188:191], v[4:7]
	v_mfma_f32_16x16x32_bf16 v[0:3], v[132:135], v[184:187], v[0:3]
	s_nop 0
	v_mfma_f32_16x16x32_bf16 v[0:3], v[128:131], v[188:191], v[0:3]
	s_setprio 0
	s_barrier
	s_add_i32 s4, s92, 0x30180
	s_add_i32 s5, s93, 0x200
	s_mov_b32 s33, 0
.LBB0_220:
	ds_read_b128 v[128:131], v203
	ds_read_b128 v[132:135], v204
	ds_read_b128 v[136:139], v205
	ds_read_b128 v[140:143], v206
	ds_read_b128 v[144:147], v207
	ds_read_b128 v[148:151], v208
	ds_read_b128 v[152:155], v209
	ds_read_b128 v[156:159], v210
	ds_read_b128 v[160:163], v219
	ds_read_b128 v[164:167], v219 offset:1024
	ds_read_b128 v[168:171], v219 offset:2048
	ds_read_b128 v[172:175], v219 offset:3072
	ds_read_b128 v[176:179], v219 offset:4096
	ds_read_b128 v[180:183], v219 offset:5120
	ds_read_b128 v[184:187], v219 offset:6144
	ds_read_b128 v[188:191], v219 offset:7168
	s_add_i32 s66, s4, 0xfffd0080
	s_cmp_eq_u32 s33, 4
	s_cselect_b32 s66, s90, s66
	s_cselect_b32 s92, s91, s5
	s_add_i32 s67, s66, 0x80
	s_mov_b32 m0, s79
	s_add_i32 s93, s4, 0xffff0000
	buffer_load_dwordx4 v196, s[8:11], s93 offen lds
	s_mov_b32 m0, s81
	s_nop 0
	buffer_load_dwordx4 v196, s[8:11], s4 offen lds
	s_waitcnt vmcnt(8)
	s_waitcnt lgkmcnt(8)
	s_barrier
	s_setprio 1
	s_waitcnt lgkmcnt(7)
	v_mfma_f32_16x16x32_bf16 v[124:127], v[128:131], v[160:163], v[124:127]
	s_waitcnt lgkmcnt(6)
	v_mfma_f32_16x16x32_bf16 v[124:127], v[132:135], v[164:167], v[124:127]
	v_mfma_f32_16x16x32_bf16 v[120:123], v[136:139], v[160:163], v[120:123]
	s_nop 0
	v_mfma_f32_16x16x32_bf16 v[120:123], v[140:143], v[164:167], v[120:123]
	s_waitcnt lgkmcnt(5)
	v_mfma_f32_16x16x32_bf16 v[116:119], v[128:131], v[168:171], v[116:119]
	s_waitcnt lgkmcnt(4)
	v_mfma_f32_16x16x32_bf16 v[116:119], v[132:135], v[172:175], v[116:119]
	v_mfma_f32_16x16x32_bf16 v[112:115], v[136:139], v[168:171], v[112:115]
	s_nop 0
	v_mfma_f32_16x16x32_bf16 v[112:115], v[140:143], v[172:175], v[112:115]
	s_waitcnt lgkmcnt(3)
	v_mfma_f32_16x16x32_bf16 v[108:111], v[128:131], v[176:179], v[108:111]
	s_waitcnt lgkmcnt(2)
	v_mfma_f32_16x16x32_bf16 v[108:111], v[132:135], v[180:183], v[108:111]
	v_mfma_f32_16x16x32_bf16 v[104:107], v[136:139], v[176:179], v[104:107]
	s_nop 0
	v_mfma_f32_16x16x32_bf16 v[104:107], v[140:143], v[180:183], v[104:107]
	s_waitcnt lgkmcnt(1)
	v_mfma_f32_16x16x32_bf16 v[100:103], v[128:131], v[184:187], v[100:103]
	s_waitcnt lgkmcnt(0)
	v_mfma_f32_16x16x32_bf16 v[100:103], v[132:135], v[188:191], v[100:103]
	v_mfma_f32_16x16x32_bf16 v[96:99], v[136:139], v[184:187], v[96:99]
	s_nop 0
	v_mfma_f32_16x16x32_bf16 v[96:99], v[140:143], v[188:191], v[96:99]
	v_mfma_f32_16x16x32_bf16 v[92:95], v[144:147], v[160:163], v[92:95]
	s_nop 0
	v_mfma_f32_16x16x32_bf16 v[92:95], v[148:151], v[164:167], v[92:95]
	v_mfma_f32_16x16x32_bf16 v[88:91], v[152:155], v[160:163], v[88:91]
	s_nop 0
	v_mfma_f32_16x16x32_bf16 v[88:91], v[156:159], v[164:167], v[88:91]
	v_mfma_f32_16x16x32_bf16 v[84:87], v[144:147], v[168:171], v[84:87]
	s_nop 0
	v_mfma_f32_16x16x32_bf16 v[84:87], v[148:151], v[172:175], v[84:87]
	v_mfma_f32_16x16x32_bf16 v[80:83], v[152:155], v[168:171], v[80:83]
	s_nop 0
	v_mfma_f32_16x16x32_bf16 v[80:83], v[156:159], v[172:175], v[80:83]
	v_mfma_f32_16x16x32_bf16 v[76:79], v[144:147], v[176:179], v[76:79]
	s_nop 0
	v_mfma_f32_16x16x32_bf16 v[76:79], v[148:151], v[180:183], v[76:79]
	v_mfma_f32_16x16x32_bf16 v[72:75], v[152:155], v[176:179], v[72:75]
	s_nop 0
	v_mfma_f32_16x16x32_bf16 v[72:75], v[156:159], v[180:183], v[72:75]
	v_mfma_f32_16x16x32_bf16 v[68:71], v[144:147], v[184:187], v[68:71]
	s_nop 0
	v_mfma_f32_16x16x32_bf16 v[68:71], v[148:151], v[188:191], v[68:71]
	v_mfma_f32_16x16x32_bf16 v[64:67], v[152:155], v[184:187], v[64:67]
	s_nop 0
	v_mfma_f32_16x16x32_bf16 v[64:67], v[156:159], v[188:191], v[64:67]
	s_setprio 0
	s_barrier
	ds_read_b128 v[160:163], v219 offset:16384
	ds_read_b128 v[164:167], v219 offset:17408
	ds_read_b128 v[168:171], v219 offset:18432
	ds_read_b128 v[172:175], v219 offset:19456
	ds_read_b128 v[176:179], v219 offset:20480
	ds_read_b128 v[180:183], v219 offset:21504
	ds_read_b128 v[184:187], v219 offset:22528
	ds_read_b128 v[188:191], v219 offset:23552
	s_mov_b32 m0, s62
	s_add_i32 s93, s92, 0x80000
	buffer_load_dwordx4 v202, s[12:15], s92 offen lds
	s_mov_b32 m0, s63
	s_nop 0
	buffer_load_dwordx4 v202, s[12:15], s93 offen lds
	s_add_i32 s93, s92, 0x8000
	s_mov_b32 m0, s64
	s_nop 0
	buffer_load_dwordx4 v202, s[12:15], s93 offen lds
	s_add_i32 s93, s92, 0x88000
	s_mov_b32 m0, s65
	s_nop 0
	buffer_load_dwordx4 v202, s[12:15], s93 offen lds
	s_mov_b32 m0, s45
	s_add_i32 s93, s66, 0x10000
	buffer_load_dwordx4 v196, s[8:11], s66 offen lds
	s_mov_b32 m0, s68
	s_nop 0
	buffer_load_dwordx4 v196, s[8:11], s93 offen lds
	s_waitcnt vmcnt(8)
	s_waitcnt lgkmcnt(6)
	s_barrier
	s_setprio 1
	s_waitcnt lgkmcnt(7)
	v_mfma_f32_16x16x32_bf16 v[60:63], v[128:131], v[160:163], v[60:63]
	s_waitcnt lgkmcnt(6)
	v_mfma_f32_16x16x32_bf16 v[60:63], v[132:135], v[164:167], v[60:63]
	v_mfma_f32_16x16x32_bf16 v[56:59], v[136:139], v[160:163], v[56:59]
	s_nop 0
	v_mfma_f32_16x16x32_bf16 v[56:59], v[140:143], v[164:167], v[56:59]
	s_waitcnt lgkmcnt(5)
	v_mfma_f32_16x16x32_bf16 v[52:55], v[128:131], v[168:171], v[52:55]
	s_waitcnt lgkmcnt(4)
	v_mfma_f32_16x16x32_bf16 v[52:55], v[132:135], v[172:175], v[52:55]
	v_mfma_f32_16x16x32_bf16 v[48:51], v[136:139], v[168:171], v[48:51]
	s_nop 0
	v_mfma_f32_16x16x32_bf16 v[48:51], v[140:143], v[172:175], v[48:51]
	s_waitcnt lgkmcnt(3)
	v_mfma_f32_16x16x32_bf16 v[44:47], v[128:131], v[176:179], v[44:47]
	s_waitcnt lgkmcnt(2)
	v_mfma_f32_16x16x32_bf16 v[44:47], v[132:135], v[180:183], v[44:47]
	v_mfma_f32_16x16x32_bf16 v[40:43], v[136:139], v[176:179], v[40:43]
	s_nop 0
	v_mfma_f32_16x16x32_bf16 v[40:43], v[140:143], v[180:183], v[40:43]
	s_waitcnt lgkmcnt(1)
	v_mfma_f32_16x16x32_bf16 v[36:39], v[128:131], v[184:187], v[36:39]
	s_waitcnt lgkmcnt(0)
	v_mfma_f32_16x16x32_bf16 v[36:39], v[132:135], v[188:191], v[36:39]
	v_mfma_f32_16x16x32_bf16 v[32:35], v[136:139], v[184:187], v[32:35]
	s_nop 0
	v_mfma_f32_16x16x32_bf16 v[32:35], v[140:143], v[188:191], v[32:35]
	v_mfma_f32_16x16x32_bf16 v[28:31], v[144:147], v[160:163], v[28:31]
	s_nop 0
	v_mfma_f32_16x16x32_bf16 v[28:31], v[148:151], v[164:167], v[28:31]
	v_mfma_f32_16x16x32_bf16 v[24:27], v[152:155], v[160:163], v[24:27]
	s_nop 0
	v_mfma_f32_16x16x32_bf16 v[24:27], v[156:159], v[164:167], v[24:27]
	v_mfma_f32_16x16x32_bf16 v[20:23], v[144:147], v[168:171], v[20:23]
	s_nop 0
	v_mfma_f32_16x16x32_bf16 v[20:23], v[148:151], v[172:175], v[20:23]
	v_mfma_f32_16x16x32_bf16 v[16:19], v[152:155], v[168:171], v[16:19]
	s_nop 0
	v_mfma_f32_16x16x32_bf16 v[16:19], v[156:159], v[172:175], v[16:19]
	v_mfma_f32_16x16x32_bf16 v[12:15], v[144:147], v[176:179], v[12:15]
	s_nop 0
	v_mfma_f32_16x16x32_bf16 v[12:15], v[148:151], v[180:183], v[12:15]
	v_mfma_f32_16x16x32_bf16 v[8:11], v[152:155], v[176:179], v[8:11]
	s_nop 0
	v_mfma_f32_16x16x32_bf16 v[8:11], v[156:159], v[180:183], v[8:11]
	v_mfma_f32_16x16x32_bf16 v[4:7], v[144:147], v[184:187], v[4:7]
	s_nop 0
	v_mfma_f32_16x16x32_bf16 v[4:7], v[148:151], v[188:191], v[4:7]
	v_mfma_f32_16x16x32_bf16 v[0:3], v[152:155], v[184:187], v[0:3]
	s_nop 0
	v_mfma_f32_16x16x32_bf16 v[0:3], v[156:159], v[188:191], v[0:3]
	s_setprio 0
	s_barrier
	ds_read_b128 v[140:143], v211
	ds_read_b128 v[144:147], v212
	ds_read_b128 v[148:151], v213
	ds_read_b128 v[152:155], v214
	ds_read_b128 v[156:159], v215
	ds_read_b128 v[136:139], v216
	ds_read_b128 v[132:135], v217
	ds_read_b128 v[128:131], v218
	ds_read_b128 v[160:163], v219 offset:32768
	ds_read_b128 v[164:167], v219 offset:33792
	ds_read_b128 v[168:171], v219 offset:34816
	ds_read_b128 v[172:175], v219 offset:35840
	ds_read_b128 v[176:179], v219 offset:36864
	ds_read_b128 v[180:183], v219 offset:37888
	ds_read_b128 v[184:187], v219 offset:38912
	ds_read_b128 v[188:191], v219 offset:39936
	s_mov_b32 m0, s69
	s_add_i32 s93, s66, 0x20000
	buffer_load_dwordx4 v196, s[8:11], s93 offen lds
	s_add_i32 s93, s66, 0x30000
	s_mov_b32 m0, s70
	s_nop 0
	buffer_load_dwordx4 v196, s[8:11], s93 offen lds
	s_waitcnt vmcnt(8)
	s_waitcnt lgkmcnt(8)
	s_barrier
	s_setprio 1
	s_waitcnt lgkmcnt(7)
	v_mfma_f32_16x16x32_bf16 v[124:127], v[140:143], v[160:163], v[124:127]
	s_waitcnt lgkmcnt(6)
	v_mfma_f32_16x16x32_bf16 v[124:127], v[144:147], v[164:167], v[124:127]
	v_mfma_f32_16x16x32_bf16 v[120:123], v[148:151], v[160:163], v[120:123]
	s_nop 0
	v_mfma_f32_16x16x32_bf16 v[120:123], v[152:155], v[164:167], v[120:123]
	s_waitcnt lgkmcnt(5)
	v_mfma_f32_16x16x32_bf16 v[116:119], v[140:143], v[168:171], v[116:119]
	s_waitcnt lgkmcnt(4)
	v_mfma_f32_16x16x32_bf16 v[116:119], v[144:147], v[172:175], v[116:119]
	v_mfma_f32_16x16x32_bf16 v[112:115], v[148:151], v[168:171], v[112:115]
	s_nop 0
	v_mfma_f32_16x16x32_bf16 v[112:115], v[152:155], v[172:175], v[112:115]
	s_waitcnt lgkmcnt(3)
	v_mfma_f32_16x16x32_bf16 v[108:111], v[140:143], v[176:179], v[108:111]
	s_waitcnt lgkmcnt(2)
	v_mfma_f32_16x16x32_bf16 v[108:111], v[144:147], v[180:183], v[108:111]
	v_mfma_f32_16x16x32_bf16 v[104:107], v[148:151], v[176:179], v[104:107]
	s_nop 0
	v_mfma_f32_16x16x32_bf16 v[104:107], v[152:155], v[180:183], v[104:107]
	s_waitcnt lgkmcnt(1)
	v_mfma_f32_16x16x32_bf16 v[100:103], v[140:143], v[184:187], v[100:103]
	s_waitcnt lgkmcnt(0)
	v_mfma_f32_16x16x32_bf16 v[100:103], v[144:147], v[188:191], v[100:103]
	v_mfma_f32_16x16x32_bf16 v[96:99], v[148:151], v[184:187], v[96:99]
	s_nop 0
	v_mfma_f32_16x16x32_bf16 v[96:99], v[152:155], v[188:191], v[96:99]
	v_mfma_f32_16x16x32_bf16 v[92:95], v[156:159], v[160:163], v[92:95]
	s_nop 0
	v_mfma_f32_16x16x32_bf16 v[92:95], v[136:139], v[164:167], v[92:95]
	v_mfma_f32_16x16x32_bf16 v[88:91], v[132:135], v[160:163], v[88:91]
	s_nop 0
	v_mfma_f32_16x16x32_bf16 v[88:91], v[128:131], v[164:167], v[88:91]
	v_mfma_f32_16x16x32_bf16 v[84:87], v[156:159], v[168:171], v[84:87]
	s_nop 0
	v_mfma_f32_16x16x32_bf16 v[84:87], v[136:139], v[172:175], v[84:87]
	v_mfma_f32_16x16x32_bf16 v[80:83], v[132:135], v[168:171], v[80:83]
	s_nop 0
	v_mfma_f32_16x16x32_bf16 v[80:83], v[128:131], v[172:175], v[80:83]
	v_mfma_f32_16x16x32_bf16 v[76:79], v[156:159], v[176:179], v[76:79]
	s_nop 0
	v_mfma_f32_16x16x32_bf16 v[76:79], v[136:139], v[180:183], v[76:79]
	v_mfma_f32_16x16x32_bf16 v[72:75], v[132:135], v[176:179], v[72:75]
	s_nop 0
	v_mfma_f32_16x16x32_bf16 v[72:75], v[128:131], v[180:183], v[72:75]
	v_mfma_f32_16x16x32_bf16 v[68:71], v[156:159], v[184:187], v[68:71]
	s_nop 0
	v_mfma_f32_16x16x32_bf16 v[68:71], v[136:139], v[188:191], v[68:71]
	v_mfma_f32_16x16x32_bf16 v[64:67], v[132:135], v[184:187], v[64:67]
	s_nop 0
	v_mfma_f32_16x16x32_bf16 v[64:67], v[128:131], v[188:191], v[64:67]
	s_setprio 0
	s_barrier
	ds_read_b128 v[160:163], v219 offset:49152
	ds_read_b128 v[164:167], v219 offset:50176
	ds_read_b128 v[168:171], v219 offset:51200
	ds_read_b128 v[172:175], v219 offset:52224
	ds_read_b128 v[176:179], v219 offset:53248
	ds_read_b128 v[180:183], v219 offset:54272
	ds_read_b128 v[184:187], v219 offset:55296
	ds_read_b128 v[188:191], v219 offset:56320
	s_mov_b32 m0, s73
	s_add_i32 s93, s92, 0x80
	buffer_load_dwordx4 v202, s[12:15], s93 offen lds
	s_add_i32 s93, s92, 0x80080
	s_mov_b32 m0, s74
	s_add_i32 s66, s66, 0x10080
	buffer_load_dwordx4 v202, s[12:15], s93 offen lds
	s_add_i32 s93, s92, 0x8080
	s_mov_b32 m0, s77
	s_add_i32 s92, s92, 0x88080
	buffer_load_dwordx4 v202, s[12:15], s93 offen lds
	s_mov_b32 m0, s78
	s_nop 0
	buffer_load_dwordx4 v202, s[12:15], s92 offen lds
	s_mov_b32 m0, s75
	s_nop 0
	buffer_load_dwordx4 v196, s[8:11], s67 offen lds
	s_mov_b32 m0, s76
	s_nop 0
	buffer_load_dwordx4 v196, s[8:11], s66 offen lds
	s_waitcnt vmcnt(8)
	s_waitcnt lgkmcnt(6)
	s_barrier
	s_setprio 1
	s_waitcnt lgkmcnt(7)
	v_mfma_f32_16x16x32_bf16 v[60:63], v[140:143], v[160:163], v[60:63]
	s_waitcnt lgkmcnt(6)
	v_mfma_f32_16x16x32_bf16 v[60:63], v[144:147], v[164:167], v[60:63]
	v_mfma_f32_16x16x32_bf16 v[56:59], v[148:151], v[160:163], v[56:59]
	s_nop 0
	v_mfma_f32_16x16x32_bf16 v[56:59], v[152:155], v[164:167], v[56:59]
	s_waitcnt lgkmcnt(5)
	v_mfma_f32_16x16x32_bf16 v[52:55], v[140:143], v[168:171], v[52:55]
	s_waitcnt lgkmcnt(4)
	v_mfma_f32_16x16x32_bf16 v[52:55], v[144:147], v[172:175], v[52:55]
	v_mfma_f32_16x16x32_bf16 v[48:51], v[148:151], v[168:171], v[48:51]
	s_nop 0
	v_mfma_f32_16x16x32_bf16 v[48:51], v[152:155], v[172:175], v[48:51]
	s_waitcnt lgkmcnt(3)
	v_mfma_f32_16x16x32_bf16 v[44:47], v[140:143], v[176:179], v[44:47]
	s_waitcnt lgkmcnt(2)
	v_mfma_f32_16x16x32_bf16 v[44:47], v[144:147], v[180:183], v[44:47]
	v_mfma_f32_16x16x32_bf16 v[40:43], v[148:151], v[176:179], v[40:43]
	s_nop 0
	v_mfma_f32_16x16x32_bf16 v[40:43], v[152:155], v[180:183], v[40:43]
	s_waitcnt lgkmcnt(1)
	v_mfma_f32_16x16x32_bf16 v[36:39], v[140:143], v[184:187], v[36:39]
	s_waitcnt lgkmcnt(0)
	v_mfma_f32_16x16x32_bf16 v[36:39], v[144:147], v[188:191], v[36:39]
	v_mfma_f32_16x16x32_bf16 v[32:35], v[148:151], v[184:187], v[32:35]
	s_nop 0
	v_mfma_f32_16x16x32_bf16 v[32:35], v[152:155], v[188:191], v[32:35]
	v_mfma_f32_16x16x32_bf16 v[28:31], v[156:159], v[160:163], v[28:31]
	s_nop 0
	v_mfma_f32_16x16x32_bf16 v[28:31], v[136:139], v[164:167], v[28:31]
	v_mfma_f32_16x16x32_bf16 v[24:27], v[132:135], v[160:163], v[24:27]
	s_nop 0
	v_mfma_f32_16x16x32_bf16 v[24:27], v[128:131], v[164:167], v[24:27]
	v_mfma_f32_16x16x32_bf16 v[20:23], v[156:159], v[168:171], v[20:23]
	s_nop 0
	v_mfma_f32_16x16x32_bf16 v[20:23], v[136:139], v[172:175], v[20:23]
	v_mfma_f32_16x16x32_bf16 v[16:19], v[132:135], v[168:171], v[16:19]
	s_nop 0
	v_mfma_f32_16x16x32_bf16 v[16:19], v[128:131], v[172:175], v[16:19]
	v_mfma_f32_16x16x32_bf16 v[12:15], v[156:159], v[176:179], v[12:15]
	s_nop 0
	v_mfma_f32_16x16x32_bf16 v[12:15], v[136:139], v[180:183], v[12:15]
	v_mfma_f32_16x16x32_bf16 v[8:11], v[132:135], v[176:179], v[8:11]
	s_nop 0
	v_mfma_f32_16x16x32_bf16 v[8:11], v[128:131], v[180:183], v[8:11]
	v_mfma_f32_16x16x32_bf16 v[4:7], v[156:159], v[184:187], v[4:7]
	s_nop 0
	v_mfma_f32_16x16x32_bf16 v[4:7], v[136:139], v[188:191], v[4:7]
	v_mfma_f32_16x16x32_bf16 v[0:3], v[132:135], v[184:187], v[0:3]
	s_nop 0
	v_mfma_f32_16x16x32_bf16 v[0:3], v[128:131], v[188:191], v[0:3]
	s_setprio 0
	s_barrier
	s_add_i32 s33, s33, 2
	s_addk_i32 s4, 0x100
	s_addk_i32 s5, 0x100
	s_cmp_gt_u32 s33, 5
	s_cbranch_scc0 .LBB0_220
	s_and_b64 vcc, exec, s[16:17]
	s_cbranch_vccz .LBB0_223
	s_barrier

.LBB0_250:
	s_waitcnt lgkmcnt(0)
	s_add_i32 s33, s91, 0x100
	s_add_i32 s66, s90, 0x100
	s_barrier
	s_setprio 1
	s_waitcnt lgkmcnt(7)
	v_mfma_f32_16x16x32_bf16 v[124:127], v[156:159], v[188:191], 0
	s_waitcnt lgkmcnt(6)
	v_mfma_f32_16x16x32_bf16 v[124:127], v[152:155], v[184:187], v[124:127]
	v_mfma_f32_16x16x32_bf16 v[120:123], v[148:151], v[188:191], 0
	s_nop 0
	v_mfma_f32_16x16x32_bf16 v[120:123], v[144:147], v[184:187], v[120:123]
	s_waitcnt lgkmcnt(5)
	v_mfma_f32_16x16x32_bf16 v[116:119], v[156:159], v[180:183], 0
	s_waitcnt lgkmcnt(4)
	v_mfma_f32_16x16x32_bf16 v[116:119], v[152:155], v[176:179], v[116:119]
	v_mfma_f32_16x16x32_bf16 v[112:115], v[148:151], v[180:183], 0
	s_nop 0
	v_mfma_f32_16x16x32_bf16 v[112:115], v[144:147], v[176:179], v[112:115]
	s_waitcnt lgkmcnt(3)
	v_mfma_f32_16x16x32_bf16 v[108:111], v[156:159], v[172:175], 0
	s_waitcnt lgkmcnt(2)
	v_mfma_f32_16x16x32_bf16 v[108:111], v[152:155], v[168:171], v[108:111]
	v_mfma_f32_16x16x32_bf16 v[104:107], v[148:151], v[172:175], 0
	s_nop 0
	v_mfma_f32_16x16x32_bf16 v[104:107], v[144:147], v[168:171], v[104:107]
	s_waitcnt lgkmcnt(1)
	v_mfma_f32_16x16x32_bf16 v[100:103], v[156:159], v[164:167], 0
	s_waitcnt lgkmcnt(0)
	v_mfma_f32_16x16x32_bf16 v[100:103], v[152:155], v[160:163], v[100:103]
	v_mfma_f32_16x16x32_bf16 v[96:99], v[148:151], v[164:167], 0
	s_nop 0
	v_mfma_f32_16x16x32_bf16 v[96:99], v[144:147], v[160:163], v[96:99]
	v_mfma_f32_16x16x32_bf16 v[92:95], v[140:143], v[188:191], 0
	s_nop 0
	v_mfma_f32_16x16x32_bf16 v[92:95], v[136:139], v[184:187], v[92:95]
	v_mfma_f32_16x16x32_bf16 v[88:91], v[132:135], v[188:191], 0
	s_nop 0
	v_mfma_f32_16x16x32_bf16 v[88:91], v[128:131], v[184:187], v[88:91]
	v_mfma_f32_16x16x32_bf16 v[84:87], v[140:143], v[180:183], 0
	s_nop 0
	v_mfma_f32_16x16x32_bf16 v[84:87], v[136:139], v[176:179], v[84:87]
	v_mfma_f32_16x16x32_bf16 v[80:83], v[132:135], v[180:183], 0
	s_nop 0
	v_mfma_f32_16x16x32_bf16 v[80:83], v[128:131], v[176:179], v[80:83]
	v_mfma_f32_16x16x32_bf16 v[76:79], v[140:143], v[172:175], 0
	s_nop 0
	v_mfma_f32_16x16x32_bf16 v[76:79], v[136:139], v[168:171], v[76:79]
	v_mfma_f32_16x16x32_bf16 v[72:75], v[132:135], v[172:175], 0
	s_nop 0
	v_mfma_f32_16x16x32_bf16 v[72:75], v[128:131], v[168:171], v[72:75]
	v_mfma_f32_16x16x32_bf16 v[68:71], v[140:143], v[164:167], 0
	s_nop 0
	v_mfma_f32_16x16x32_bf16 v[68:71], v[136:139], v[160:163], v[68:71]
	v_mfma_f32_16x16x32_bf16 v[64:67], v[132:135], v[164:167], 0
	s_nop 0
	v_mfma_f32_16x16x32_bf16 v[64:67], v[128:131], v[160:163], v[64:67]
	s_setprio 0
	s_barrier
	s_mov_b32 m0, s62
	s_mov_b32 s10, s6
	s_mov_b32 s11, s7
	buffer_load_dwordx4 v192, s[8:11], s66 offen lds
	s_add_i32 s66, s90, 0x20100
	s_mov_b32 m0, s63
	s_and_b64 vcc, exec, s[42:43]
	buffer_load_dwordx4 v192, s[8:11], s66 offen lds
	s_add_i32 s66, s90, 0x2100
	s_mov_b32 m0, s64
	s_nop 0
	buffer_load_dwordx4 v192, s[8:11], s66 offen lds
	s_add_i32 s66, s90, 0x22100
	s_mov_b32 m0, s65
	s_nop 0
	buffer_load_dwordx4 v192, s[8:11], s66 offen lds
	s_mov_b32 m0, s47
	s_add_i32 s10, s91, 0x10100
	buffer_load_dwordx4 v196, s[4:7], s33 offen lds
	s_mov_b32 m0, s68
	s_nop 0
	buffer_load_dwordx4 v196, s[4:7], s10 offen lds
	ds_read_b128 v[188:191], v197 offset:16384
	ds_read_b128 v[184:187], v197 offset:17408
	ds_read_b128 v[180:183], v197 offset:18432
	ds_read_b128 v[176:179], v197 offset:19456
	ds_read_b128 v[172:175], v197 offset:20480
	ds_read_b128 v[168:171], v197 offset:21504
	ds_read_b128 v[164:167], v197 offset:22528
	ds_read_b128 v[160:163], v197 offset:23552
	s_cbranch_vccz .LBB0_261
	s_waitcnt vmcnt(24)
	s_cbranch_execnz .LBB0_253

.LBB0_253:
	s_waitcnt lgkmcnt(0)
	s_add_i32 s33, s91, 0x180
	s_add_i32 s42, s90, 0x180
	s_barrier
	s_setprio 1
	s_waitcnt lgkmcnt(7)
	v_mfma_f32_16x16x32_bf16 v[60:63], v[156:159], v[188:191], 0
	s_waitcnt lgkmcnt(6)
	v_mfma_f32_16x16x32_bf16 v[60:63], v[152:155], v[184:187], v[60:63]
	v_mfma_f32_16x16x32_bf16 v[56:59], v[148:151], v[188:191], 0
	s_nop 0
	v_mfma_f32_16x16x32_bf16 v[56:59], v[144:147], v[184:187], v[56:59]
	s_waitcnt lgkmcnt(5)
	v_mfma_f32_16x16x32_bf16 v[52:55], v[156:159], v[180:183], 0
	s_waitcnt lgkmcnt(4)
	v_mfma_f32_16x16x32_bf16 v[52:55], v[152:155], v[176:179], v[52:55]
	v_mfma_f32_16x16x32_bf16 v[48:51], v[148:151], v[180:183], 0
	s_nop 0
	v_mfma_f32_16x16x32_bf16 v[48:51], v[144:147], v[176:179], v[48:51]
	s_waitcnt lgkmcnt(3)
	v_mfma_f32_16x16x32_bf16 v[44:47], v[156:159], v[172:175], 0
	s_waitcnt lgkmcnt(2)
	v_mfma_f32_16x16x32_bf16 v[44:47], v[152:155], v[168:171], v[44:47]
	v_mfma_f32_16x16x32_bf16 v[40:43], v[148:151], v[172:175], 0
	s_nop 0
	v_mfma_f32_16x16x32_bf16 v[40:43], v[144:147], v[168:171], v[40:43]
	s_waitcnt lgkmcnt(1)
	v_mfma_f32_16x16x32_bf16 v[36:39], v[156:159], v[164:167], 0
	s_waitcnt lgkmcnt(0)
	v_mfma_f32_16x16x32_bf16 v[36:39], v[152:155], v[160:163], v[36:39]
	v_mfma_f32_16x16x32_bf16 v[32:35], v[148:151], v[164:167], 0
	s_nop 0
	v_mfma_f32_16x16x32_bf16 v[32:35], v[144:147], v[160:163], v[32:35]
	v_mfma_f32_16x16x32_bf16 v[28:31], v[140:143], v[188:191], 0
	s_nop 0
	v_mfma_f32_16x16x32_bf16 v[28:31], v[136:139], v[184:187], v[28:31]
	v_mfma_f32_16x16x32_bf16 v[24:27], v[132:135], v[188:191], 0
	s_nop 0
	v_mfma_f32_16x16x32_bf16 v[24:27], v[128:131], v[184:187], v[24:27]
	v_mfma_f32_16x16x32_bf16 v[20:23], v[140:143], v[180:183], 0
	s_nop 0
	v_mfma_f32_16x16x32_bf16 v[20:23], v[136:139], v[176:179], v[20:23]
	v_mfma_f32_16x16x32_bf16 v[16:19], v[132:135], v[180:183], 0
	s_nop 0
	v_mfma_f32_16x16x32_bf16 v[16:19], v[128:131], v[176:179], v[16:19]
	v_mfma_f32_16x16x32_bf16 v[12:15], v[140:143], v[172:175], 0
	s_nop 0
	v_mfma_f32_16x16x32_bf16 v[12:15], v[136:139], v[168:171], v[12:15]
	v_mfma_f32_16x16x32_bf16 v[8:11], v[132:135], v[172:175], 0
	s_nop 0
	v_mfma_f32_16x16x32_bf16 v[8:11], v[128:131], v[168:171], v[8:11]
	v_mfma_f32_16x16x32_bf16 v[4:7], v[140:143], v[164:167], 0
	s_nop 0
	v_mfma_f32_16x16x32_bf16 v[4:7], v[136:139], v[160:163], v[4:7]
	v_mfma_f32_16x16x32_bf16 v[0:3], v[132:135], v[164:167], 0
	s_nop 0
	v_mfma_f32_16x16x32_bf16 v[0:3], v[128:131], v[160:163], v[0:3]
	s_setprio 0
	s_barrier
	ds_read_b128 v[156:159], v203
	ds_read_b128 v[152:155], v204
	ds_read_b128 v[148:151], v205
	ds_read_b128 v[144:147], v206
	ds_read_b128 v[140:143], v207
	ds_read_b128 v[136:139], v208
	ds_read_b128 v[132:135], v209
	ds_read_b128 v[128:131], v210
	ds_read_b128 v[160:163], v197 offset:32768
	ds_read_b128 v[164:167], v197 offset:33792
	ds_read_b128 v[168:171], v197 offset:34816
	ds_read_b128 v[172:175], v197 offset:35840
	ds_read_b128 v[176:179], v197 offset:36864
	ds_read_b128 v[180:183], v197 offset:37888
	ds_read_b128 v[184:187], v197 offset:38912
	ds_read_b128 v[188:191], v197 offset:39936
	s_mov_b32 m0, s69
	s_add_i32 s10, s91, 0x20100
	buffer_load_dwordx4 v196, s[4:7], s10 offen lds
	s_add_i32 s10, s91, 0x30100
	s_mov_b32 m0, s70
	s_nop 0
	buffer_load_dwordx4 v196, s[4:7], s10 offen lds
	s_waitcnt vmcnt(8)
	s_waitcnt lgkmcnt(8)
	s_barrier
	s_setprio 1
	s_waitcnt lgkmcnt(7)
	v_mfma_f32_16x16x32_bf16 v[124:127], v[156:159], v[160:163], v[124:127]
	s_waitcnt lgkmcnt(6)
	v_mfma_f32_16x16x32_bf16 v[124:127], v[152:155], v[164:167], v[124:127]
	v_mfma_f32_16x16x32_bf16 v[120:123], v[148:151], v[160:163], v[120:123]
	s_nop 0
	v_mfma_f32_16x16x32_bf16 v[120:123], v[144:147], v[164:167], v[120:123]
	s_waitcnt lgkmcnt(5)
	v_mfma_f32_16x16x32_bf16 v[116:119], v[156:159], v[168:171], v[116:119]
	s_waitcnt lgkmcnt(4)
	v_mfma_f32_16x16x32_bf16 v[116:119], v[152:155], v[172:175], v[116:119]
	v_mfma_f32_16x16x32_bf16 v[112:115], v[148:151], v[168:171], v[112:115]
	s_nop 0
	v_mfma_f32_16x16x32_bf16 v[112:115], v[144:147], v[172:175], v[112:115]
	s_waitcnt lgkmcnt(3)
	v_mfma_f32_16x16x32_bf16 v[108:111], v[156:159], v[176:179], v[108:111]
	s_waitcnt lgkmcnt(2)
	v_mfma_f32_16x16x32_bf16 v[108:111], v[152:155], v[180:183], v[108:111]
	v_mfma_f32_16x16x32_bf16 v[104:107], v[148:151], v[176:179], v[104:107]
	s_nop 0
	v_mfma_f32_16x16x32_bf16 v[104:107], v[144:147], v[180:183], v[104:107]
	s_waitcnt lgkmcnt(1)
	v_mfma_f32_16x16x32_bf16 v[100:103], v[156:159], v[184:187], v[100:103]
	s_waitcnt lgkmcnt(0)
	v_mfma_f32_16x16x32_bf16 v[100:103], v[152:155], v[188:191], v[100:103]
	v_mfma_f32_16x16x32_bf16 v[96:99], v[148:151], v[184:187], v[96:99]
	s_nop 0
	v_mfma_f32_16x16x32_bf16 v[96:99], v[144:147], v[188:191], v[96:99]
	v_mfma_f32_16x16x32_bf16 v[92:95], v[140:143], v[160:163], v[92:95]
	s_nop 0
	v_mfma_f32_16x16x32_bf16 v[92:95], v[136:139], v[164:167], v[92:95]
	v_mfma_f32_16x16x32_bf16 v[88:91], v[132:135], v[160:163], v[88:91]
	s_nop 0
	v_mfma_f32_16x16x32_bf16 v[88:91], v[128:131], v[164:167], v[88:91]
	v_mfma_f32_16x16x32_bf16 v[84:87], v[140:143], v[168:171], v[84:87]
	s_nop 0
	v_mfma_f32_16x16x32_bf16 v[84:87], v[136:139], v[172:175], v[84:87]
	v_mfma_f32_16x16x32_bf16 v[80:83], v[132:135], v[168:171], v[80:83]
	s_nop 0
	v_mfma_f32_16x16x32_bf16 v[80:83], v[128:131], v[172:175], v[80:83]
	v_mfma_f32_16x16x32_bf16 v[76:79], v[140:143], v[176:179], v[76:79]
	s_nop 0
	v_mfma_f32_16x16x32_bf16 v[76:79], v[136:139], v[180:183], v[76:79]
	v_mfma_f32_16x16x32_bf16 v[72:75], v[132:135], v[176:179], v[72:75]
	s_nop 0
	v_mfma_f32_16x16x32_bf16 v[72:75], v[128:131], v[180:183], v[72:75]
	v_mfma_f32_16x16x32_bf16 v[68:71], v[140:143], v[184:187], v[68:71]
	s_nop 0
	v_mfma_f32_16x16x32_bf16 v[68:71], v[136:139], v[188:191], v[68:71]
	v_mfma_f32_16x16x32_bf16 v[64:67], v[132:135], v[184:187], v[64:67]
	s_nop 0
	v_mfma_f32_16x16x32_bf16 v[64:67], v[128:131], v[188:191], v[64:67]
	s_setprio 0
	s_barrier
	ds_read_b128 v[160:163], v197 offset:49152
	ds_read_b128 v[164:167], v197 offset:50176
	ds_read_b128 v[168:171], v197 offset:51200
	ds_read_b128 v[172:175], v197 offset:52224
	ds_read_b128 v[176:179], v197 offset:53248
	ds_read_b128 v[180:183], v197 offset:54272
	ds_read_b128 v[184:187], v197 offset:55296
	ds_read_b128 v[188:191], v197 offset:56320
	s_mov_b32 m0, s72
	s_mov_b32 s10, s6
	s_mov_b32 s11, s7
	buffer_load_dwordx4 v192, s[8:11], s42 offen lds
	s_add_i32 s42, s90, 0x20180
	s_mov_b32 m0, s73
	s_nop 0
	buffer_load_dwordx4 v192, s[8:11], s42 offen lds
	s_add_i32 s42, s90, 0x2180
	s_mov_b32 m0, s76
	s_nop 0
	buffer_load_dwordx4 v192, s[8:11], s42 offen lds
	s_add_i32 s42, s90, 0x22180
	s_mov_b32 m0, s77
	s_nop 0
	buffer_load_dwordx4 v192, s[8:11], s42 offen lds
	s_mov_b32 m0, s74
	s_nop 0
	buffer_load_dwordx4 v196, s[4:7], s33 offen lds
	s_add_i32 s33, s91, 0x10180
	s_mov_b32 m0, s75
	s_nop 0
	buffer_load_dwordx4 v196, s[4:7], s33 offen lds
	s_waitcnt vmcnt(8)
	s_waitcnt lgkmcnt(6)
	s_barrier
	s_setprio 1
	s_waitcnt lgkmcnt(7)
	v_mfma_f32_16x16x32_bf16 v[60:63], v[156:159], v[160:163], v[60:63]
	s_waitcnt lgkmcnt(6)
	v_mfma_f32_16x16x32_bf16 v[60:63], v[152:155], v[164:167], v[60:63]
	v_mfma_f32_16x16x32_bf16 v[56:59], v[148:151], v[160:163], v[56:59]
	s_nop 0
	v_mfma_f32_16x16x32_bf16 v[56:59], v[144:147], v[164:167], v[56:59]
	s_waitcnt lgkmcnt(5)
	v_mfma_f32_16x16x32_bf16 v[52:55], v[156:159], v[168:171], v[52:55]
	s_waitcnt lgkmcnt(4)
	v_mfma_f32_16x16x32_bf16 v[52:55], v[152:155], v[172:175], v[52:55]
	v_mfma_f32_16x16x32_bf16 v[48:51], v[148:151], v[168:171], v[48:51]
	s_nop 0
	v_mfma_f32_16x16x32_bf16 v[48:51], v[144:147], v[172:175], v[48:51]
	s_waitcnt lgkmcnt(3)
	v_mfma_f32_16x16x32_bf16 v[44:47], v[156:159], v[176:179], v[44:47]
	s_waitcnt lgkmcnt(2)
	v_mfma_f32_16x16x32_bf16 v[44:47], v[152:155], v[180:183], v[44:47]
	v_mfma_f32_16x16x32_bf16 v[40:43], v[148:151], v[176:179], v[40:43]
	s_nop 0
	v_mfma_f32_16x16x32_bf16 v[40:43], v[144:147], v[180:183], v[40:43]
	s_waitcnt lgkmcnt(1)
	v_mfma_f32_16x16x32_bf16 v[36:39], v[156:159], v[184:187], v[36:39]
	s_waitcnt lgkmcnt(0)
	v_mfma_f32_16x16x32_bf16 v[36:39], v[152:155], v[188:191], v[36:39]
	v_mfma_f32_16x16x32_bf16 v[32:35], v[148:151], v[184:187], v[32:35]
	s_nop 0
	v_mfma_f32_16x16x32_bf16 v[32:35], v[144:147], v[188:191], v[32:35]
	v_mfma_f32_16x16x32_bf16 v[28:31], v[140:143], v[160:163], v[28:31]
	s_nop 0
	v_mfma_f32_16x16x32_bf16 v[28:31], v[136:139], v[164:167], v[28:31]
	v_mfma_f32_16x16x32_bf16 v[24:27], v[132:135], v[160:163], v[24:27]
	s_nop 0
	v_mfma_f32_16x16x32_bf16 v[24:27], v[128:131], v[164:167], v[24:27]
	v_mfma_f32_16x16x32_bf16 v[20:23], v[140:143], v[168:171], v[20:23]
	s_nop 0
	v_mfma_f32_16x16x32_bf16 v[20:23], v[136:139], v[172:175], v[20:23]
	v_mfma_f32_16x16x32_bf16 v[16:19], v[132:135], v[168:171], v[16:19]
	s_nop 0
	v_mfma_f32_16x16x32_bf16 v[16:19], v[128:131], v[172:175], v[16:19]
	v_mfma_f32_16x16x32_bf16 v[12:15], v[140:143], v[176:179], v[12:15]
	s_nop 0
	v_mfma_f32_16x16x32_bf16 v[12:15], v[136:139], v[180:183], v[12:15]
	v_mfma_f32_16x16x32_bf16 v[8:11], v[132:135], v[176:179], v[8:11]
	s_nop 0
	v_mfma_f32_16x16x32_bf16 v[8:11], v[128:131], v[180:183], v[8:11]
	v_mfma_f32_16x16x32_bf16 v[4:7], v[140:143], v[184:187], v[4:7]
	s_nop 0
	v_mfma_f32_16x16x32_bf16 v[4:7], v[136:139], v[188:191], v[4:7]
	v_mfma_f32_16x16x32_bf16 v[0:3], v[132:135], v[184:187], v[0:3]
	s_nop 0
	v_mfma_f32_16x16x32_bf16 v[0:3], v[128:131], v[188:191], v[0:3]
	s_setprio 0
	s_barrier
	s_add_i32 s33, s91, 0x30180
	s_add_i32 s42, s90, 0x200
	s_mov_b32 s43, 0
.LBB0_254:
	ds_read_b128 v[128:131], v193
	ds_read_b128 v[132:135], v194
	ds_read_b128 v[136:139], v195
	ds_read_b128 v[140:143], v198
	ds_read_b128 v[144:147], v199
	ds_read_b128 v[148:151], v200
	ds_read_b128 v[152:155], v201
	ds_read_b128 v[156:159], v202
	ds_read_b128 v[160:163], v197
	ds_read_b128 v[164:167], v197 offset:1024
	ds_read_b128 v[168:171], v197 offset:2048
	ds_read_b128 v[172:175], v197 offset:3072
	ds_read_b128 v[176:179], v197 offset:4096
	ds_read_b128 v[180:183], v197 offset:5120
	ds_read_b128 v[184:187], v197 offset:6144
	ds_read_b128 v[188:191], v197 offset:7168
	s_add_i32 s66, s33, 0xfffd0080
	s_cmp_eq_u32 s43, 4
	s_cselect_b32 s66, s88, s66
	s_cselect_b32 s90, s89, s42
	s_add_i32 s67, s66, 0x80
	s_mov_b32 m0, s78
	s_add_i32 s91, s33, 0xffff0000
	buffer_load_dwordx4 v196, s[4:7], s91 offen lds
	s_mov_b32 m0, s79
	s_nop 0
	buffer_load_dwordx4 v196, s[4:7], s33 offen lds
	s_waitcnt vmcnt(8)
	s_waitcnt lgkmcnt(8)
	s_barrier
	s_setprio 1
	s_waitcnt lgkmcnt(7)
	v_mfma_f32_16x16x32_bf16 v[124:127], v[128:131], v[160:163], v[124:127]
	s_waitcnt lgkmcnt(6)
	v_mfma_f32_16x16x32_bf16 v[124:127], v[132:135], v[164:167], v[124:127]
	v_mfma_f32_16x16x32_bf16 v[120:123], v[136:139], v[160:163], v[120:123]
	s_nop 0
	v_mfma_f32_16x16x32_bf16 v[120:123], v[140:143], v[164:167], v[120:123]
	s_waitcnt lgkmcnt(5)
	v_mfma_f32_16x16x32_bf16 v[116:119], v[128:131], v[168:171], v[116:119]
	s_waitcnt lgkmcnt(4)
	v_mfma_f32_16x16x32_bf16 v[116:119], v[132:135], v[172:175], v[116:119]
	v_mfma_f32_16x16x32_bf16 v[112:115], v[136:139], v[168:171], v[112:115]
	s_nop 0
	v_mfma_f32_16x16x32_bf16 v[112:115], v[140:143], v[172:175], v[112:115]
	s_waitcnt lgkmcnt(3)
	v_mfma_f32_16x16x32_bf16 v[108:111], v[128:131], v[176:179], v[108:111]
	s_waitcnt lgkmcnt(2)
	v_mfma_f32_16x16x32_bf16 v[108:111], v[132:135], v[180:183], v[108:111]
	v_mfma_f32_16x16x32_bf16 v[104:107], v[136:139], v[176:179], v[104:107]
	s_nop 0
	v_mfma_f32_16x16x32_bf16 v[104:107], v[140:143], v[180:183], v[104:107]
	s_waitcnt lgkmcnt(1)
	v_mfma_f32_16x16x32_bf16 v[100:103], v[128:131], v[184:187], v[100:103]
	s_waitcnt lgkmcnt(0)
	v_mfma_f32_16x16x32_bf16 v[100:103], v[132:135], v[188:191], v[100:103]
	v_mfma_f32_16x16x32_bf16 v[96:99], v[136:139], v[184:187], v[96:99]
	s_nop 0
	v_mfma_f32_16x16x32_bf16 v[96:99], v[140:143], v[188:191], v[96:99]
	v_mfma_f32_16x16x32_bf16 v[92:95], v[144:147], v[160:163], v[92:95]
	s_nop 0
	v_mfma_f32_16x16x32_bf16 v[92:95], v[148:151], v[164:167], v[92:95]
	v_mfma_f32_16x16x32_bf16 v[88:91], v[152:155], v[160:163], v[88:91]
	s_nop 0
	v_mfma_f32_16x16x32_bf16 v[88:91], v[156:159], v[164:167], v[88:91]
	v_mfma_f32_16x16x32_bf16 v[84:87], v[144:147], v[168:171], v[84:87]
	s_nop 0
	v_mfma_f32_16x16x32_bf16 v[84:87], v[148:151], v[172:175], v[84:87]
	v_mfma_f32_16x16x32_bf16 v[80:83], v[152:155], v[168:171], v[80:83]
	s_nop 0
	v_mfma_f32_16x16x32_bf16 v[80:83], v[156:159], v[172:175], v[80:83]
	v_mfma_f32_16x16x32_bf16 v[76:79], v[144:147], v[176:179], v[76:79]
	s_nop 0
	v_mfma_f32_16x16x32_bf16 v[76:79], v[148:151], v[180:183], v[76:79]
	v_mfma_f32_16x16x32_bf16 v[72:75], v[152:155], v[176:179], v[72:75]
	s_nop 0
	v_mfma_f32_16x16x32_bf16 v[72:75], v[156:159], v[180:183], v[72:75]
	v_mfma_f32_16x16x32_bf16 v[68:71], v[144:147], v[184:187], v[68:71]
	s_nop 0
	v_mfma_f32_16x16x32_bf16 v[68:71], v[148:151], v[188:191], v[68:71]
	v_mfma_f32_16x16x32_bf16 v[64:67], v[152:155], v[184:187], v[64:67]
	s_nop 0
	v_mfma_f32_16x16x32_bf16 v[64:67], v[156:159], v[188:191], v[64:67]
	s_setprio 0
	s_barrier
	ds_read_b128 v[160:163], v197 offset:16384
	ds_read_b128 v[164:167], v197 offset:17408
	ds_read_b128 v[168:171], v197 offset:18432
	ds_read_b128 v[172:175], v197 offset:19456
	ds_read_b128 v[176:179], v197 offset:20480
	ds_read_b128 v[180:183], v197 offset:21504
	ds_read_b128 v[184:187], v197 offset:22528
	ds_read_b128 v[188:191], v197 offset:23552
	s_mov_b32 m0, s62
	s_add_i32 s91, s90, 0x20000
	buffer_load_dwordx4 v192, s[8:11], s90 offen lds
	s_mov_b32 m0, s63
	s_nop 0
	buffer_load_dwordx4 v192, s[8:11], s91 offen lds
	s_add_i32 s91, s90, 0x2000
	s_mov_b32 m0, s64
	s_nop 0
	buffer_load_dwordx4 v192, s[8:11], s91 offen lds
	s_add_i32 s91, s90, 0x22000
	s_mov_b32 m0, s65
	s_nop 0
	buffer_load_dwordx4 v192, s[8:11], s91 offen lds
	s_mov_b32 m0, s47
	s_add_i32 s91, s66, 0x10000
	buffer_load_dwordx4 v196, s[4:7], s66 offen lds
	s_mov_b32 m0, s68
	s_nop 0
	buffer_load_dwordx4 v196, s[4:7], s91 offen lds
	s_waitcnt vmcnt(8)
	s_waitcnt lgkmcnt(6)
	s_barrier
	s_setprio 1
	s_waitcnt lgkmcnt(7)
	v_mfma_f32_16x16x32_bf16 v[60:63], v[128:131], v[160:163], v[60:63]
	s_waitcnt lgkmcnt(6)
	v_mfma_f32_16x16x32_bf16 v[60:63], v[132:135], v[164:167], v[60:63]
	v_mfma_f32_16x16x32_bf16 v[56:59], v[136:139], v[160:163], v[56:59]
	s_nop 0
	v_mfma_f32_16x16x32_bf16 v[56:59], v[140:143], v[164:167], v[56:59]
	s_waitcnt lgkmcnt(5)
	v_mfma_f32_16x16x32_bf16 v[52:55], v[128:131], v[168:171], v[52:55]
	s_waitcnt lgkmcnt(4)
	v_mfma_f32_16x16x32_bf16 v[52:55], v[132:135], v[172:175], v[52:55]
	v_mfma_f32_16x16x32_bf16 v[48:51], v[136:139], v[168:171], v[48:51]
	s_nop 0
	v_mfma_f32_16x16x32_bf16 v[48:51], v[140:143], v[172:175], v[48:51]
	s_waitcnt lgkmcnt(3)
	v_mfma_f32_16x16x32_bf16 v[44:47], v[128:131], v[176:179], v[44:47]
	s_waitcnt lgkmcnt(2)
	v_mfma_f32_16x16x32_bf16 v[44:47], v[132:135], v[180:183], v[44:47]
	v_mfma_f32_16x16x32_bf16 v[40:43], v[136:139], v[176:179], v[40:43]
	s_nop 0
	v_mfma_f32_16x16x32_bf16 v[40:43], v[140:143], v[180:183], v[40:43]
	s_waitcnt lgkmcnt(1)
	v_mfma_f32_16x16x32_bf16 v[36:39], v[128:131], v[184:187], v[36:39]
	s_waitcnt lgkmcnt(0)
	v_mfma_f32_16x16x32_bf16 v[36:39], v[132:135], v[188:191], v[36:39]
	v_mfma_f32_16x16x32_bf16 v[32:35], v[136:139], v[184:187], v[32:35]
	s_nop 0
	v_mfma_f32_16x16x32_bf16 v[32:35], v[140:143], v[188:191], v[32:35]
	v_mfma_f32_16x16x32_bf16 v[28:31], v[144:147], v[160:163], v[28:31]
	s_nop 0
	v_mfma_f32_16x16x32_bf16 v[28:31], v[148:151], v[164:167], v[28:31]
	v_mfma_f32_16x16x32_bf16 v[24:27], v[152:155], v[160:163], v[24:27]
	s_nop 0
	v_mfma_f32_16x16x32_bf16 v[24:27], v[156:159], v[164:167], v[24:27]
	v_mfma_f32_16x16x32_bf16 v[20:23], v[144:147], v[168:171], v[20:23]
	s_nop 0
	v_mfma_f32_16x16x32_bf16 v[20:23], v[148:151], v[172:175], v[20:23]
	v_mfma_f32_16x16x32_bf16 v[16:19], v[152:155], v[168:171], v[16:19]
	s_nop 0
	v_mfma_f32_16x16x32_bf16 v[16:19], v[156:159], v[172:175], v[16:19]
	v_mfma_f32_16x16x32_bf16 v[12:15], v[144:147], v[176:179], v[12:15]
	s_nop 0
	v_mfma_f32_16x16x32_bf16 v[12:15], v[148:151], v[180:183], v[12:15]
	v_mfma_f32_16x16x32_bf16 v[8:11], v[152:155], v[176:179], v[8:11]
	s_nop 0
	v_mfma_f32_16x16x32_bf16 v[8:11], v[156:159], v[180:183], v[8:11]
	v_mfma_f32_16x16x32_bf16 v[4:7], v[144:147], v[184:187], v[4:7]
	s_nop 0
	v_mfma_f32_16x16x32_bf16 v[4:7], v[148:151], v[188:191], v[4:7]
	v_mfma_f32_16x16x32_bf16 v[0:3], v[152:155], v[184:187], v[0:3]
	s_nop 0
	v_mfma_f32_16x16x32_bf16 v[0:3], v[156:159], v[188:191], v[0:3]
	s_setprio 0
	s_barrier
	ds_read_b128 v[140:143], v203
	ds_read_b128 v[144:147], v204
	ds_read_b128 v[148:151], v205
	ds_read_b128 v[152:155], v206
	ds_read_b128 v[156:159], v207
	ds_read_b128 v[136:139], v208
	ds_read_b128 v[132:135], v209
	ds_read_b128 v[128:131], v210
	ds_read_b128 v[160:163], v197 offset:32768
	ds_read_b128 v[164:167], v197 offset:33792
	ds_read_b128 v[168:171], v197 offset:34816
	ds_read_b128 v[172:175], v197 offset:35840
	ds_read_b128 v[176:179], v197 offset:36864
	ds_read_b128 v[180:183], v197 offset:37888
	ds_read_b128 v[184:187], v197 offset:38912
	ds_read_b128 v[188:191], v197 offset:39936
	s_mov_b32 m0, s69
	s_add_i32 s91, s66, 0x20000
	buffer_load_dwordx4 v196, s[4:7], s91 offen lds
	s_add_i32 s91, s66, 0x30000
	s_mov_b32 m0, s70
	s_nop 0
	buffer_load_dwordx4 v196, s[4:7], s91 offen lds
	s_waitcnt vmcnt(8)
	s_waitcnt lgkmcnt(8)
	s_barrier
	s_setprio 1
	s_waitcnt lgkmcnt(7)
	v_mfma_f32_16x16x32_bf16 v[124:127], v[140:143], v[160:163], v[124:127]
	s_waitcnt lgkmcnt(6)
	v_mfma_f32_16x16x32_bf16 v[124:127], v[144:147], v[164:167], v[124:127]
	v_mfma_f32_16x16x32_bf16 v[120:123], v[148:151], v[160:163], v[120:123]
	s_nop 0
	v_mfma_f32_16x16x32_bf16 v[120:123], v[152:155], v[164:167], v[120:123]
	s_waitcnt lgkmcnt(5)
	v_mfma_f32_16x16x32_bf16 v[116:119], v[140:143], v[168:171], v[116:119]
	s_waitcnt lgkmcnt(4)
	v_mfma_f32_16x16x32_bf16 v[116:119], v[144:147], v[172:175], v[116:119]
	v_mfma_f32_16x16x32_bf16 v[112:115], v[148:151], v[168:171], v[112:115]
	s_nop 0
	v_mfma_f32_16x16x32_bf16 v[112:115], v[152:155], v[172:175], v[112:115]
	s_waitcnt lgkmcnt(3)
	v_mfma_f32_16x16x32_bf16 v[108:111], v[140:143], v[176:179], v[108:111]
	s_waitcnt lgkmcnt(2)
	v_mfma_f32_16x16x32_bf16 v[108:111], v[144:147], v[180:183], v[108:111]
	v_mfma_f32_16x16x32_bf16 v[104:107], v[148:151], v[176:179], v[104:107]
	s_nop 0
	v_mfma_f32_16x16x32_bf16 v[104:107], v[152:155], v[180:183], v[104:107]
	s_waitcnt lgkmcnt(1)
	v_mfma_f32_16x16x32_bf16 v[100:103], v[140:143], v[184:187], v[100:103]
	s_waitcnt lgkmcnt(0)
	v_mfma_f32_16x16x32_bf16 v[100:103], v[144:147], v[188:191], v[100:103]
	v_mfma_f32_16x16x32_bf16 v[96:99], v[148:151], v[184:187], v[96:99]
	s_nop 0
	v_mfma_f32_16x16x32_bf16 v[96:99], v[152:155], v[188:191], v[96:99]
	v_mfma_f32_16x16x32_bf16 v[92:95], v[156:159], v[160:163], v[92:95]
	s_nop 0
	v_mfma_f32_16x16x32_bf16 v[92:95], v[136:139], v[164:167], v[92:95]
	v_mfma_f32_16x16x32_bf16 v[88:91], v[132:135], v[160:163], v[88:91]
	s_nop 0
	v_mfma_f32_16x16x32_bf16 v[88:91], v[128:131], v[164:167], v[88:91]
	v_mfma_f32_16x16x32_bf16 v[84:87], v[156:159], v[168:171], v[84:87]
	s_nop 0
	v_mfma_f32_16x16x32_bf16 v[84:87], v[136:139], v[172:175], v[84:87]
	v_mfma_f32_16x16x32_bf16 v[80:83], v[132:135], v[168:171], v[80:83]
	s_nop 0
	v_mfma_f32_16x16x32_bf16 v[80:83], v[128:131], v[172:175], v[80:83]
	v_mfma_f32_16x16x32_bf16 v[76:79], v[156:159], v[176:179], v[76:79]
	s_nop 0
	v_mfma_f32_16x16x32_bf16 v[76:79], v[136:139], v[180:183], v[76:79]
	v_mfma_f32_16x16x32_bf16 v[72:75], v[132:135], v[176:179], v[72:75]
	s_nop 0
	v_mfma_f32_16x16x32_bf16 v[72:75], v[128:131], v[180:183], v[72:75]
	v_mfma_f32_16x16x32_bf16 v[68:71], v[156:159], v[184:187], v[68:71]
	s_nop 0
	v_mfma_f32_16x16x32_bf16 v[68:71], v[136:139], v[188:191], v[68:71]
	v_mfma_f32_16x16x32_bf16 v[64:67], v[132:135], v[184:187], v[64:67]
	s_nop 0
	v_mfma_f32_16x16x32_bf16 v[64:67], v[128:131], v[188:191], v[64:67]
	s_setprio 0
	s_barrier
	ds_read_b128 v[160:163], v197 offset:49152
	ds_read_b128 v[164:167], v197 offset:50176
	ds_read_b128 v[168:171], v197 offset:51200
	ds_read_b128 v[172:175], v197 offset:52224
	ds_read_b128 v[176:179], v197 offset:53248
	ds_read_b128 v[180:183], v197 offset:54272
	ds_read_b128 v[184:187], v197 offset:55296
	ds_read_b128 v[188:191], v197 offset:56320
	s_mov_b32 m0, s72
	s_add_i32 s91, s90, 0x80
	buffer_load_dwordx4 v192, s[8:11], s91 offen lds
	s_add_i32 s91, s90, 0x20080
	s_mov_b32 m0, s73
	s_add_i32 s66, s66, 0x10080
	buffer_load_dwordx4 v192, s[8:11], s91 offen lds
	s_add_i32 s91, s90, 0x2080
	s_mov_b32 m0, s76
	s_add_i32 s90, s90, 0x22080
	buffer_load_dwordx4 v192, s[8:11], s91 offen lds
	s_mov_b32 m0, s77
	s_nop 0
	buffer_load_dwordx4 v192, s[8:11], s90 offen lds
	s_mov_b32 m0, s74
	s_nop 0
	buffer_load_dwordx4 v196, s[4:7], s67 offen lds
	s_mov_b32 m0, s75
	s_nop 0
	buffer_load_dwordx4 v196, s[4:7], s66 offen lds
	s_waitcnt vmcnt(8)
	s_waitcnt lgkmcnt(6)
	s_barrier
	s_setprio 1
	s_waitcnt lgkmcnt(7)
	v_mfma_f32_16x16x32_bf16 v[60:63], v[140:143], v[160:163], v[60:63]
	s_waitcnt lgkmcnt(6)
	v_mfma_f32_16x16x32_bf16 v[60:63], v[144:147], v[164:167], v[60:63]
	v_mfma_f32_16x16x32_bf16 v[56:59], v[148:151], v[160:163], v[56:59]
	s_nop 0
	v_mfma_f32_16x16x32_bf16 v[56:59], v[152:155], v[164:167], v[56:59]
	s_waitcnt lgkmcnt(5)
	v_mfma_f32_16x16x32_bf16 v[52:55], v[140:143], v[168:171], v[52:55]
	s_waitcnt lgkmcnt(4)
	v_mfma_f32_16x16x32_bf16 v[52:55], v[144:147], v[172:175], v[52:55]
	v_mfma_f32_16x16x32_bf16 v[48:51], v[148:151], v[168:171], v[48:51]
	s_nop 0
	v_mfma_f32_16x16x32_bf16 v[48:51], v[152:155], v[172:175], v[48:51]
	s_waitcnt lgkmcnt(3)
	v_mfma_f32_16x16x32_bf16 v[44:47], v[140:143], v[176:179], v[44:47]
	s_waitcnt lgkmcnt(2)
	v_mfma_f32_16x16x32_bf16 v[44:47], v[144:147], v[180:183], v[44:47]
	v_mfma_f32_16x16x32_bf16 v[40:43], v[148:151], v[176:179], v[40:43]
	s_nop 0
	v_mfma_f32_16x16x32_bf16 v[40:43], v[152:155], v[180:183], v[40:43]
	s_waitcnt lgkmcnt(1)
	v_mfma_f32_16x16x32_bf16 v[36:39], v[140:143], v[184:187], v[36:39]
	s_waitcnt lgkmcnt(0)
	v_mfma_f32_16x16x32_bf16 v[36:39], v[144:147], v[188:191], v[36:39]
	v_mfma_f32_16x16x32_bf16 v[32:35], v[148:151], v[184:187], v[32:35]
	s_nop 0
	v_mfma_f32_16x16x32_bf16 v[32:35], v[152:155], v[188:191], v[32:35]
	v_mfma_f32_16x16x32_bf16 v[28:31], v[156:159], v[160:163], v[28:31]
	s_nop 0
	v_mfma_f32_16x16x32_bf16 v[28:31], v[136:139], v[164:167], v[28:31]
	v_mfma_f32_16x16x32_bf16 v[24:27], v[132:135], v[160:163], v[24:27]
	s_nop 0
	v_mfma_f32_16x16x32_bf16 v[24:27], v[128:131], v[164:167], v[24:27]
	v_mfma_f32_16x16x32_bf16 v[20:23], v[156:159], v[168:171], v[20:23]
	s_nop 0
	v_mfma_f32_16x16x32_bf16 v[20:23], v[136:139], v[172:175], v[20:23]
	v_mfma_f32_16x16x32_bf16 v[16:19], v[132:135], v[168:171], v[16:19]
	s_nop 0
	v_mfma_f32_16x16x32_bf16 v[16:19], v[128:131], v[172:175], v[16:19]
	v_mfma_f32_16x16x32_bf16 v[12:15], v[156:159], v[176:179], v[12:15]
	s_nop 0
	v_mfma_f32_16x16x32_bf16 v[12:15], v[136:139], v[180:183], v[12:15]
	v_mfma_f32_16x16x32_bf16 v[8:11], v[132:135], v[176:179], v[8:11]
	s_nop 0
	v_mfma_f32_16x16x32_bf16 v[8:11], v[128:131], v[180:183], v[8:11]
	v_mfma_f32_16x16x32_bf16 v[4:7], v[156:159], v[184:187], v[4:7]
	s_nop 0
	v_mfma_f32_16x16x32_bf16 v[4:7], v[136:139], v[188:191], v[4:7]
	v_mfma_f32_16x16x32_bf16 v[0:3], v[132:135], v[184:187], v[0:3]
	s_nop 0
	v_mfma_f32_16x16x32_bf16 v[0:3], v[128:131], v[188:191], v[0:3]
	s_setprio 0
	s_barrier
	s_add_i32 s43, s43, 2
	s_addk_i32 s33, 0x100
	s_addk_i32 s42, 0x100
	s_cmp_gt_u32 s43, 5
	s_cbranch_scc0 .LBB0_254
	s_and_b64 vcc, exec, s[14:15]
	s_cbranch_vccz .LBB0_257
	s_barrier

.LBB0_341:
	s_waitcnt lgkmcnt(0)
	s_add_i32 s16, s60, 0x100
	s_add_i32 s17, s36, 0x100
	s_barrier
	s_setprio 1
	s_waitcnt lgkmcnt(7)
	v_mfma_f32_16x16x32_bf16 v[124:127], v[164:167], v[196:199], 0
	s_waitcnt lgkmcnt(6)
	v_mfma_f32_16x16x32_bf16 v[124:127], v[160:163], v[192:195], v[124:127]
	v_mfma_f32_16x16x32_bf16 v[120:123], v[156:159], v[196:199], 0
	s_nop 0
	v_mfma_f32_16x16x32_bf16 v[120:123], v[152:155], v[192:195], v[120:123]
	s_waitcnt lgkmcnt(5)
	v_mfma_f32_16x16x32_bf16 v[116:119], v[164:167], v[188:191], 0
	s_waitcnt lgkmcnt(4)
	v_mfma_f32_16x16x32_bf16 v[116:119], v[160:163], v[184:187], v[116:119]
	v_mfma_f32_16x16x32_bf16 v[112:115], v[156:159], v[188:191], 0
	s_nop 0
	v_mfma_f32_16x16x32_bf16 v[112:115], v[152:155], v[184:187], v[112:115]
	s_waitcnt lgkmcnt(3)
	v_mfma_f32_16x16x32_bf16 v[108:111], v[164:167], v[180:183], 0
	s_waitcnt lgkmcnt(2)
	v_mfma_f32_16x16x32_bf16 v[108:111], v[160:163], v[176:179], v[108:111]
	v_mfma_f32_16x16x32_bf16 v[104:107], v[156:159], v[180:183], 0
	s_nop 0
	v_mfma_f32_16x16x32_bf16 v[104:107], v[152:155], v[176:179], v[104:107]
	s_waitcnt lgkmcnt(1)
	v_mfma_f32_16x16x32_bf16 v[100:103], v[164:167], v[172:175], 0
	s_waitcnt lgkmcnt(0)
	v_mfma_f32_16x16x32_bf16 v[100:103], v[160:163], v[168:171], v[100:103]
	v_mfma_f32_16x16x32_bf16 v[96:99], v[156:159], v[172:175], 0
	s_nop 0
	v_mfma_f32_16x16x32_bf16 v[96:99], v[152:155], v[168:171], v[96:99]
	v_mfma_f32_16x16x32_bf16 v[92:95], v[148:151], v[196:199], 0
	s_nop 0
	v_mfma_f32_16x16x32_bf16 v[92:95], v[144:147], v[192:195], v[92:95]
	v_mfma_f32_16x16x32_bf16 v[88:91], v[140:143], v[196:199], 0
	s_nop 0
	v_mfma_f32_16x16x32_bf16 v[88:91], v[136:139], v[192:195], v[88:91]
	v_mfma_f32_16x16x32_bf16 v[84:87], v[148:151], v[188:191], 0
	s_nop 0
	v_mfma_f32_16x16x32_bf16 v[84:87], v[144:147], v[184:187], v[84:87]
	v_mfma_f32_16x16x32_bf16 v[80:83], v[140:143], v[188:191], 0
	s_nop 0
	v_mfma_f32_16x16x32_bf16 v[80:83], v[136:139], v[184:187], v[80:83]
	v_mfma_f32_16x16x32_bf16 v[76:79], v[148:151], v[180:183], 0
	s_nop 0
	v_mfma_f32_16x16x32_bf16 v[76:79], v[144:147], v[176:179], v[76:79]
	v_mfma_f32_16x16x32_bf16 v[72:75], v[140:143], v[180:183], 0
	s_nop 0
	v_mfma_f32_16x16x32_bf16 v[72:75], v[136:139], v[176:179], v[72:75]
	v_mfma_f32_16x16x32_bf16 v[68:71], v[148:151], v[172:175], 0
	s_nop 0
	v_mfma_f32_16x16x32_bf16 v[68:71], v[144:147], v[168:171], v[68:71]
	v_mfma_f32_16x16x32_bf16 v[64:67], v[140:143], v[172:175], 0
	s_nop 0
	v_mfma_f32_16x16x32_bf16 v[64:67], v[136:139], v[168:171], v[64:67]
	s_setprio 0
	s_barrier
	s_mov_b32 m0, s65
	s_mov_b32 s14, s10
	s_mov_b32 s15, s11
	buffer_load_dwordx4 v215, s[12:15], s17 offen lds
	s_add_i32 s17, s36, 0x100100
	s_mov_b32 m0, s68
	s_and_b64 vcc, exec, s[4:5]
	buffer_load_dwordx4 v215, s[12:15], s17 offen lds
	s_add_i32 s17, s36, 0x10100
	s_mov_b32 m0, s69
	s_nop 0
	buffer_load_dwordx4 v215, s[12:15], s17 offen lds
	s_add_i32 s17, s36, 0x110100
	s_mov_b32 m0, s70
	s_nop 0
	buffer_load_dwordx4 v215, s[12:15], s17 offen lds
	s_mov_b32 m0, s64
	s_add_i32 s14, s60, 0x80100
	buffer_load_dwordx4 v214, s[8:11], s16 offen lds
	s_mov_b32 m0, s71
	s_nop 0
	buffer_load_dwordx4 v214, s[8:11], s14 offen lds
	ds_read_b128 v[196:199], v233 offset:16384
	ds_read_b128 v[192:195], v233 offset:17408
	ds_read_b128 v[188:191], v233 offset:18432
	ds_read_b128 v[184:187], v233 offset:19456
	ds_read_b128 v[180:183], v233 offset:20480
	ds_read_b128 v[176:179], v233 offset:21504
	ds_read_b128 v[172:175], v233 offset:22528
	ds_read_b128 v[168:171], v233 offset:23552
	s_cbranch_vccz .LBB0_359
	s_waitcnt vmcnt(34)
	s_cbranch_execnz .LBB0_344

.LBB0_344:
	s_waitcnt lgkmcnt(0)
	s_add_i32 s4, s60, 0x180
	s_add_i32 s5, s36, 0x180
	s_barrier
	s_setprio 1
	s_waitcnt lgkmcnt(7)
	v_mfma_f32_16x16x32_bf16 v[60:63], v[164:167], v[196:199], 0
	s_waitcnt lgkmcnt(6)
	v_mfma_f32_16x16x32_bf16 v[60:63], v[160:163], v[192:195], v[60:63]
	v_mfma_f32_16x16x32_bf16 v[56:59], v[156:159], v[196:199], 0
	s_nop 0
	v_mfma_f32_16x16x32_bf16 v[56:59], v[152:155], v[192:195], v[56:59]
	s_waitcnt lgkmcnt(5)
	v_mfma_f32_16x16x32_bf16 v[52:55], v[164:167], v[188:191], 0
	s_waitcnt lgkmcnt(4)
	v_mfma_f32_16x16x32_bf16 v[52:55], v[160:163], v[184:187], v[52:55]
	v_mfma_f32_16x16x32_bf16 v[48:51], v[156:159], v[188:191], 0
	s_nop 0
	v_mfma_f32_16x16x32_bf16 v[48:51], v[152:155], v[184:187], v[48:51]
	s_waitcnt lgkmcnt(3)
	v_mfma_f32_16x16x32_bf16 v[44:47], v[164:167], v[180:183], 0
	s_waitcnt lgkmcnt(2)
	v_mfma_f32_16x16x32_bf16 v[44:47], v[160:163], v[176:179], v[44:47]
	v_mfma_f32_16x16x32_bf16 v[40:43], v[156:159], v[180:183], 0
	s_nop 0
	v_mfma_f32_16x16x32_bf16 v[40:43], v[152:155], v[176:179], v[40:43]
	s_waitcnt lgkmcnt(1)
	v_mfma_f32_16x16x32_bf16 v[36:39], v[164:167], v[172:175], 0
	s_waitcnt lgkmcnt(0)
	v_mfma_f32_16x16x32_bf16 v[36:39], v[160:163], v[168:171], v[36:39]
	v_mfma_f32_16x16x32_bf16 v[32:35], v[156:159], v[172:175], 0
	s_nop 0
	v_mfma_f32_16x16x32_bf16 v[32:35], v[152:155], v[168:171], v[32:35]
	v_mfma_f32_16x16x32_bf16 v[28:31], v[148:151], v[196:199], 0
	s_nop 0
	v_mfma_f32_16x16x32_bf16 v[28:31], v[144:147], v[192:195], v[28:31]
	v_mfma_f32_16x16x32_bf16 v[24:27], v[140:143], v[196:199], 0
	s_nop 0
	v_mfma_f32_16x16x32_bf16 v[24:27], v[136:139], v[192:195], v[24:27]
	v_mfma_f32_16x16x32_bf16 v[20:23], v[148:151], v[188:191], 0
	s_nop 0
	v_mfma_f32_16x16x32_bf16 v[20:23], v[144:147], v[184:187], v[20:23]
	v_mfma_f32_16x16x32_bf16 v[16:19], v[140:143], v[188:191], 0
	s_nop 0
	v_mfma_f32_16x16x32_bf16 v[16:19], v[136:139], v[184:187], v[16:19]
	v_mfma_f32_16x16x32_bf16 v[12:15], v[148:151], v[180:183], 0
	s_nop 0
	v_mfma_f32_16x16x32_bf16 v[12:15], v[144:147], v[176:179], v[12:15]
	v_mfma_f32_16x16x32_bf16 v[8:11], v[140:143], v[180:183], 0
	s_nop 0
	v_mfma_f32_16x16x32_bf16 v[8:11], v[136:139], v[176:179], v[8:11]
	v_mfma_f32_16x16x32_bf16 v[4:7], v[148:151], v[172:175], 0
	s_nop 0
	v_mfma_f32_16x16x32_bf16 v[4:7], v[144:147], v[168:171], v[4:7]
	v_mfma_f32_16x16x32_bf16 v[0:3], v[140:143], v[172:175], 0
	s_nop 0
	v_mfma_f32_16x16x32_bf16 v[0:3], v[136:139], v[168:171], v[0:3]
	s_setprio 0
	s_barrier
	ds_read_b128 v[164:167], v225
	ds_read_b128 v[160:163], v226
	ds_read_b128 v[156:159], v227
	ds_read_b128 v[152:155], v228
	ds_read_b128 v[148:151], v229
	ds_read_b128 v[144:147], v230
	ds_read_b128 v[140:143], v231
	ds_read_b128 v[136:139], v232
	ds_read_b128 v[168:171], v233 offset:32768
	ds_read_b128 v[172:175], v233 offset:33792
	ds_read_b128 v[176:179], v233 offset:34816
	ds_read_b128 v[180:183], v233 offset:35840
	ds_read_b128 v[184:187], v233 offset:36864
	ds_read_b128 v[188:191], v233 offset:37888
	ds_read_b128 v[192:195], v233 offset:38912
	ds_read_b128 v[196:199], v233 offset:39936
	s_mov_b32 m0, s72
	s_add_i32 s14, s60, 0x100100
	buffer_load_dwordx4 v214, s[8:11], s14 offen lds
	s_add_i32 s14, s60, 0x180100
	s_mov_b32 m0, s73
	s_nop 0
	buffer_load_dwordx4 v214, s[8:11], s14 offen lds
	s_waitcnt vmcnt(10)
	s_waitcnt lgkmcnt(8)
	s_barrier
	s_setprio 1
	s_waitcnt lgkmcnt(7)
	v_mfma_f32_16x16x32_bf16 v[124:127], v[164:167], v[168:171], v[124:127]
	s_waitcnt lgkmcnt(6)
	v_mfma_f32_16x16x32_bf16 v[124:127], v[160:163], v[172:175], v[124:127]
	v_mfma_f32_16x16x32_bf16 v[120:123], v[156:159], v[168:171], v[120:123]
	s_nop 0
	v_mfma_f32_16x16x32_bf16 v[120:123], v[152:155], v[172:175], v[120:123]
	s_waitcnt lgkmcnt(5)
	v_mfma_f32_16x16x32_bf16 v[116:119], v[164:167], v[176:179], v[116:119]
	s_waitcnt lgkmcnt(4)
	v_mfma_f32_16x16x32_bf16 v[116:119], v[160:163], v[180:183], v[116:119]
	v_mfma_f32_16x16x32_bf16 v[112:115], v[156:159], v[176:179], v[112:115]
	s_nop 0
	v_mfma_f32_16x16x32_bf16 v[112:115], v[152:155], v[180:183], v[112:115]
	s_waitcnt lgkmcnt(3)
	v_mfma_f32_16x16x32_bf16 v[108:111], v[164:167], v[184:187], v[108:111]
	s_waitcnt lgkmcnt(2)
	v_mfma_f32_16x16x32_bf16 v[108:111], v[160:163], v[188:191], v[108:111]
	v_mfma_f32_16x16x32_bf16 v[104:107], v[156:159], v[184:187], v[104:107]
	s_nop 0
	v_mfma_f32_16x16x32_bf16 v[104:107], v[152:155], v[188:191], v[104:107]
	s_waitcnt lgkmcnt(1)
	v_mfma_f32_16x16x32_bf16 v[100:103], v[164:167], v[192:195], v[100:103]
	s_waitcnt lgkmcnt(0)
	v_mfma_f32_16x16x32_bf16 v[100:103], v[160:163], v[196:199], v[100:103]
	v_mfma_f32_16x16x32_bf16 v[96:99], v[156:159], v[192:195], v[96:99]
	s_nop 0
	v_mfma_f32_16x16x32_bf16 v[96:99], v[152:155], v[196:199], v[96:99]
	v_mfma_f32_16x16x32_bf16 v[92:95], v[148:151], v[168:171], v[92:95]
	s_nop 0
	v_mfma_f32_16x16x32_bf16 v[92:95], v[144:147], v[172:175], v[92:95]
	v_mfma_f32_16x16x32_bf16 v[88:91], v[140:143], v[168:171], v[88:91]
	s_nop 0
	v_mfma_f32_16x16x32_bf16 v[88:91], v[136:139], v[172:175], v[88:91]
	v_mfma_f32_16x16x32_bf16 v[84:87], v[148:151], v[176:179], v[84:87]
	s_nop 0
	v_mfma_f32_16x16x32_bf16 v[84:87], v[144:147], v[180:183], v[84:87]
	v_mfma_f32_16x16x32_bf16 v[80:83], v[140:143], v[176:179], v[80:83]
	s_nop 0
	v_mfma_f32_16x16x32_bf16 v[80:83], v[136:139], v[180:183], v[80:83]
	v_mfma_f32_16x16x32_bf16 v[76:79], v[148:151], v[184:187], v[76:79]
	s_nop 0
	v_mfma_f32_16x16x32_bf16 v[76:79], v[144:147], v[188:191], v[76:79]
	v_mfma_f32_16x16x32_bf16 v[72:75], v[140:143], v[184:187], v[72:75]
	s_nop 0
	v_mfma_f32_16x16x32_bf16 v[72:75], v[136:139], v[188:191], v[72:75]
	v_mfma_f32_16x16x32_bf16 v[68:71], v[148:151], v[192:195], v[68:71]
	s_nop 0
	v_mfma_f32_16x16x32_bf16 v[68:71], v[144:147], v[196:199], v[68:71]
	v_mfma_f32_16x16x32_bf16 v[64:67], v[140:143], v[192:195], v[64:67]
	s_nop 0
	v_mfma_f32_16x16x32_bf16 v[64:67], v[136:139], v[196:199], v[64:67]
	s_setprio 0
	s_barrier
	ds_read_b128 v[168:171], v233 offset:49152
	ds_read_b128 v[172:175], v233 offset:50176
	ds_read_b128 v[176:179], v233 offset:51200
	ds_read_b128 v[180:183], v233 offset:52224
	ds_read_b128 v[184:187], v233 offset:53248
	ds_read_b128 v[188:191], v233 offset:54272
	ds_read_b128 v[192:195], v233 offset:55296
	ds_read_b128 v[196:199], v233 offset:56320
	s_mov_b32 m0, s76
	s_mov_b32 s14, s10
	s_mov_b32 s15, s11
	buffer_load_dwordx4 v215, s[12:15], s5 offen lds
	s_add_i32 s5, s36, 0x100180
	s_mov_b32 m0, s77
	s_nop 0
	buffer_load_dwordx4 v215, s[12:15], s5 offen lds
	s_add_i32 s5, s36, 0x10180
	s_mov_b32 m0, s80
	s_nop 0
	buffer_load_dwordx4 v215, s[12:15], s5 offen lds
	s_add_i32 s5, s36, 0x110180
	s_mov_b32 m0, s81
	s_nop 0
	buffer_load_dwordx4 v215, s[12:15], s5 offen lds
	s_mov_b32 m0, s78
	s_nop 0
	buffer_load_dwordx4 v214, s[8:11], s4 offen lds
	s_add_i32 s4, s60, 0x80180
	s_mov_b32 m0, s79
	s_nop 0
	buffer_load_dwordx4 v214, s[8:11], s4 offen lds
	s_waitcnt vmcnt(8)
	s_waitcnt lgkmcnt(6)
	s_barrier
	s_setprio 1
	s_waitcnt lgkmcnt(7)
	v_mfma_f32_16x16x32_bf16 v[60:63], v[164:167], v[168:171], v[60:63]
	s_waitcnt lgkmcnt(6)
	v_mfma_f32_16x16x32_bf16 v[60:63], v[160:163], v[172:175], v[60:63]
	v_mfma_f32_16x16x32_bf16 v[56:59], v[156:159], v[168:171], v[56:59]
	s_nop 0
	v_mfma_f32_16x16x32_bf16 v[56:59], v[152:155], v[172:175], v[56:59]
	s_waitcnt lgkmcnt(5)
	v_mfma_f32_16x16x32_bf16 v[52:55], v[164:167], v[176:179], v[52:55]
	s_waitcnt lgkmcnt(4)
	v_mfma_f32_16x16x32_bf16 v[52:55], v[160:163], v[180:183], v[52:55]
	v_mfma_f32_16x16x32_bf16 v[48:51], v[156:159], v[176:179], v[48:51]
	s_nop 0
	v_mfma_f32_16x16x32_bf16 v[48:51], v[152:155], v[180:183], v[48:51]
	s_waitcnt lgkmcnt(3)
	v_mfma_f32_16x16x32_bf16 v[44:47], v[164:167], v[184:187], v[44:47]
	s_waitcnt lgkmcnt(2)
	v_mfma_f32_16x16x32_bf16 v[44:47], v[160:163], v[188:191], v[44:47]
	v_mfma_f32_16x16x32_bf16 v[40:43], v[156:159], v[184:187], v[40:43]
	s_nop 0
	v_mfma_f32_16x16x32_bf16 v[40:43], v[152:155], v[188:191], v[40:43]
	s_waitcnt lgkmcnt(1)
	v_mfma_f32_16x16x32_bf16 v[36:39], v[164:167], v[192:195], v[36:39]
	s_waitcnt lgkmcnt(0)
	v_mfma_f32_16x16x32_bf16 v[36:39], v[160:163], v[196:199], v[36:39]
	v_mfma_f32_16x16x32_bf16 v[32:35], v[156:159], v[192:195], v[32:35]
	s_nop 0
	v_mfma_f32_16x16x32_bf16 v[32:35], v[152:155], v[196:199], v[32:35]
	v_mfma_f32_16x16x32_bf16 v[28:31], v[148:151], v[168:171], v[28:31]
	s_nop 0
	v_mfma_f32_16x16x32_bf16 v[28:31], v[144:147], v[172:175], v[28:31]
	v_mfma_f32_16x16x32_bf16 v[24:27], v[140:143], v[168:171], v[24:27]
	s_nop 0
	v_mfma_f32_16x16x32_bf16 v[24:27], v[136:139], v[172:175], v[24:27]
	v_mfma_f32_16x16x32_bf16 v[20:23], v[148:151], v[176:179], v[20:23]
	s_nop 0
	v_mfma_f32_16x16x32_bf16 v[20:23], v[144:147], v[180:183], v[20:23]
	v_mfma_f32_16x16x32_bf16 v[16:19], v[140:143], v[176:179], v[16:19]
	s_nop 0
	v_mfma_f32_16x16x32_bf16 v[16:19], v[136:139], v[180:183], v[16:19]
	v_mfma_f32_16x16x32_bf16 v[12:15], v[148:151], v[184:187], v[12:15]
	s_nop 0
	v_mfma_f32_16x16x32_bf16 v[12:15], v[144:147], v[188:191], v[12:15]
	v_mfma_f32_16x16x32_bf16 v[8:11], v[140:143], v[184:187], v[8:11]
	s_nop 0
	v_mfma_f32_16x16x32_bf16 v[8:11], v[136:139], v[188:191], v[8:11]
	v_mfma_f32_16x16x32_bf16 v[4:7], v[148:151], v[192:195], v[4:7]
	s_nop 0
	v_mfma_f32_16x16x32_bf16 v[4:7], v[144:147], v[196:199], v[4:7]
	v_mfma_f32_16x16x32_bf16 v[0:3], v[140:143], v[192:195], v[0:3]
	s_nop 0
	v_mfma_f32_16x16x32_bf16 v[0:3], v[136:139], v[196:199], v[0:3]
	s_setprio 0
	s_barrier
	s_waitcnt vmcnt(14)
	v_mul_f32_e32 v132, 0x42800000, v132
	v_mul_f32_e32 v128, 0x42800000, v128
	v_mul_f32_e32 v133, 0x42800000, v133
	v_mul_f32_e32 v129, 0x42800000, v129
	v_mul_f32_e32 v134, 0x42800000, v134
	v_mul_f32_e32 v130, 0x42800000, v130
	v_mul_f32_e32 v135, 0x42800000, v135
	v_mul_f32_e32 v131, 0x42800000, v131
	v_cvt_pk_fp8_f32 v204, v128, v132
	v_cvt_pk_fp8_f32 v234, v129, v133
	v_cvt_pk_fp8_f32 v235, v130, v134
	v_cvt_pk_fp8_f32 v236, v131, v135
	s_add_i32 s33, s36, 0x200
	s_mov_b32 s61, 0
	s_mov_b32 s66, s75
	s_mov_b32 s94, s86
	s_branch .LBB0_347

.LBB0_347:
	v_mov_b32_e32 v152, v204
	v_mov_b32_e32 v153, v234
	v_mov_b32_e32 v154, v235
	v_mov_b32_e32 v155, v236
	ds_read_b128 v[158:161], v217
	ds_read_b128 v[162:165], v218
	ds_read_b128 v[166:169], v219
	ds_read_b128 v[170:173], v220
	ds_read_b128 v[148:151], v221
	ds_read_b128 v[144:147], v222
	ds_read_b128 v[140:143], v223
	ds_read_b128 v[136:139], v224
	ds_read_b128 v[174:177], v233
	ds_read_b128 v[178:181], v233 offset:1024
	ds_read_b128 v[182:185], v233 offset:2048
	ds_read_b128 v[186:189], v233 offset:3072
	ds_read_b128 v[190:193], v233 offset:4096
	ds_read_b128 v[194:197], v233 offset:5120
	ds_read_b128 v[234:237], v233 offset:6144
	ds_read_b128 v[238:241], v233 offset:7168
	s_add_i32 s4, s60, s61
	s_mov_b32 s46, s94
	s_add_i32 s94, s94, 1
	s_add_i32 s5, s4, 0x200
	s_add_i32 s16, s33, s61
	s_cmpk_eq_i32 s61, 0x1e00
	s_cselect_b32 s47, s90, s5
	s_cselect_b32 s97, s91, s16
	s_add_i32 s96, s47, 0x80
	s_mov_b32 m0, s82
	s_add_i32 s5, s4, 0x100180
	buffer_load_dwordx4 v214, s[8:11], s5 offen lds
	s_add_i32 s4, s4, 0x180180
	s_mov_b32 m0, s85
	s_add_i32 vcc_lo, s97, 0x80
	buffer_load_dwordx4 v214, s[8:11], s4 offen lds
	s_lshr_b32 s4, s94, 2
	s_mul_i32 s5, s4, s34
	s_add_i32 s16, s5, s2
	s_cmp_lt_i32 s4, s3
	s_cselect_b64 s[4:5], -1, 0
	s_and_b64 s[44:45], s[4:5], exec
	s_cselect_b32 s16, s16, 0
	s_bfe_u32 s17, s94, 0x10001
	s_or_b32 s17, s17, s83
	s_bfe_u32 s67, s16, 0x50007
	s_bfe_u32 s36, s16, 0x50002
	s_and_b32 s95, s16, 3
	s_cmpk_gt_i32 s16, 0xfff
	s_cselect_b64 s[44:45], -1, 0
	v_lshl_or_b32 v156, s17, 3, v216
	s_and_b64 s[16:17], s[44:45], exec
	s_cselect_b32 s16, s25, s21
	s_cselect_b32 s17, s24, s20
	s_lshl_b32 vcc_hi, s67, 23
	s_add_u32 s17, s17, vcc_hi
	s_addc_u32 s16, s16, 0
	s_lshl_b32 vcc_hi, s36, 18
	s_add_u32 s17, s17, vcc_hi
	s_addc_u32 vcc_hi, s16, 0
	s_lshl_b32 s16, s95, 9
	s_add_u32 s16, s17, s16
	v_and_or_b32 v204, s66, 2, v200
	s_addc_u32 s17, vcc_hi, 0
	v_lshlrev_b64 v[128:129], 11, v[204:205]
	v_lshl_add_u64 v[128:129], s[16:17], 0, v[128:129]
	v_lshlrev_b32_e32 v204, 4, v156
	v_lshl_add_u64 v[132:133], v[128:129], 0, v[204:205]
	global_load_dwordx4 v[128:131], v[132:133], off nt
	s_nop 0
	global_load_dwordx4 v[132:135], v[132:133], off offset:2048 nt
	s_waitcnt vmcnt(10)
	s_waitcnt lgkmcnt(8)
	s_barrier
	s_setprio 1
	s_waitcnt lgkmcnt(7)
	v_mfma_f32_16x16x32_bf16 v[124:127], v[158:161], v[174:177], v[124:127]
	s_waitcnt lgkmcnt(6)
	v_mfma_f32_16x16x32_bf16 v[124:127], v[162:165], v[178:181], v[124:127]
	v_mfma_f32_16x16x32_bf16 v[120:123], v[166:169], v[174:177], v[120:123]
	s_nop 0
	v_mfma_f32_16x16x32_bf16 v[120:123], v[170:173], v[178:181], v[120:123]
	s_waitcnt lgkmcnt(5)
	v_mfma_f32_16x16x32_bf16 v[116:119], v[158:161], v[182:185], v[116:119]
	s_waitcnt lgkmcnt(4)
	v_mfma_f32_16x16x32_bf16 v[116:119], v[162:165], v[186:189], v[116:119]
	v_mfma_f32_16x16x32_bf16 v[112:115], v[166:169], v[182:185], v[112:115]
	s_nop 0
	v_mfma_f32_16x16x32_bf16 v[112:115], v[170:173], v[186:189], v[112:115]
	s_waitcnt lgkmcnt(3)
	v_mfma_f32_16x16x32_bf16 v[108:111], v[158:161], v[190:193], v[108:111]
	s_waitcnt lgkmcnt(2)
	v_mfma_f32_16x16x32_bf16 v[108:111], v[162:165], v[194:197], v[108:111]
	v_mfma_f32_16x16x32_bf16 v[104:107], v[166:169], v[190:193], v[104:107]
	s_nop 0
	v_mfma_f32_16x16x32_bf16 v[104:107], v[170:173], v[194:197], v[104:107]
	s_waitcnt lgkmcnt(1)
	v_mfma_f32_16x16x32_bf16 v[100:103], v[158:161], v[234:237], v[100:103]
	s_waitcnt lgkmcnt(0)
	v_mfma_f32_16x16x32_bf16 v[100:103], v[162:165], v[238:241], v[100:103]
	v_mfma_f32_16x16x32_bf16 v[96:99], v[166:169], v[234:237], v[96:99]
	s_nop 0
	v_mfma_f32_16x16x32_bf16 v[96:99], v[170:173], v[238:241], v[96:99]
	v_mfma_f32_16x16x32_bf16 v[92:95], v[148:151], v[174:177], v[92:95]
	s_nop 0
	v_mfma_f32_16x16x32_bf16 v[92:95], v[144:147], v[178:181], v[92:95]
	v_mfma_f32_16x16x32_bf16 v[88:91], v[140:143], v[174:177], v[88:91]
	s_nop 0
	v_mfma_f32_16x16x32_bf16 v[88:91], v[136:139], v[178:181], v[88:91]
	v_mfma_f32_16x16x32_bf16 v[84:87], v[148:151], v[182:185], v[84:87]
	s_nop 0
	v_mfma_f32_16x16x32_bf16 v[84:87], v[144:147], v[186:189], v[84:87]
	v_mfma_f32_16x16x32_bf16 v[80:83], v[140:143], v[182:185], v[80:83]
	s_nop 0
	v_mfma_f32_16x16x32_bf16 v[80:83], v[136:139], v[186:189], v[80:83]
	v_mfma_f32_16x16x32_bf16 v[76:79], v[148:151], v[190:193], v[76:79]
	s_nop 0
	v_mfma_f32_16x16x32_bf16 v[76:79], v[144:147], v[194:197], v[76:79]
	v_mfma_f32_16x16x32_bf16 v[72:75], v[140:143], v[190:193], v[72:75]
	s_nop 0
	v_mfma_f32_16x16x32_bf16 v[72:75], v[136:139], v[194:197], v[72:75]
	v_mfma_f32_16x16x32_bf16 v[68:71], v[148:151], v[234:237], v[68:71]
	s_nop 0
	v_mfma_f32_16x16x32_bf16 v[68:71], v[144:147], v[238:241], v[68:71]
	v_mfma_f32_16x16x32_bf16 v[64:67], v[140:143], v[234:237], v[64:67]
	s_nop 0
	v_mfma_f32_16x16x32_bf16 v[64:67], v[136:139], v[238:241], v[64:67]
	s_setprio 0
	s_barrier
	ds_read_b128 v[174:177], v233 offset:16384
	ds_read_b128 v[178:181], v233 offset:17408
	ds_read_b128 v[182:185], v233 offset:18432
	ds_read_b128 v[186:189], v233 offset:19456
	ds_read_b128 v[190:193], v233 offset:20480
	ds_read_b128 v[194:197], v233 offset:21504
	ds_read_b128 v[234:237], v233 offset:22528
	ds_read_b128 v[238:241], v233 offset:23552
	s_mov_b32 m0, s65
	s_add_i32 s16, s97, 0x100000
	buffer_load_dwordx4 v215, s[12:15], s97 offen lds
	s_mov_b32 m0, s68
	s_nop 0
	buffer_load_dwordx4 v215, s[12:15], s16 offen lds
	s_add_i32 s16, s97, 0x10000
	s_mov_b32 m0, s69
	s_nop 0
	buffer_load_dwordx4 v215, s[12:15], s16 offen lds
	s_add_i32 s16, s97, 0x110000
	s_mov_b32 m0, s70
	s_nop 0
	buffer_load_dwordx4 v215, s[12:15], s16 offen lds
	s_mov_b32 m0, s64
	s_add_i32 s16, s47, 0x80000
	buffer_load_dwordx4 v214, s[8:11], s47 offen lds
	s_mov_b32 m0, s71
	s_nop 0
	buffer_load_dwordx4 v214, s[8:11], s16 offen lds
	s_waitcnt vmcnt(10)
	s_waitcnt lgkmcnt(6)
	s_barrier
	s_setprio 1
	s_waitcnt lgkmcnt(7)
	v_mfma_f32_16x16x32_bf16 v[60:63], v[158:161], v[174:177], v[60:63]
	s_waitcnt lgkmcnt(6)
	v_mfma_f32_16x16x32_bf16 v[60:63], v[162:165], v[178:181], v[60:63]
	v_mfma_f32_16x16x32_bf16 v[56:59], v[166:169], v[174:177], v[56:59]
	s_nop 0
	v_mfma_f32_16x16x32_bf16 v[56:59], v[170:173], v[178:181], v[56:59]
	s_waitcnt lgkmcnt(5)
	v_mfma_f32_16x16x32_bf16 v[52:55], v[158:161], v[182:185], v[52:55]
	s_waitcnt lgkmcnt(4)
	v_mfma_f32_16x16x32_bf16 v[52:55], v[162:165], v[186:189], v[52:55]
	v_mfma_f32_16x16x32_bf16 v[48:51], v[166:169], v[182:185], v[48:51]
	s_nop 0
	v_mfma_f32_16x16x32_bf16 v[48:51], v[170:173], v[186:189], v[48:51]
	s_waitcnt lgkmcnt(3)
	v_mfma_f32_16x16x32_bf16 v[44:47], v[158:161], v[190:193], v[44:47]
	s_waitcnt lgkmcnt(2)
	v_mfma_f32_16x16x32_bf16 v[44:47], v[162:165], v[194:197], v[44:47]
	v_mfma_f32_16x16x32_bf16 v[40:43], v[166:169], v[190:193], v[40:43]
	s_nop 0
	v_mfma_f32_16x16x32_bf16 v[40:43], v[170:173], v[194:197], v[40:43]
	s_waitcnt lgkmcnt(1)
	v_mfma_f32_16x16x32_bf16 v[36:39], v[158:161], v[234:237], v[36:39]
	s_waitcnt lgkmcnt(0)
	v_mfma_f32_16x16x32_bf16 v[36:39], v[162:165], v[238:241], v[36:39]
	v_mfma_f32_16x16x32_bf16 v[32:35], v[166:169], v[234:237], v[32:35]
	s_nop 0
	v_mfma_f32_16x16x32_bf16 v[32:35], v[170:173], v[238:241], v[32:35]
	v_mfma_f32_16x16x32_bf16 v[28:31], v[148:151], v[174:177], v[28:31]
	s_nop 0
	v_mfma_f32_16x16x32_bf16 v[28:31], v[144:147], v[178:181], v[28:31]
	v_mfma_f32_16x16x32_bf16 v[24:27], v[140:143], v[174:177], v[24:27]
	s_nop 0
	v_mfma_f32_16x16x32_bf16 v[24:27], v[136:139], v[178:181], v[24:27]
	v_mfma_f32_16x16x32_bf16 v[20:23], v[148:151], v[182:185], v[20:23]
	s_nop 0
	v_mfma_f32_16x16x32_bf16 v[20:23], v[144:147], v[186:189], v[20:23]
	v_mfma_f32_16x16x32_bf16 v[16:19], v[140:143], v[182:185], v[16:19]
	s_nop 0
	v_mfma_f32_16x16x32_bf16 v[16:19], v[136:139], v[186:189], v[16:19]
	v_mfma_f32_16x16x32_bf16 v[12:15], v[148:151], v[190:193], v[12:15]
	s_nop 0
	v_mfma_f32_16x16x32_bf16 v[12:15], v[144:147], v[194:197], v[12:15]
	v_mfma_f32_16x16x32_bf16 v[8:11], v[140:143], v[190:193], v[8:11]
	s_nop 0
	v_mfma_f32_16x16x32_bf16 v[8:11], v[136:139], v[194:197], v[8:11]
	v_mfma_f32_16x16x32_bf16 v[4:7], v[148:151], v[234:237], v[4:7]
	s_nop 0
	v_mfma_f32_16x16x32_bf16 v[4:7], v[144:147], v[238:241], v[4:7]
	v_mfma_f32_16x16x32_bf16 v[0:3], v[140:143], v[234:237], v[0:3]
	s_nop 0
	v_mfma_f32_16x16x32_bf16 v[0:3], v[136:139], v[238:241], v[0:3]
	s_setprio 0
	s_barrier
	ds_read_b128 v[136:139], v225
	ds_read_b128 v[140:143], v226
	ds_read_b128 v[144:147], v227
	ds_read_b128 v[148:151], v228
	ds_read_b128 v[158:161], v229
	ds_read_b128 v[162:165], v230
	ds_read_b128 v[166:169], v231
	ds_read_b128 v[170:173], v232
	ds_read_b128 v[174:177], v233 offset:32768
	ds_read_b128 v[178:181], v233 offset:33792
	ds_read_b128 v[182:185], v233 offset:34816
	ds_read_b128 v[186:189], v233 offset:35840
	ds_read_b128 v[190:193], v233 offset:36864
	ds_read_b128 v[194:197], v233 offset:37888
	ds_read_b128 v[234:237], v233 offset:38912
	ds_read_b128 v[238:241], v233 offset:39936
	s_mov_b32 m0, s72
	s_add_i32 s16, s47, 0x100000
	buffer_load_dwordx4 v214, s[8:11], s16 offen lds
	s_add_i32 s16, s47, 0x180000
	s_mov_b32 m0, s73
	s_nop 0
	buffer_load_dwordx4 v214, s[8:11], s16 offen lds
	s_waitcnt vmcnt(10)
	s_waitcnt lgkmcnt(8)
	s_barrier
	s_setprio 1
	s_waitcnt lgkmcnt(7)
	v_mfma_f32_16x16x32_bf16 v[124:127], v[136:139], v[174:177], v[124:127]
	s_waitcnt lgkmcnt(6)
	v_mfma_f32_16x16x32_bf16 v[124:127], v[140:143], v[178:181], v[124:127]
	v_mfma_f32_16x16x32_bf16 v[120:123], v[144:147], v[174:177], v[120:123]
	s_nop 0
	v_mfma_f32_16x16x32_bf16 v[120:123], v[148:151], v[178:181], v[120:123]
	s_waitcnt lgkmcnt(5)
	v_mfma_f32_16x16x32_bf16 v[116:119], v[136:139], v[182:185], v[116:119]
	s_waitcnt lgkmcnt(4)
	v_mfma_f32_16x16x32_bf16 v[116:119], v[140:143], v[186:189], v[116:119]
	v_mfma_f32_16x16x32_bf16 v[112:115], v[144:147], v[182:185], v[112:115]
	s_nop 0
	v_mfma_f32_16x16x32_bf16 v[112:115], v[148:151], v[186:189], v[112:115]
	s_waitcnt lgkmcnt(3)
	v_mfma_f32_16x16x32_bf16 v[108:111], v[136:139], v[190:193], v[108:111]
	s_waitcnt lgkmcnt(2)
	v_mfma_f32_16x16x32_bf16 v[108:111], v[140:143], v[194:197], v[108:111]
	v_mfma_f32_16x16x32_bf16 v[104:107], v[144:147], v[190:193], v[104:107]
	s_nop 0
	v_mfma_f32_16x16x32_bf16 v[104:107], v[148:151], v[194:197], v[104:107]
	s_waitcnt lgkmcnt(1)
	v_mfma_f32_16x16x32_bf16 v[100:103], v[136:139], v[234:237], v[100:103]
	s_waitcnt lgkmcnt(0)
	v_mfma_f32_16x16x32_bf16 v[100:103], v[140:143], v[238:241], v[100:103]
	v_mfma_f32_16x16x32_bf16 v[96:99], v[144:147], v[234:237], v[96:99]
	s_nop 0
	v_mfma_f32_16x16x32_bf16 v[96:99], v[148:151], v[238:241], v[96:99]
	v_mfma_f32_16x16x32_bf16 v[92:95], v[158:161], v[174:177], v[92:95]
	s_nop 0
	v_mfma_f32_16x16x32_bf16 v[92:95], v[162:165], v[178:181], v[92:95]
	v_mfma_f32_16x16x32_bf16 v[88:91], v[166:169], v[174:177], v[88:91]
	s_nop 0
	v_mfma_f32_16x16x32_bf16 v[88:91], v[170:173], v[178:181], v[88:91]
	v_mfma_f32_16x16x32_bf16 v[84:87], v[158:161], v[182:185], v[84:87]
	s_nop 0
	v_mfma_f32_16x16x32_bf16 v[84:87], v[162:165], v[186:189], v[84:87]
	v_mfma_f32_16x16x32_bf16 v[80:83], v[166:169], v[182:185], v[80:83]
	s_nop 0
	v_mfma_f32_16x16x32_bf16 v[80:83], v[170:173], v[186:189], v[80:83]
	v_mfma_f32_16x16x32_bf16 v[76:79], v[158:161], v[190:193], v[76:79]
	s_nop 0
	v_mfma_f32_16x16x32_bf16 v[76:79], v[162:165], v[194:197], v[76:79]
	v_mfma_f32_16x16x32_bf16 v[72:75], v[166:169], v[190:193], v[72:75]
	s_nop 0
	v_mfma_f32_16x16x32_bf16 v[72:75], v[170:173], v[194:197], v[72:75]
	v_mfma_f32_16x16x32_bf16 v[68:71], v[158:161], v[234:237], v[68:71]
	s_nop 0
	v_mfma_f32_16x16x32_bf16 v[68:71], v[162:165], v[238:241], v[68:71]
	v_mfma_f32_16x16x32_bf16 v[64:67], v[166:169], v[234:237], v[64:67]
	s_nop 0
	v_mfma_f32_16x16x32_bf16 v[64:67], v[170:173], v[238:241], v[64:67]
	s_setprio 0
	s_barrier
	ds_read_b128 v[174:177], v233 offset:49152
	ds_read_b128 v[178:181], v233 offset:50176
	ds_read_b128 v[182:185], v233 offset:51200
	ds_read_b128 v[186:189], v233 offset:52224
	ds_read_b128 v[190:193], v233 offset:53248
	ds_read_b128 v[194:197], v233 offset:54272
	ds_read_b128 v[234:237], v233 offset:55296
	ds_read_b128 v[238:241], v233 offset:56320
	s_mov_b32 m0, s76
	s_add_i32 s16, s97, 0x100080
	buffer_load_dwordx4 v215, s[12:15], vcc_lo offen lds
	s_mov_b32 m0, s77
	s_add_i32 s47, s47, 0x80080
	buffer_load_dwordx4 v215, s[12:15], s16 offen lds
	s_add_i32 s16, s97, 0x10080
	s_mov_b32 m0, s80
	s_add_i32 s97, s97, 0x110080
	buffer_load_dwordx4 v215, s[12:15], s16 offen lds
	s_mov_b32 m0, s81
	s_nop 0
	buffer_load_dwordx4 v215, s[12:15], s97 offen lds
	s_mov_b32 m0, s78
	s_nop 0
	buffer_load_dwordx4 v214, s[8:11], s96 offen lds
	s_mov_b32 m0, s79
	s_nop 0
	buffer_load_dwordx4 v214, s[8:11], s47 offen lds
	s_waitcnt vmcnt(8)
	s_waitcnt lgkmcnt(6)
	s_barrier
	s_setprio 1
	s_waitcnt lgkmcnt(7)
	v_mfma_f32_16x16x32_bf16 v[60:63], v[136:139], v[174:177], v[60:63]
	s_waitcnt lgkmcnt(6)
	v_mfma_f32_16x16x32_bf16 v[60:63], v[140:143], v[178:181], v[60:63]
	v_mfma_f32_16x16x32_bf16 v[56:59], v[144:147], v[174:177], v[56:59]
	s_nop 0
	v_mfma_f32_16x16x32_bf16 v[56:59], v[148:151], v[178:181], v[56:59]
	s_waitcnt lgkmcnt(5)
	v_mfma_f32_16x16x32_bf16 v[52:55], v[136:139], v[182:185], v[52:55]
	s_waitcnt lgkmcnt(4)
	v_mfma_f32_16x16x32_bf16 v[52:55], v[140:143], v[186:189], v[52:55]
	v_mfma_f32_16x16x32_bf16 v[48:51], v[144:147], v[182:185], v[48:51]
	s_nop 0
	v_mfma_f32_16x16x32_bf16 v[48:51], v[148:151], v[186:189], v[48:51]
	s_waitcnt lgkmcnt(3)
	v_mfma_f32_16x16x32_bf16 v[44:47], v[136:139], v[190:193], v[44:47]
	s_waitcnt lgkmcnt(2)
	v_mfma_f32_16x16x32_bf16 v[44:47], v[140:143], v[194:197], v[44:47]
	v_mfma_f32_16x16x32_bf16 v[40:43], v[144:147], v[190:193], v[40:43]
	s_nop 0
	v_mfma_f32_16x16x32_bf16 v[40:43], v[148:151], v[194:197], v[40:43]
	s_waitcnt lgkmcnt(1)
	v_mfma_f32_16x16x32_bf16 v[36:39], v[136:139], v[234:237], v[36:39]
	s_waitcnt lgkmcnt(0)
	v_mfma_f32_16x16x32_bf16 v[36:39], v[140:143], v[238:241], v[36:39]
	v_mfma_f32_16x16x32_bf16 v[32:35], v[144:147], v[234:237], v[32:35]
	s_nop 0
	v_mfma_f32_16x16x32_bf16 v[32:35], v[148:151], v[238:241], v[32:35]
	v_mfma_f32_16x16x32_bf16 v[28:31], v[158:161], v[174:177], v[28:31]
	s_nop 0
	v_mfma_f32_16x16x32_bf16 v[28:31], v[162:165], v[178:181], v[28:31]
	v_mfma_f32_16x16x32_bf16 v[24:27], v[166:169], v[174:177], v[24:27]
	s_nop 0
	v_mfma_f32_16x16x32_bf16 v[24:27], v[170:173], v[178:181], v[24:27]
	v_mfma_f32_16x16x32_bf16 v[20:23], v[158:161], v[182:185], v[20:23]
	s_nop 0
	v_mfma_f32_16x16x32_bf16 v[20:23], v[162:165], v[186:189], v[20:23]
	v_mfma_f32_16x16x32_bf16 v[16:19], v[166:169], v[182:185], v[16:19]
	s_nop 0
	v_mfma_f32_16x16x32_bf16 v[16:19], v[170:173], v[186:189], v[16:19]
	v_mfma_f32_16x16x32_bf16 v[12:15], v[158:161], v[190:193], v[12:15]
	s_nop 0
	v_mfma_f32_16x16x32_bf16 v[12:15], v[162:165], v[194:197], v[12:15]
	v_mfma_f32_16x16x32_bf16 v[8:11], v[166:169], v[190:193], v[8:11]
	s_nop 0
	v_mfma_f32_16x16x32_bf16 v[8:11], v[170:173], v[194:197], v[8:11]
	v_mfma_f32_16x16x32_bf16 v[4:7], v[158:161], v[234:237], v[4:7]
	s_nop 0
	v_mfma_f32_16x16x32_bf16 v[4:7], v[162:165], v[238:241], v[4:7]
	v_mfma_f32_16x16x32_bf16 v[0:3], v[166:169], v[234:237], v[0:3]
	s_nop 0
	v_mfma_f32_16x16x32_bf16 v[0:3], v[170:173], v[238:241], v[0:3]
	s_setprio 0
	s_barrier
	s_bitcmp0_b32 s46, 0
	s_waitcnt vmcnt(15)
	v_mul_f32_e32 v128, 0x42800000, v128
	s_waitcnt vmcnt(14)
	v_mul_f32_e32 v132, 0x42800000, v132
	v_mul_f32_e32 v129, 0x42800000, v129
	v_mul_f32_e32 v133, 0x42800000, v133
	v_mul_f32_e32 v130, 0x42800000, v130
	v_mul_f32_e32 v134, 0x42800000, v134
	v_mul_f32_e32 v131, 0x42800000, v131
	v_mul_f32_e32 v135, 0x42800000, v135
	s_mov_b64 s[46:47], -1
	s_cbranch_scc0 .LBB0_350
	s_andn2_b64 vcc, exec, s[46:47]
	s_cbranch_vccnz .LBB0_346
	s_branch .LBB0_351

.LBB0_589:
	s_waitcnt lgkmcnt(0)
	s_add_i32 s33, s60, 0x100
	s_add_i32 s43, s42, 0x100
	s_barrier
	s_setprio 1
	s_waitcnt lgkmcnt(7)
	v_mfma_f32_16x16x32_bf16 v[124:127], v[164:167], v[196:199], 0
	s_waitcnt lgkmcnt(6)
	v_mfma_f32_16x16x32_bf16 v[124:127], v[160:163], v[192:195], v[124:127]
	v_mfma_f32_16x16x32_bf16 v[120:123], v[156:159], v[196:199], 0
	s_nop 0
	v_mfma_f32_16x16x32_bf16 v[120:123], v[152:155], v[192:195], v[120:123]
	s_waitcnt lgkmcnt(5)
	v_mfma_f32_16x16x32_bf16 v[116:119], v[164:167], v[188:191], 0
	s_waitcnt lgkmcnt(4)
	v_mfma_f32_16x16x32_bf16 v[116:119], v[160:163], v[184:187], v[116:119]
	v_mfma_f32_16x16x32_bf16 v[112:115], v[156:159], v[188:191], 0
	s_nop 0
	v_mfma_f32_16x16x32_bf16 v[112:115], v[152:155], v[184:187], v[112:115]
	s_waitcnt lgkmcnt(3)
	v_mfma_f32_16x16x32_bf16 v[108:111], v[164:167], v[180:183], 0
	s_waitcnt lgkmcnt(2)
	v_mfma_f32_16x16x32_bf16 v[108:111], v[160:163], v[176:179], v[108:111]
	v_mfma_f32_16x16x32_bf16 v[104:107], v[156:159], v[180:183], 0
	s_nop 0
	v_mfma_f32_16x16x32_bf16 v[104:107], v[152:155], v[176:179], v[104:107]
	s_waitcnt lgkmcnt(1)
	v_mfma_f32_16x16x32_bf16 v[100:103], v[164:167], v[172:175], 0
	s_waitcnt lgkmcnt(0)
	v_mfma_f32_16x16x32_bf16 v[100:103], v[160:163], v[168:171], v[100:103]
	v_mfma_f32_16x16x32_bf16 v[96:99], v[156:159], v[172:175], 0
	s_nop 0
	v_mfma_f32_16x16x32_bf16 v[96:99], v[152:155], v[168:171], v[96:99]
	v_mfma_f32_16x16x32_bf16 v[92:95], v[148:151], v[196:199], 0
	s_nop 0
	v_mfma_f32_16x16x32_bf16 v[92:95], v[144:147], v[192:195], v[92:95]
	v_mfma_f32_16x16x32_bf16 v[88:91], v[140:143], v[196:199], 0
	s_nop 0
	v_mfma_f32_16x16x32_bf16 v[88:91], v[136:139], v[192:195], v[88:91]
	v_mfma_f32_16x16x32_bf16 v[84:87], v[148:151], v[188:191], 0
	s_nop 0
	v_mfma_f32_16x16x32_bf16 v[84:87], v[144:147], v[184:187], v[84:87]
	v_mfma_f32_16x16x32_bf16 v[80:83], v[140:143], v[188:191], 0
	s_nop 0
	v_mfma_f32_16x16x32_bf16 v[80:83], v[136:139], v[184:187], v[80:83]
	v_mfma_f32_16x16x32_bf16 v[76:79], v[148:151], v[180:183], 0
	s_nop 0
	v_mfma_f32_16x16x32_bf16 v[76:79], v[144:147], v[176:179], v[76:79]
	v_mfma_f32_16x16x32_bf16 v[72:75], v[140:143], v[180:183], 0
	s_nop 0
	v_mfma_f32_16x16x32_bf16 v[72:75], v[136:139], v[176:179], v[72:75]
	v_mfma_f32_16x16x32_bf16 v[68:71], v[148:151], v[172:175], 0
	s_nop 0
	v_mfma_f32_16x16x32_bf16 v[68:71], v[144:147], v[168:171], v[68:71]
	v_mfma_f32_16x16x32_bf16 v[64:67], v[140:143], v[172:175], 0
	s_nop 0
	v_mfma_f32_16x16x32_bf16 v[64:67], v[136:139], v[168:171], v[64:67]
	s_setprio 0
	s_barrier
	s_mov_b32 m0, s47
	s_mov_b32 s10, s14
	s_mov_b32 s11, s15
	buffer_load_dwordx4 v214, s[8:11], s43 offen lds
	s_add_i32 s43, s42, 0x40100
	s_mov_b32 m0, s62
	s_and_b64 vcc, exec, s[4:5]
	buffer_load_dwordx4 v214, s[8:11], s43 offen lds
	s_add_i32 s43, s42, 0x4100
	s_mov_b32 m0, s63
	s_nop 0
	buffer_load_dwordx4 v214, s[8:11], s43 offen lds
	s_add_i32 s43, s42, 0x44100
	s_mov_b32 m0, s64
	s_nop 0
	buffer_load_dwordx4 v214, s[8:11], s43 offen lds
	s_mov_b32 m0, s46
	s_add_i32 s10, s60, 0x80100
	buffer_load_dwordx4 v213, s[12:15], s33 offen lds
	s_mov_b32 m0, s65
	s_nop 0
	buffer_load_dwordx4 v213, s[12:15], s10 offen lds
	ds_read_b128 v[196:199], v232 offset:16384
	ds_read_b128 v[192:195], v232 offset:17408
	ds_read_b128 v[188:191], v232 offset:18432
	ds_read_b128 v[184:187], v232 offset:19456
	ds_read_b128 v[180:183], v232 offset:20480
	ds_read_b128 v[176:179], v232 offset:21504
	ds_read_b128 v[172:175], v232 offset:22528
	ds_read_b128 v[168:171], v232 offset:23552
	s_cbranch_vccz .LBB0_607
	s_waitcnt vmcnt(26)
	s_cbranch_execnz .LBB0_592

.LBB0_592:
	s_waitcnt lgkmcnt(0)
	s_add_i32 s4, s60, 0x180
	s_add_i32 s5, s42, 0x180
	s_barrier
	s_setprio 1
	s_waitcnt lgkmcnt(7)
	v_mfma_f32_16x16x32_bf16 v[60:63], v[164:167], v[196:199], 0
	s_waitcnt lgkmcnt(6)
	v_mfma_f32_16x16x32_bf16 v[60:63], v[160:163], v[192:195], v[60:63]
	v_mfma_f32_16x16x32_bf16 v[56:59], v[156:159], v[196:199], 0
	s_nop 0
	v_mfma_f32_16x16x32_bf16 v[56:59], v[152:155], v[192:195], v[56:59]
	s_waitcnt lgkmcnt(5)
	v_mfma_f32_16x16x32_bf16 v[52:55], v[164:167], v[188:191], 0
	s_waitcnt lgkmcnt(4)
	v_mfma_f32_16x16x32_bf16 v[52:55], v[160:163], v[184:187], v[52:55]
	v_mfma_f32_16x16x32_bf16 v[48:51], v[156:159], v[188:191], 0
	s_nop 0
	v_mfma_f32_16x16x32_bf16 v[48:51], v[152:155], v[184:187], v[48:51]
	s_waitcnt lgkmcnt(3)
	v_mfma_f32_16x16x32_bf16 v[44:47], v[164:167], v[180:183], 0
	s_waitcnt lgkmcnt(2)
	v_mfma_f32_16x16x32_bf16 v[44:47], v[160:163], v[176:179], v[44:47]
	v_mfma_f32_16x16x32_bf16 v[40:43], v[156:159], v[180:183], 0
	s_nop 0
	v_mfma_f32_16x16x32_bf16 v[40:43], v[152:155], v[176:179], v[40:43]
	s_waitcnt lgkmcnt(1)
	v_mfma_f32_16x16x32_bf16 v[36:39], v[164:167], v[172:175], 0
	s_waitcnt lgkmcnt(0)
	v_mfma_f32_16x16x32_bf16 v[36:39], v[160:163], v[168:171], v[36:39]
	v_mfma_f32_16x16x32_bf16 v[32:35], v[156:159], v[172:175], 0
	s_nop 0
	v_mfma_f32_16x16x32_bf16 v[32:35], v[152:155], v[168:171], v[32:35]
	v_mfma_f32_16x16x32_bf16 v[28:31], v[148:151], v[196:199], 0
	s_nop 0
	v_mfma_f32_16x16x32_bf16 v[28:31], v[144:147], v[192:195], v[28:31]
	v_mfma_f32_16x16x32_bf16 v[24:27], v[140:143], v[196:199], 0
	s_nop 0
	v_mfma_f32_16x16x32_bf16 v[24:27], v[136:139], v[192:195], v[24:27]
	v_mfma_f32_16x16x32_bf16 v[20:23], v[148:151], v[188:191], 0
	s_nop 0
	v_mfma_f32_16x16x32_bf16 v[20:23], v[144:147], v[184:187], v[20:23]
	v_mfma_f32_16x16x32_bf16 v[16:19], v[140:143], v[188:191], 0
	s_nop 0
	v_mfma_f32_16x16x32_bf16 v[16:19], v[136:139], v[184:187], v[16:19]
	v_mfma_f32_16x16x32_bf16 v[12:15], v[148:151], v[180:183], 0
	s_nop 0
	v_mfma_f32_16x16x32_bf16 v[12:15], v[144:147], v[176:179], v[12:15]
	v_mfma_f32_16x16x32_bf16 v[8:11], v[140:143], v[180:183], 0
	s_nop 0
	v_mfma_f32_16x16x32_bf16 v[8:11], v[136:139], v[176:179], v[8:11]
	v_mfma_f32_16x16x32_bf16 v[4:7], v[148:151], v[172:175], 0
	s_nop 0
	v_mfma_f32_16x16x32_bf16 v[4:7], v[144:147], v[168:171], v[4:7]
	v_mfma_f32_16x16x32_bf16 v[0:3], v[140:143], v[172:175], 0
	s_nop 0
	v_mfma_f32_16x16x32_bf16 v[0:3], v[136:139], v[168:171], v[0:3]
	s_setprio 0
	s_barrier
	ds_read_b128 v[164:167], v224
	ds_read_b128 v[160:163], v225
	ds_read_b128 v[156:159], v226
	ds_read_b128 v[152:155], v227
	ds_read_b128 v[148:151], v228
	ds_read_b128 v[144:147], v229
	ds_read_b128 v[140:143], v230
	ds_read_b128 v[136:139], v231
	ds_read_b128 v[168:171], v232 offset:32768
	ds_read_b128 v[172:175], v232 offset:33792
	ds_read_b128 v[176:179], v232 offset:34816
	ds_read_b128 v[180:183], v232 offset:35840
	ds_read_b128 v[184:187], v232 offset:36864
	ds_read_b128 v[188:191], v232 offset:37888
	ds_read_b128 v[192:195], v232 offset:38912
	ds_read_b128 v[196:199], v232 offset:39936
	s_mov_b32 m0, s68
	s_add_i32 s10, s60, 0x100100
	buffer_load_dwordx4 v213, s[12:15], s10 offen lds
	s_add_i32 s10, s60, 0x180100
	s_mov_b32 m0, s69
	s_nop 0
	buffer_load_dwordx4 v213, s[12:15], s10 offen lds
	s_waitcnt vmcnt(10)
	s_waitcnt lgkmcnt(8)
	s_barrier
	s_setprio 1
	s_waitcnt lgkmcnt(7)
	v_mfma_f32_16x16x32_bf16 v[124:127], v[164:167], v[168:171], v[124:127]
	s_waitcnt lgkmcnt(6)
	v_mfma_f32_16x16x32_bf16 v[124:127], v[160:163], v[172:175], v[124:127]
	v_mfma_f32_16x16x32_bf16 v[120:123], v[156:159], v[168:171], v[120:123]
	s_nop 0
	v_mfma_f32_16x16x32_bf16 v[120:123], v[152:155], v[172:175], v[120:123]
	s_waitcnt lgkmcnt(5)
	v_mfma_f32_16x16x32_bf16 v[116:119], v[164:167], v[176:179], v[116:119]
	s_waitcnt lgkmcnt(4)
	v_mfma_f32_16x16x32_bf16 v[116:119], v[160:163], v[180:183], v[116:119]
	v_mfma_f32_16x16x32_bf16 v[112:115], v[156:159], v[176:179], v[112:115]
	s_nop 0
	v_mfma_f32_16x16x32_bf16 v[112:115], v[152:155], v[180:183], v[112:115]
	s_waitcnt lgkmcnt(3)
	v_mfma_f32_16x16x32_bf16 v[108:111], v[164:167], v[184:187], v[108:111]
	s_waitcnt lgkmcnt(2)
	v_mfma_f32_16x16x32_bf16 v[108:111], v[160:163], v[188:191], v[108:111]
	v_mfma_f32_16x16x32_bf16 v[104:107], v[156:159], v[184:187], v[104:107]
	s_nop 0
	v_mfma_f32_16x16x32_bf16 v[104:107], v[152:155], v[188:191], v[104:107]
	s_waitcnt lgkmcnt(1)
	v_mfma_f32_16x16x32_bf16 v[100:103], v[164:167], v[192:195], v[100:103]
	s_waitcnt lgkmcnt(0)
	v_mfma_f32_16x16x32_bf16 v[100:103], v[160:163], v[196:199], v[100:103]
	v_mfma_f32_16x16x32_bf16 v[96:99], v[156:159], v[192:195], v[96:99]
	s_nop 0
	v_mfma_f32_16x16x32_bf16 v[96:99], v[152:155], v[196:199], v[96:99]
	v_mfma_f32_16x16x32_bf16 v[92:95], v[148:151], v[168:171], v[92:95]
	s_nop 0
	v_mfma_f32_16x16x32_bf16 v[92:95], v[144:147], v[172:175], v[92:95]
	v_mfma_f32_16x16x32_bf16 v[88:91], v[140:143], v[168:171], v[88:91]
	s_nop 0
	v_mfma_f32_16x16x32_bf16 v[88:91], v[136:139], v[172:175], v[88:91]
	v_mfma_f32_16x16x32_bf16 v[84:87], v[148:151], v[176:179], v[84:87]
	s_nop 0
	v_mfma_f32_16x16x32_bf16 v[84:87], v[144:147], v[180:183], v[84:87]
	v_mfma_f32_16x16x32_bf16 v[80:83], v[140:143], v[176:179], v[80:83]
	s_nop 0
	v_mfma_f32_16x16x32_bf16 v[80:83], v[136:139], v[180:183], v[80:83]
	v_mfma_f32_16x16x32_bf16 v[76:79], v[148:151], v[184:187], v[76:79]
	s_nop 0
	v_mfma_f32_16x16x32_bf16 v[76:79], v[144:147], v[188:191], v[76:79]
	v_mfma_f32_16x16x32_bf16 v[72:75], v[140:143], v[184:187], v[72:75]
	s_nop 0
	v_mfma_f32_16x16x32_bf16 v[72:75], v[136:139], v[188:191], v[72:75]
	v_mfma_f32_16x16x32_bf16 v[68:71], v[148:151], v[192:195], v[68:71]
	s_nop 0
	v_mfma_f32_16x16x32_bf16 v[68:71], v[144:147], v[196:199], v[68:71]
	v_mfma_f32_16x16x32_bf16 v[64:67], v[140:143], v[192:195], v[64:67]
	s_nop 0
	v_mfma_f32_16x16x32_bf16 v[64:67], v[136:139], v[196:199], v[64:67]
	s_setprio 0
	s_barrier
	ds_read_b128 v[168:171], v232 offset:49152
	ds_read_b128 v[172:175], v232 offset:50176
	ds_read_b128 v[176:179], v232 offset:51200
	ds_read_b128 v[180:183], v232 offset:52224
	ds_read_b128 v[184:187], v232 offset:53248
	ds_read_b128 v[188:191], v232 offset:54272
	ds_read_b128 v[192:195], v232 offset:55296
	ds_read_b128 v[196:199], v232 offset:56320
	s_mov_b32 m0, s72
	s_mov_b32 s10, s14
	s_mov_b32 s11, s15
	buffer_load_dwordx4 v214, s[8:11], s5 offen lds
	s_add_i32 s5, s42, 0x40180
	s_mov_b32 m0, s73
	s_nop 0
	buffer_load_dwordx4 v214, s[8:11], s5 offen lds
	s_add_i32 s5, s42, 0x4180
	s_mov_b32 m0, s76
	s_nop 0
	buffer_load_dwordx4 v214, s[8:11], s5 offen lds
	s_add_i32 s5, s42, 0x44180
	s_mov_b32 m0, s77
	s_nop 0
	buffer_load_dwordx4 v214, s[8:11], s5 offen lds
	s_mov_b32 m0, s74
	s_nop 0
	buffer_load_dwordx4 v213, s[12:15], s4 offen lds
	s_add_i32 s4, s60, 0x80180
	s_mov_b32 m0, s75
	s_nop 0
	buffer_load_dwordx4 v213, s[12:15], s4 offen lds
	s_waitcnt vmcnt(8)
	s_waitcnt lgkmcnt(6)
	s_barrier
	s_setprio 1
	s_waitcnt lgkmcnt(7)
	v_mfma_f32_16x16x32_bf16 v[60:63], v[164:167], v[168:171], v[60:63]
	s_waitcnt lgkmcnt(6)
	v_mfma_f32_16x16x32_bf16 v[60:63], v[160:163], v[172:175], v[60:63]
	v_mfma_f32_16x16x32_bf16 v[56:59], v[156:159], v[168:171], v[56:59]
	s_nop 0
	v_mfma_f32_16x16x32_bf16 v[56:59], v[152:155], v[172:175], v[56:59]
	s_waitcnt lgkmcnt(5)
	v_mfma_f32_16x16x32_bf16 v[52:55], v[164:167], v[176:179], v[52:55]
	s_waitcnt lgkmcnt(4)
	v_mfma_f32_16x16x32_bf16 v[52:55], v[160:163], v[180:183], v[52:55]
	v_mfma_f32_16x16x32_bf16 v[48:51], v[156:159], v[176:179], v[48:51]
	s_nop 0
	v_mfma_f32_16x16x32_bf16 v[48:51], v[152:155], v[180:183], v[48:51]
	s_waitcnt lgkmcnt(3)
	v_mfma_f32_16x16x32_bf16 v[44:47], v[164:167], v[184:187], v[44:47]
	s_waitcnt lgkmcnt(2)
	v_mfma_f32_16x16x32_bf16 v[44:47], v[160:163], v[188:191], v[44:47]
	v_mfma_f32_16x16x32_bf16 v[40:43], v[156:159], v[184:187], v[40:43]
	s_nop 0
	v_mfma_f32_16x16x32_bf16 v[40:43], v[152:155], v[188:191], v[40:43]
	s_waitcnt lgkmcnt(1)
	v_mfma_f32_16x16x32_bf16 v[36:39], v[164:167], v[192:195], v[36:39]
	s_waitcnt lgkmcnt(0)
	v_mfma_f32_16x16x32_bf16 v[36:39], v[160:163], v[196:199], v[36:39]
	v_mfma_f32_16x16x32_bf16 v[32:35], v[156:159], v[192:195], v[32:35]
	s_nop 0
	v_mfma_f32_16x16x32_bf16 v[32:35], v[152:155], v[196:199], v[32:35]
	v_mfma_f32_16x16x32_bf16 v[28:31], v[148:151], v[168:171], v[28:31]
	s_nop 0
	v_mfma_f32_16x16x32_bf16 v[28:31], v[144:147], v[172:175], v[28:31]
	v_mfma_f32_16x16x32_bf16 v[24:27], v[140:143], v[168:171], v[24:27]
	s_nop 0
	v_mfma_f32_16x16x32_bf16 v[24:27], v[136:139], v[172:175], v[24:27]
	v_mfma_f32_16x16x32_bf16 v[20:23], v[148:151], v[176:179], v[20:23]
	s_nop 0
	v_mfma_f32_16x16x32_bf16 v[20:23], v[144:147], v[180:183], v[20:23]
	v_mfma_f32_16x16x32_bf16 v[16:19], v[140:143], v[176:179], v[16:19]
	s_nop 0
	v_mfma_f32_16x16x32_bf16 v[16:19], v[136:139], v[180:183], v[16:19]
	v_mfma_f32_16x16x32_bf16 v[12:15], v[148:151], v[184:187], v[12:15]
	s_nop 0
	v_mfma_f32_16x16x32_bf16 v[12:15], v[144:147], v[188:191], v[12:15]
	v_mfma_f32_16x16x32_bf16 v[8:11], v[140:143], v[184:187], v[8:11]
	s_nop 0
	v_mfma_f32_16x16x32_bf16 v[8:11], v[136:139], v[188:191], v[8:11]
	v_mfma_f32_16x16x32_bf16 v[4:7], v[148:151], v[192:195], v[4:7]
	s_nop 0
	v_mfma_f32_16x16x32_bf16 v[4:7], v[144:147], v[196:199], v[4:7]
	v_mfma_f32_16x16x32_bf16 v[0:3], v[140:143], v[192:195], v[0:3]
	s_nop 0
	v_mfma_f32_16x16x32_bf16 v[0:3], v[136:139], v[196:199], v[0:3]
	s_setprio 0
	s_barrier
	s_waitcnt vmcnt(14)
	v_mul_f32_e32 v132, 0x42800000, v132
	v_mul_f32_e32 v128, 0x42800000, v128
	v_mul_f32_e32 v133, 0x42800000, v133
	v_mul_f32_e32 v129, 0x42800000, v129
	v_mul_f32_e32 v134, 0x42800000, v134
	v_mul_f32_e32 v130, 0x42800000, v130
	v_mul_f32_e32 v135, 0x42800000, v135
	v_mul_f32_e32 v131, 0x42800000, v131
	v_cvt_pk_fp8_f32 v202, v128, v132
	v_cvt_pk_fp8_f32 v233, v129, v133
	v_cvt_pk_fp8_f32 v234, v130, v134
	v_cvt_pk_fp8_f32 v235, v131, v135
	s_add_i32 s33, s42, 0x200
	s_mov_b32 s66, 0
	s_mov_b32 s89, s70
	s_mov_b32 s90, s71
	s_branch .LBB0_595

.LBB0_595:
	v_mov_b32_e32 v152, v202
	v_mov_b32_e32 v153, v233
	v_mov_b32_e32 v154, v234
	v_mov_b32_e32 v155, v235
	ds_read_b128 v[158:161], v216
	ds_read_b128 v[162:165], v217
	ds_read_b128 v[166:169], v218
	ds_read_b128 v[170:173], v219
	ds_read_b128 v[148:151], v220
	ds_read_b128 v[144:147], v221
	ds_read_b128 v[140:143], v222
	ds_read_b128 v[136:139], v223
	ds_read_b128 v[174:177], v232
	ds_read_b128 v[178:181], v232 offset:1024
	ds_read_b128 v[182:185], v232 offset:2048
	ds_read_b128 v[186:189], v232 offset:3072
	ds_read_b128 v[190:193], v232 offset:4096
	ds_read_b128 v[194:197], v232 offset:5120
	ds_read_b128 v[234:237], v232 offset:6144
	ds_read_b128 v[238:241], v232 offset:7168
	s_add_i32 s4, s60, s66
	s_mov_b32 s42, s90
	s_add_i32 s90, s90, 1
	s_add_i32 s5, s4, 0x200
	s_add_i32 s67, s33, s66
	s_cmpk_eq_i32 s66, 0x200
	s_cselect_b32 s43, s87, s5
	s_cselect_b32 s93, s88, s67
	s_add_i32 s92, s43, 0x80
	s_mov_b32 m0, s78
	s_add_i32 s5, s4, 0x100180
	buffer_load_dwordx4 v213, s[12:15], s5 offen lds
	s_add_i32 s4, s4, 0x180180
	s_mov_b32 m0, s81
	s_add_i32 s94, s93, 0x80
	buffer_load_dwordx4 v213, s[12:15], s4 offen lds
	s_lshr_b32 s4, s90, 2
	s_mul_i32 s67, s4, s34
	s_add_i32 s67, s67, s2
	s_cmp_lt_i32 s4, s3
	s_cselect_b64 s[4:5], -1, 0
	s_and_b64 s[96:97], s[4:5], exec
	s_cselect_b32 s91, s67, 0
	s_ashr_i32 s96, s91, 7
	s_bfe_u32 s95, s90, 0x10001
	s_ashr_i32 s97, s96, 31
	s_or_b32 s95, s95, s79
	s_lshl_b64 s[96:97], s[96:97], 23
	s_add_u32 s96, s48, s96
	s_addc_u32 s97, s49, s97
	s_lshl_b32 vcc_lo, s91, 16
	s_and_b32 vcc_lo, vcc_lo, 0x600000
	s_add_u32 s96, s96, vcc_lo
	s_addc_u32 s97, s97, 0
	s_lshl_b32 s91, s91, 7
	s_and_b32 s91, s91, 0xf80
	s_lshl_b32 vcc_lo, s91, 2
	s_add_u32 s96, s96, vcc_lo
	v_and_or_b32 v202, s89, 2, v200
	s_addc_u32 s97, s97, 0
	v_lshl_or_b32 v156, s95, 5, v215
	v_lshlrev_b64 v[128:129], 14, v[202:203]
	v_lshl_add_u64 v[128:129], s[96:97], 0, v[128:129]
	v_lshlrev_b32_e32 v202, 2, v156
	v_lshl_add_u64 v[128:129], v[128:129], 0, v[202:203]
	s_movk_i32 s95, 0x4000
	v_add_co_u32_e32 v132, vcc, s95, v128
	s_nop 1
	v_addc_co_u32_e32 v133, vcc, 0, v129, vcc
	global_load_dwordx4 v[128:131], v[128:129], off nt
	s_nop 0
	global_load_dwordx4 v[132:135], v[132:133], off nt
	s_waitcnt vmcnt(10)
	s_waitcnt lgkmcnt(8)
	s_barrier
	s_setprio 1
	s_waitcnt lgkmcnt(7)
	v_mfma_f32_16x16x32_bf16 v[124:127], v[158:161], v[174:177], v[124:127]
	s_waitcnt lgkmcnt(6)
	v_mfma_f32_16x16x32_bf16 v[124:127], v[162:165], v[178:181], v[124:127]
	v_mfma_f32_16x16x32_bf16 v[120:123], v[166:169], v[174:177], v[120:123]
	s_nop 0
	v_mfma_f32_16x16x32_bf16 v[120:123], v[170:173], v[178:181], v[120:123]
	s_waitcnt lgkmcnt(5)
	v_mfma_f32_16x16x32_bf16 v[116:119], v[158:161], v[182:185], v[116:119]
	s_waitcnt lgkmcnt(4)
	v_mfma_f32_16x16x32_bf16 v[116:119], v[162:165], v[186:189], v[116:119]
	v_mfma_f32_16x16x32_bf16 v[112:115], v[166:169], v[182:185], v[112:115]
	s_nop 0
	v_mfma_f32_16x16x32_bf16 v[112:115], v[170:173], v[186:189], v[112:115]
	s_waitcnt lgkmcnt(3)
	v_mfma_f32_16x16x32_bf16 v[108:111], v[158:161], v[190:193], v[108:111]
	s_waitcnt lgkmcnt(2)
	v_mfma_f32_16x16x32_bf16 v[108:111], v[162:165], v[194:197], v[108:111]
	v_mfma_f32_16x16x32_bf16 v[104:107], v[166:169], v[190:193], v[104:107]
	s_nop 0
	v_mfma_f32_16x16x32_bf16 v[104:107], v[170:173], v[194:197], v[104:107]
	s_waitcnt lgkmcnt(1)
	v_mfma_f32_16x16x32_bf16 v[100:103], v[158:161], v[234:237], v[100:103]
	s_waitcnt lgkmcnt(0)
	v_mfma_f32_16x16x32_bf16 v[100:103], v[162:165], v[238:241], v[100:103]
	v_mfma_f32_16x16x32_bf16 v[96:99], v[166:169], v[234:237], v[96:99]
	s_nop 0
	v_mfma_f32_16x16x32_bf16 v[96:99], v[170:173], v[238:241], v[96:99]
	v_mfma_f32_16x16x32_bf16 v[92:95], v[148:151], v[174:177], v[92:95]
	s_nop 0
	v_mfma_f32_16x16x32_bf16 v[92:95], v[144:147], v[178:181], v[92:95]
	v_mfma_f32_16x16x32_bf16 v[88:91], v[140:143], v[174:177], v[88:91]
	s_nop 0
	v_mfma_f32_16x16x32_bf16 v[88:91], v[136:139], v[178:181], v[88:91]
	v_mfma_f32_16x16x32_bf16 v[84:87], v[148:151], v[182:185], v[84:87]
	s_nop 0
	v_mfma_f32_16x16x32_bf16 v[84:87], v[144:147], v[186:189], v[84:87]
	v_mfma_f32_16x16x32_bf16 v[80:83], v[140:143], v[182:185], v[80:83]
	s_nop 0
	v_mfma_f32_16x16x32_bf16 v[80:83], v[136:139], v[186:189], v[80:83]
	v_mfma_f32_16x16x32_bf16 v[76:79], v[148:151], v[190:193], v[76:79]
	s_nop 0
	v_mfma_f32_16x16x32_bf16 v[76:79], v[144:147], v[194:197], v[76:79]
	v_mfma_f32_16x16x32_bf16 v[72:75], v[140:143], v[190:193], v[72:75]
	s_nop 0
	v_mfma_f32_16x16x32_bf16 v[72:75], v[136:139], v[194:197], v[72:75]
	v_mfma_f32_16x16x32_bf16 v[68:71], v[148:151], v[234:237], v[68:71]
	s_nop 0
	v_mfma_f32_16x16x32_bf16 v[68:71], v[144:147], v[238:241], v[68:71]
	v_mfma_f32_16x16x32_bf16 v[64:67], v[140:143], v[234:237], v[64:67]
	s_nop 0
	v_mfma_f32_16x16x32_bf16 v[64:67], v[136:139], v[238:241], v[64:67]
	s_setprio 0
	s_barrier
	ds_read_b128 v[174:177], v232 offset:16384
	ds_read_b128 v[178:181], v232 offset:17408
	ds_read_b128 v[182:185], v232 offset:18432
	ds_read_b128 v[186:189], v232 offset:19456
	ds_read_b128 v[190:193], v232 offset:20480
	ds_read_b128 v[194:197], v232 offset:21504
	ds_read_b128 v[234:237], v232 offset:22528
	ds_read_b128 v[238:241], v232 offset:23552
	s_mov_b32 m0, s47
	s_add_i32 s95, s93, 0x40000
	buffer_load_dwordx4 v214, s[8:11], s93 offen lds
	s_mov_b32 m0, s62
	s_nop 0
	buffer_load_dwordx4 v214, s[8:11], s95 offen lds
	s_add_i32 s95, s93, 0x4000
	s_mov_b32 m0, s63
	s_nop 0
	buffer_load_dwordx4 v214, s[8:11], s95 offen lds
	s_add_i32 s95, s93, 0x44000
	s_mov_b32 m0, s64
	s_nop 0
	buffer_load_dwordx4 v214, s[8:11], s95 offen lds
	s_mov_b32 m0, s46
	s_add_i32 s95, s43, 0x80000
	buffer_load_dwordx4 v213, s[12:15], s43 offen lds
	s_mov_b32 m0, s65
	s_nop 0
	buffer_load_dwordx4 v213, s[12:15], s95 offen lds
	s_waitcnt vmcnt(10)
	s_waitcnt lgkmcnt(6)
	s_barrier
	s_setprio 1
	s_waitcnt lgkmcnt(7)
	v_mfma_f32_16x16x32_bf16 v[60:63], v[158:161], v[174:177], v[60:63]
	s_waitcnt lgkmcnt(6)
	v_mfma_f32_16x16x32_bf16 v[60:63], v[162:165], v[178:181], v[60:63]
	v_mfma_f32_16x16x32_bf16 v[56:59], v[166:169], v[174:177], v[56:59]
	s_nop 0
	v_mfma_f32_16x16x32_bf16 v[56:59], v[170:173], v[178:181], v[56:59]
	s_waitcnt lgkmcnt(5)
	v_mfma_f32_16x16x32_bf16 v[52:55], v[158:161], v[182:185], v[52:55]
	s_waitcnt lgkmcnt(4)
	v_mfma_f32_16x16x32_bf16 v[52:55], v[162:165], v[186:189], v[52:55]
	v_mfma_f32_16x16x32_bf16 v[48:51], v[166:169], v[182:185], v[48:51]
	s_nop 0
	v_mfma_f32_16x16x32_bf16 v[48:51], v[170:173], v[186:189], v[48:51]
	s_waitcnt lgkmcnt(3)
	v_mfma_f32_16x16x32_bf16 v[44:47], v[158:161], v[190:193], v[44:47]
	s_waitcnt lgkmcnt(2)
	v_mfma_f32_16x16x32_bf16 v[44:47], v[162:165], v[194:197], v[44:47]
	v_mfma_f32_16x16x32_bf16 v[40:43], v[166:169], v[190:193], v[40:43]
	s_nop 0
	v_mfma_f32_16x16x32_bf16 v[40:43], v[170:173], v[194:197], v[40:43]
	s_waitcnt lgkmcnt(1)
	v_mfma_f32_16x16x32_bf16 v[36:39], v[158:161], v[234:237], v[36:39]
	s_waitcnt lgkmcnt(0)
	v_mfma_f32_16x16x32_bf16 v[36:39], v[162:165], v[238:241], v[36:39]
	v_mfma_f32_16x16x32_bf16 v[32:35], v[166:169], v[234:237], v[32:35]
	s_nop 0
	v_mfma_f32_16x16x32_bf16 v[32:35], v[170:173], v[238:241], v[32:35]
	v_mfma_f32_16x16x32_bf16 v[28:31], v[148:151], v[174:177], v[28:31]
	s_nop 0
	v_mfma_f32_16x16x32_bf16 v[28:31], v[144:147], v[178:181], v[28:31]
	v_mfma_f32_16x16x32_bf16 v[24:27], v[140:143], v[174:177], v[24:27]
	s_nop 0
	v_mfma_f32_16x16x32_bf16 v[24:27], v[136:139], v[178:181], v[24:27]
	v_mfma_f32_16x16x32_bf16 v[20:23], v[148:151], v[182:185], v[20:23]
	s_nop 0
	v_mfma_f32_16x16x32_bf16 v[20:23], v[144:147], v[186:189], v[20:23]
	v_mfma_f32_16x16x32_bf16 v[16:19], v[140:143], v[182:185], v[16:19]
	s_nop 0
	v_mfma_f32_16x16x32_bf16 v[16:19], v[136:139], v[186:189], v[16:19]
	v_mfma_f32_16x16x32_bf16 v[12:15], v[148:151], v[190:193], v[12:15]
	s_nop 0
	v_mfma_f32_16x16x32_bf16 v[12:15], v[144:147], v[194:197], v[12:15]
	v_mfma_f32_16x16x32_bf16 v[8:11], v[140:143], v[190:193], v[8:11]
	s_nop 0
	v_mfma_f32_16x16x32_bf16 v[8:11], v[136:139], v[194:197], v[8:11]
	v_mfma_f32_16x16x32_bf16 v[4:7], v[148:151], v[234:237], v[4:7]
	s_nop 0
	v_mfma_f32_16x16x32_bf16 v[4:7], v[144:147], v[238:241], v[4:7]
	v_mfma_f32_16x16x32_bf16 v[0:3], v[140:143], v[234:237], v[0:3]
	s_nop 0
	v_mfma_f32_16x16x32_bf16 v[0:3], v[136:139], v[238:241], v[0:3]
	s_setprio 0
	s_barrier
	ds_read_b128 v[136:139], v224
	ds_read_b128 v[140:143], v225
	ds_read_b128 v[144:147], v226
	ds_read_b128 v[148:151], v227
	ds_read_b128 v[158:161], v228
	ds_read_b128 v[162:165], v229
	ds_read_b128 v[166:169], v230
	ds_read_b128 v[170:173], v231
	ds_read_b128 v[174:177], v232 offset:32768
	ds_read_b128 v[178:181], v232 offset:33792
	ds_read_b128 v[182:185], v232 offset:34816
	ds_read_b128 v[186:189], v232 offset:35840
	ds_read_b128 v[190:193], v232 offset:36864
	ds_read_b128 v[194:197], v232 offset:37888
	ds_read_b128 v[234:237], v232 offset:38912
	ds_read_b128 v[238:241], v232 offset:39936
	s_mov_b32 m0, s68
	s_add_i32 s95, s43, 0x100000
	buffer_load_dwordx4 v213, s[12:15], s95 offen lds
	s_add_i32 s95, s43, 0x180000
	s_mov_b32 m0, s69
	s_nop 0
	buffer_load_dwordx4 v213, s[12:15], s95 offen lds
	s_waitcnt vmcnt(10)
	s_waitcnt lgkmcnt(8)
	s_barrier
	s_setprio 1
	s_waitcnt lgkmcnt(7)
	v_mfma_f32_16x16x32_bf16 v[124:127], v[136:139], v[174:177], v[124:127]
	s_waitcnt lgkmcnt(6)
	v_mfma_f32_16x16x32_bf16 v[124:127], v[140:143], v[178:181], v[124:127]
	v_mfma_f32_16x16x32_bf16 v[120:123], v[144:147], v[174:177], v[120:123]
	s_nop 0
	v_mfma_f32_16x16x32_bf16 v[120:123], v[148:151], v[178:181], v[120:123]
	s_waitcnt lgkmcnt(5)
	v_mfma_f32_16x16x32_bf16 v[116:119], v[136:139], v[182:185], v[116:119]
	s_waitcnt lgkmcnt(4)
	v_mfma_f32_16x16x32_bf16 v[116:119], v[140:143], v[186:189], v[116:119]
	v_mfma_f32_16x16x32_bf16 v[112:115], v[144:147], v[182:185], v[112:115]
	s_nop 0
	v_mfma_f32_16x16x32_bf16 v[112:115], v[148:151], v[186:189], v[112:115]
	s_waitcnt lgkmcnt(3)
	v_mfma_f32_16x16x32_bf16 v[108:111], v[136:139], v[190:193], v[108:111]
	s_waitcnt lgkmcnt(2)
	v_mfma_f32_16x16x32_bf16 v[108:111], v[140:143], v[194:197], v[108:111]
	v_mfma_f32_16x16x32_bf16 v[104:107], v[144:147], v[190:193], v[104:107]
	s_nop 0
	v_mfma_f32_16x16x32_bf16 v[104:107], v[148:151], v[194:197], v[104:107]
	s_waitcnt lgkmcnt(1)
	v_mfma_f32_16x16x32_bf16 v[100:103], v[136:139], v[234:237], v[100:103]
	s_waitcnt lgkmcnt(0)
	v_mfma_f32_16x16x32_bf16 v[100:103], v[140:143], v[238:241], v[100:103]
	v_mfma_f32_16x16x32_bf16 v[96:99], v[144:147], v[234:237], v[96:99]
	s_nop 0
	v_mfma_f32_16x16x32_bf16 v[96:99], v[148:151], v[238:241], v[96:99]
	v_mfma_f32_16x16x32_bf16 v[92:95], v[158:161], v[174:177], v[92:95]
	s_nop 0
	v_mfma_f32_16x16x32_bf16 v[92:95], v[162:165], v[178:181], v[92:95]
	v_mfma_f32_16x16x32_bf16 v[88:91], v[166:169], v[174:177], v[88:91]
	s_nop 0
	v_mfma_f32_16x16x32_bf16 v[88:91], v[170:173], v[178:181], v[88:91]
	v_mfma_f32_16x16x32_bf16 v[84:87], v[158:161], v[182:185], v[84:87]
	s_nop 0
	v_mfma_f32_16x16x32_bf16 v[84:87], v[162:165], v[186:189], v[84:87]
	v_mfma_f32_16x16x32_bf16 v[80:83], v[166:169], v[182:185], v[80:83]
	s_nop 0
	v_mfma_f32_16x16x32_bf16 v[80:83], v[170:173], v[186:189], v[80:83]
	v_mfma_f32_16x16x32_bf16 v[76:79], v[158:161], v[190:193], v[76:79]
	s_nop 0
	v_mfma_f32_16x16x32_bf16 v[76:79], v[162:165], v[194:197], v[76:79]
	v_mfma_f32_16x16x32_bf16 v[72:75], v[166:169], v[190:193], v[72:75]
	s_nop 0
	v_mfma_f32_16x16x32_bf16 v[72:75], v[170:173], v[194:197], v[72:75]
	v_mfma_f32_16x16x32_bf16 v[68:71], v[158:161], v[234:237], v[68:71]
	s_nop 0
	v_mfma_f32_16x16x32_bf16 v[68:71], v[162:165], v[238:241], v[68:71]
	v_mfma_f32_16x16x32_bf16 v[64:67], v[166:169], v[234:237], v[64:67]
	s_nop 0
	v_mfma_f32_16x16x32_bf16 v[64:67], v[170:173], v[238:241], v[64:67]
	s_setprio 0
	s_barrier
	ds_read_b128 v[174:177], v232 offset:49152
	ds_read_b128 v[178:181], v232 offset:50176
	ds_read_b128 v[182:185], v232 offset:51200
	ds_read_b128 v[186:189], v232 offset:52224
	ds_read_b128 v[190:193], v232 offset:53248
	ds_read_b128 v[194:197], v232 offset:54272
	ds_read_b128 v[234:237], v232 offset:55296
	ds_read_b128 v[238:241], v232 offset:56320
	s_mov_b32 m0, s72
	s_add_i32 s43, s43, 0x80080
	buffer_load_dwordx4 v214, s[8:11], s94 offen lds
	s_add_i32 s94, s93, 0x40080
	s_mov_b32 m0, s73
	s_nop 0
	buffer_load_dwordx4 v214, s[8:11], s94 offen lds
	s_add_i32 s94, s93, 0x4080
	s_mov_b32 m0, s76
	s_add_i32 s93, s93, 0x44080
	buffer_load_dwordx4 v214, s[8:11], s94 offen lds
	s_mov_b32 m0, s77
	s_nop 0
	buffer_load_dwordx4 v214, s[8:11], s93 offen lds
	s_mov_b32 m0, s74
	s_nop 0
	buffer_load_dwordx4 v213, s[12:15], s92 offen lds
	s_mov_b32 m0, s75
	s_nop 0
	buffer_load_dwordx4 v213, s[12:15], s43 offen lds
	s_waitcnt vmcnt(8)
	s_waitcnt lgkmcnt(6)
	s_barrier
	s_setprio 1
	s_waitcnt lgkmcnt(7)
	v_mfma_f32_16x16x32_bf16 v[60:63], v[136:139], v[174:177], v[60:63]
	s_waitcnt lgkmcnt(6)
	v_mfma_f32_16x16x32_bf16 v[60:63], v[140:143], v[178:181], v[60:63]
	v_mfma_f32_16x16x32_bf16 v[56:59], v[144:147], v[174:177], v[56:59]
	s_nop 0
	v_mfma_f32_16x16x32_bf16 v[56:59], v[148:151], v[178:181], v[56:59]
	s_waitcnt lgkmcnt(5)
	v_mfma_f32_16x16x32_bf16 v[52:55], v[136:139], v[182:185], v[52:55]
	s_waitcnt lgkmcnt(4)
	v_mfma_f32_16x16x32_bf16 v[52:55], v[140:143], v[186:189], v[52:55]
	v_mfma_f32_16x16x32_bf16 v[48:51], v[144:147], v[182:185], v[48:51]
	s_nop 0
	v_mfma_f32_16x16x32_bf16 v[48:51], v[148:151], v[186:189], v[48:51]
	s_waitcnt lgkmcnt(3)
	v_mfma_f32_16x16x32_bf16 v[44:47], v[136:139], v[190:193], v[44:47]
	s_waitcnt lgkmcnt(2)
	v_mfma_f32_16x16x32_bf16 v[44:47], v[140:143], v[194:197], v[44:47]
	v_mfma_f32_16x16x32_bf16 v[40:43], v[144:147], v[190:193], v[40:43]
	s_nop 0
	v_mfma_f32_16x16x32_bf16 v[40:43], v[148:151], v[194:197], v[40:43]
	s_waitcnt lgkmcnt(1)
	v_mfma_f32_16x16x32_bf16 v[36:39], v[136:139], v[234:237], v[36:39]
	s_waitcnt lgkmcnt(0)
	v_mfma_f32_16x16x32_bf16 v[36:39], v[140:143], v[238:241], v[36:39]
	v_mfma_f32_16x16x32_bf16 v[32:35], v[144:147], v[234:237], v[32:35]
	s_nop 0
	v_mfma_f32_16x16x32_bf16 v[32:35], v[148:151], v[238:241], v[32:35]
	v_mfma_f32_16x16x32_bf16 v[28:31], v[158:161], v[174:177], v[28:31]
	s_nop 0
	v_mfma_f32_16x16x32_bf16 v[28:31], v[162:165], v[178:181], v[28:31]
	v_mfma_f32_16x16x32_bf16 v[24:27], v[166:169], v[174:177], v[24:27]
	s_nop 0
	v_mfma_f32_16x16x32_bf16 v[24:27], v[170:173], v[178:181], v[24:27]
	v_mfma_f32_16x16x32_bf16 v[20:23], v[158:161], v[182:185], v[20:23]
	s_nop 0
	v_mfma_f32_16x16x32_bf16 v[20:23], v[162:165], v[186:189], v[20:23]
	v_mfma_f32_16x16x32_bf16 v[16:19], v[166:169], v[182:185], v[16:19]
	s_nop 0
	v_mfma_f32_16x16x32_bf16 v[16:19], v[170:173], v[186:189], v[16:19]
	v_mfma_f32_16x16x32_bf16 v[12:15], v[158:161], v[190:193], v[12:15]
	s_nop 0
	v_mfma_f32_16x16x32_bf16 v[12:15], v[162:165], v[194:197], v[12:15]
	v_mfma_f32_16x16x32_bf16 v[8:11], v[166:169], v[190:193], v[8:11]
	s_nop 0
	v_mfma_f32_16x16x32_bf16 v[8:11], v[170:173], v[194:197], v[8:11]
	v_mfma_f32_16x16x32_bf16 v[4:7], v[158:161], v[234:237], v[4:7]
	s_nop 0
	v_mfma_f32_16x16x32_bf16 v[4:7], v[162:165], v[238:241], v[4:7]
	v_mfma_f32_16x16x32_bf16 v[0:3], v[166:169], v[234:237], v[0:3]
	s_nop 0
	v_mfma_f32_16x16x32_bf16 v[0:3], v[170:173], v[238:241], v[0:3]
	s_setprio 0
	s_barrier
	s_bitcmp0_b32 s42, 0
	s_waitcnt vmcnt(15)
	v_mul_f32_e32 v128, 0x42800000, v128
	s_waitcnt vmcnt(14)
	v_mul_f32_e32 v132, 0x42800000, v132
	v_mul_f32_e32 v129, 0x42800000, v129
	v_mul_f32_e32 v133, 0x42800000, v133
	v_mul_f32_e32 v130, 0x42800000, v130
	v_mul_f32_e32 v134, 0x42800000, v134
	v_mul_f32_e32 v131, 0x42800000, v131
	v_mul_f32_e32 v135, 0x42800000, v135
	s_mov_b64 s[42:43], -1
	s_cbranch_scc0 .LBB0_598
	s_andn2_b64 vcc, exec, s[42:43]
	s_cbranch_vccnz .LBB0_594
	s_branch .LBB0_599

.LBB0_920:
	s_add_i32 s3, s94, 0x100
	s_add_i32 s16, s36, 0x100
	s_waitcnt lgkmcnt(4)
	s_barrier
	s_setprio 1
	v_mfma_scale_f32_16x16x128_f8f6f4 v[188:191], v[24:31], v[56:63], 0, v213, v213 op_sel_hi:[0,0,0]
	v_mfma_scale_f32_16x16x128_f8f6f4 v[184:187], v[16:23], v[56:63], 0, v213, v213 op_sel_hi:[0,0,0]
	v_mfma_scale_f32_16x16x128_f8f6f4 v[180:183], v[24:31], v[48:55], 0, v213, v213 op_sel_hi:[0,0,0]
	v_mfma_scale_f32_16x16x128_f8f6f4 v[176:179], v[16:23], v[48:55], 0, v213, v213 op_sel_hi:[0,0,0]
	v_mfma_scale_f32_16x16x128_f8f6f4 v[172:175], v[24:31], v[40:47], 0, v213, v213 op_sel_hi:[0,0,0]
	v_mfma_scale_f32_16x16x128_f8f6f4 v[168:171], v[16:23], v[40:47], 0, v213, v213 op_sel_hi:[0,0,0]
	v_mfma_scale_f32_16x16x128_f8f6f4 v[164:167], v[24:31], v[32:39], 0, v213, v213 op_sel_hi:[0,0,0]
	v_mfma_scale_f32_16x16x128_f8f6f4 v[160:163], v[16:23], v[32:39], 0, v213, v213 op_sel_hi:[0,0,0]
	s_waitcnt lgkmcnt(2)
	v_mfma_scale_f32_16x16x128_f8f6f4 v[156:159], v[8:15], v[56:63], 0, v213, v213 op_sel_hi:[0,0,0]
	s_waitcnt lgkmcnt(0)
	v_mfma_scale_f32_16x16x128_f8f6f4 v[152:155], v[0:7], v[56:63], 0, v213, v213 op_sel_hi:[0,0,0]
	v_mfma_scale_f32_16x16x128_f8f6f4 v[148:151], v[8:15], v[48:55], 0, v213, v213 op_sel_hi:[0,0,0]
	v_mfma_scale_f32_16x16x128_f8f6f4 v[144:147], v[0:7], v[48:55], 0, v213, v213 op_sel_hi:[0,0,0]
	v_mfma_scale_f32_16x16x128_f8f6f4 v[140:143], v[8:15], v[40:47], 0, v213, v213 op_sel_hi:[0,0,0]
	v_mfma_scale_f32_16x16x128_f8f6f4 v[136:139], v[0:7], v[40:47], 0, v213, v213 op_sel_hi:[0,0,0]
	v_mfma_scale_f32_16x16x128_f8f6f4 v[132:135], v[8:15], v[32:39], 0, v213, v213 op_sel_hi:[0,0,0]
	v_mfma_scale_f32_16x16x128_f8f6f4 v[128:131], v[0:7], v[32:39], 0, v213, v213 op_sel_hi:[0,0,0]
	s_setprio 0
	s_barrier
	s_mov_b32 m0, s71
	s_mov_b32 s10, s14
	s_mov_b32 s11, s15
	ds_read_b128 v[56:59], v216 offset:0x4000
	ds_read_b128 v[60:63], v216 offset:0x4400
	ds_read_b128 v[48:51], v216 offset:0x4800
	ds_read_b128 v[52:55], v216 offset:0x4c00
	ds_read_b128 v[40:43], v216 offset:0x5000
	ds_read_b128 v[44:47], v216 offset:0x5400
	ds_read_b128 v[32:35], v216 offset:0x5800
	ds_read_b128 v[36:39], v216 offset:0x5c00
	buffer_load_dwordx4 v215, s[8:11], s16 offen lds
	s_add_i32 s16, s36, 0x80100
	s_mov_b32 m0, s72
	s_and_b64 vcc, exec, s[4:5]
	buffer_load_dwordx4 v215, s[8:11], s16 offen lds
	s_add_i32 s16, s36, 0x8100
	s_mov_b32 m0, s73
	s_nop 0
	buffer_load_dwordx4 v215, s[8:11], s16 offen lds
	s_add_i32 s16, s36, 0x88100
	s_mov_b32 m0, s74
	s_nop 0
	buffer_load_dwordx4 v215, s[8:11], s16 offen lds
	s_mov_b32 m0, s70
	s_nop 0
	buffer_load_dwordx4 v214, s[12:15], s3 offen lds
	s_add_i32 s3, s94, 0x40100
	s_mov_b32 m0, s75
	s_nop 0
	buffer_load_dwordx4 v214, s[12:15], s3 offen lds
	s_cbranch_vccz .LBB0_938
	s_waitcnt vmcnt(54)
	s_cbranch_execnz .LBB0_923

.LBB0_923:
	s_add_i32 s3, s94, 0x180
	s_add_i32 s4, s36, 0x180
	s_waitcnt lgkmcnt(0)
	s_barrier
	s_setprio 1
	v_mfma_scale_f32_16x16x128_f8f6f4 v[124:127], v[24:31], v[56:63], 0, v213, v213 op_sel_hi:[0,0,0]
	v_mfma_scale_f32_16x16x128_f8f6f4 v[120:123], v[16:23], v[56:63], 0, v213, v213 op_sel_hi:[0,0,0]
	v_mfma_scale_f32_16x16x128_f8f6f4 v[116:119], v[24:31], v[48:55], 0, v213, v213 op_sel_hi:[0,0,0]
	v_mfma_scale_f32_16x16x128_f8f6f4 v[112:115], v[16:23], v[48:55], 0, v213, v213 op_sel_hi:[0,0,0]
	v_mfma_scale_f32_16x16x128_f8f6f4 v[108:111], v[24:31], v[40:47], 0, v213, v213 op_sel_hi:[0,0,0]
	v_mfma_scale_f32_16x16x128_f8f6f4 v[104:107], v[16:23], v[40:47], 0, v213, v213 op_sel_hi:[0,0,0]
	v_mfma_scale_f32_16x16x128_f8f6f4 v[100:103], v[24:31], v[32:39], 0, v213, v213 op_sel_hi:[0,0,0]
	v_mfma_scale_f32_16x16x128_f8f6f4 v[96:99], v[16:23], v[32:39], 0, v213, v213 op_sel_hi:[0,0,0]
	v_mfma_scale_f32_16x16x128_f8f6f4 v[92:95], v[8:15], v[56:63], 0, v213, v213 op_sel_hi:[0,0,0]
	v_mfma_scale_f32_16x16x128_f8f6f4 v[88:91], v[0:7], v[56:63], 0, v213, v213 op_sel_hi:[0,0,0]
	v_mfma_scale_f32_16x16x128_f8f6f4 v[84:87], v[8:15], v[48:55], 0, v213, v213 op_sel_hi:[0,0,0]
	v_mfma_scale_f32_16x16x128_f8f6f4 v[80:83], v[0:7], v[48:55], 0, v213, v213 op_sel_hi:[0,0,0]
	v_mfma_scale_f32_16x16x128_f8f6f4 v[76:79], v[8:15], v[40:47], 0, v213, v213 op_sel_hi:[0,0,0]
	v_mfma_scale_f32_16x16x128_f8f6f4 v[72:75], v[0:7], v[40:47], 0, v213, v213 op_sel_hi:[0,0,0]
	v_mfma_scale_f32_16x16x128_f8f6f4 v[68:71], v[8:15], v[32:39], 0, v213, v213 op_sel_hi:[0,0,0]
	v_mfma_scale_f32_16x16x128_f8f6f4 v[64:67], v[0:7], v[32:39], 0, v213, v213 op_sel_hi:[0,0,0]
	s_setprio 0
	s_barrier
	ds_read_b128 v[24:27], v217 offset:0x8000
	ds_read_b128 v[28:31], v217 offset:0x8400
	ds_read_b128 v[16:19], v217 offset:0x8800
	ds_read_b128 v[20:23], v217 offset:0x8c00
	ds_read_b128 v[32:35], v216 offset:0x8000
	ds_read_b128 v[36:39], v216 offset:0x8400
	ds_read_b128 v[40:43], v216 offset:0x8800
	ds_read_b128 v[44:47], v216 offset:0x8c00
	ds_read_b128 v[48:51], v216 offset:0x9000
	ds_read_b128 v[52:55], v216 offset:0x9400
	ds_read_b128 v[56:59], v216 offset:0x9800
	ds_read_b128 v[60:63], v216 offset:0x9c00
	ds_read_b128 v[8:11], v217 offset:0xc000
	ds_read_b128 v[12:15], v217 offset:0xc400
	ds_read_b128 v[0:3], v217 offset:0xc800
	ds_read_b128 v[4:7], v217 offset:0xcc00
	s_mov_b32 m0, s76
	s_add_i32 s5, s94, 0x80100
	buffer_load_dwordx4 v214, s[12:15], s5 offen lds
	s_add_i32 s5, s94, 0xc0100
	s_mov_b32 m0, s77
	s_nop 0
	buffer_load_dwordx4 v214, s[12:15], s5 offen lds
	s_waitcnt vmcnt(10)
	s_waitcnt lgkmcnt(4)
	s_barrier
	s_setprio 1
	v_mfma_scale_f32_16x16x128_f8f6f4 v[188:191], v[24:31], v[32:39], v[188:191], v213, v213 op_sel_hi:[0,0,0]
	v_mfma_scale_f32_16x16x128_f8f6f4 v[184:187], v[16:23], v[32:39], v[184:187], v213, v213 op_sel_hi:[0,0,0]
	v_mfma_scale_f32_16x16x128_f8f6f4 v[180:183], v[24:31], v[40:47], v[180:183], v213, v213 op_sel_hi:[0,0,0]
	v_mfma_scale_f32_16x16x128_f8f6f4 v[176:179], v[16:23], v[40:47], v[176:179], v213, v213 op_sel_hi:[0,0,0]
	v_mfma_scale_f32_16x16x128_f8f6f4 v[172:175], v[24:31], v[48:55], v[172:175], v213, v213 op_sel_hi:[0,0,0]
	v_mfma_scale_f32_16x16x128_f8f6f4 v[168:171], v[16:23], v[48:55], v[168:171], v213, v213 op_sel_hi:[0,0,0]
	v_mfma_scale_f32_16x16x128_f8f6f4 v[164:167], v[24:31], v[56:63], v[164:167], v213, v213 op_sel_hi:[0,0,0]
	v_mfma_scale_f32_16x16x128_f8f6f4 v[160:163], v[16:23], v[56:63], v[160:163], v213, v213 op_sel_hi:[0,0,0]
	s_waitcnt lgkmcnt(2)
	v_mfma_scale_f32_16x16x128_f8f6f4 v[156:159], v[8:15], v[32:39], v[156:159], v213, v213 op_sel_hi:[0,0,0]
	s_waitcnt lgkmcnt(0)
	v_mfma_scale_f32_16x16x128_f8f6f4 v[152:155], v[0:7], v[32:39], v[152:155], v213, v213 op_sel_hi:[0,0,0]
	v_mfma_scale_f32_16x16x128_f8f6f4 v[148:151], v[8:15], v[40:47], v[148:151], v213, v213 op_sel_hi:[0,0,0]
	v_mfma_scale_f32_16x16x128_f8f6f4 v[144:147], v[0:7], v[40:47], v[144:147], v213, v213 op_sel_hi:[0,0,0]
	v_mfma_scale_f32_16x16x128_f8f6f4 v[140:143], v[8:15], v[48:55], v[140:143], v213, v213 op_sel_hi:[0,0,0]
	v_mfma_scale_f32_16x16x128_f8f6f4 v[136:139], v[0:7], v[48:55], v[136:139], v213, v213 op_sel_hi:[0,0,0]
	v_mfma_scale_f32_16x16x128_f8f6f4 v[132:135], v[8:15], v[56:63], v[132:135], v213, v213 op_sel_hi:[0,0,0]
	v_mfma_scale_f32_16x16x128_f8f6f4 v[128:131], v[0:7], v[56:63], v[128:131], v213, v213 op_sel_hi:[0,0,0]
	s_setprio 0
	s_barrier
	ds_read_b128 v[32:35], v216 offset:0xc000
	ds_read_b128 v[36:39], v216 offset:0xc400
	ds_read_b128 v[40:43], v216 offset:0xc800
	ds_read_b128 v[44:47], v216 offset:0xcc00
	ds_read_b128 v[48:51], v216 offset:0xd000
	ds_read_b128 v[52:55], v216 offset:0xd400
	ds_read_b128 v[56:59], v216 offset:0xd800
	ds_read_b128 v[60:63], v216 offset:0xdc00
	s_mov_b32 m0, s80
	s_mov_b32 s10, s14
	s_mov_b32 s11, s15
	buffer_load_dwordx4 v215, s[8:11], s4 offen lds
	s_add_i32 s4, s36, 0x80180
	s_mov_b32 m0, s81
	s_nop 0
	buffer_load_dwordx4 v215, s[8:11], s4 offen lds
	s_add_i32 s4, s36, 0x8180
	s_mov_b32 m0, s84
	s_nop 0
	buffer_load_dwordx4 v215, s[8:11], s4 offen lds
	s_add_i32 s4, s36, 0x88180
	s_mov_b32 m0, s85
	s_nop 0
	buffer_load_dwordx4 v215, s[8:11], s4 offen lds
	s_mov_b32 m0, s82
	s_nop 0
	buffer_load_dwordx4 v214, s[12:15], s3 offen lds
	s_add_i32 s3, s94, 0x40180
	s_mov_b32 m0, s83
	s_nop 0
	buffer_load_dwordx4 v214, s[12:15], s3 offen lds
	s_waitcnt vmcnt(8)
	s_waitcnt lgkmcnt(0)
	s_barrier
	s_setprio 1
	v_mfma_scale_f32_16x16x128_f8f6f4 v[124:127], v[24:31], v[32:39], v[124:127], v213, v213 op_sel_hi:[0,0,0]
	v_mfma_scale_f32_16x16x128_f8f6f4 v[120:123], v[16:23], v[32:39], v[120:123], v213, v213 op_sel_hi:[0,0,0]
	v_mfma_scale_f32_16x16x128_f8f6f4 v[116:119], v[24:31], v[40:47], v[116:119], v213, v213 op_sel_hi:[0,0,0]
	v_mfma_scale_f32_16x16x128_f8f6f4 v[112:115], v[16:23], v[40:47], v[112:115], v213, v213 op_sel_hi:[0,0,0]
	v_mfma_scale_f32_16x16x128_f8f6f4 v[108:111], v[24:31], v[48:55], v[108:111], v213, v213 op_sel_hi:[0,0,0]
	v_mfma_scale_f32_16x16x128_f8f6f4 v[104:107], v[16:23], v[48:55], v[104:107], v213, v213 op_sel_hi:[0,0,0]
	v_mfma_scale_f32_16x16x128_f8f6f4 v[100:103], v[24:31], v[56:63], v[100:103], v213, v213 op_sel_hi:[0,0,0]
	v_mfma_scale_f32_16x16x128_f8f6f4 v[96:99], v[16:23], v[56:63], v[96:99], v213, v213 op_sel_hi:[0,0,0]
	v_mfma_scale_f32_16x16x128_f8f6f4 v[92:95], v[8:15], v[32:39], v[92:95], v213, v213 op_sel_hi:[0,0,0]
	v_mfma_scale_f32_16x16x128_f8f6f4 v[88:91], v[0:7], v[32:39], v[88:91], v213, v213 op_sel_hi:[0,0,0]
	v_mfma_scale_f32_16x16x128_f8f6f4 v[84:87], v[8:15], v[40:47], v[84:87], v213, v213 op_sel_hi:[0,0,0]
	v_mfma_scale_f32_16x16x128_f8f6f4 v[80:83], v[0:7], v[40:47], v[80:83], v213, v213 op_sel_hi:[0,0,0]
	v_mfma_scale_f32_16x16x128_f8f6f4 v[76:79], v[8:15], v[48:55], v[76:79], v213, v213 op_sel_hi:[0,0,0]
	v_mfma_scale_f32_16x16x128_f8f6f4 v[72:75], v[0:7], v[48:55], v[72:75], v213, v213 op_sel_hi:[0,0,0]
	v_mfma_scale_f32_16x16x128_f8f6f4 v[68:71], v[8:15], v[56:63], v[68:71], v213, v213 op_sel_hi:[0,0,0]
	v_mfma_scale_f32_16x16x128_f8f6f4 v[64:67], v[0:7], v[56:63], v[64:67], v213, v213 op_sel_hi:[0,0,0]
	s_setprio 0
	s_barrier
	s_waitcnt vmcnt(14)
	v_mul_f32_e32 v0, 0x42800000, v196
	v_mul_f32_e32 v1, 0x42800000, v192
	v_mul_f32_e32 v2, 0x42800000, v197
	v_mul_f32_e32 v3, 0x42800000, v193
	v_mul_f32_e32 v4, 0x42800000, v198
	v_mul_f32_e32 v5, 0x42800000, v194
	v_mul_f32_e32 v6, 0x42800000, v199
	v_mul_f32_e32 v7, 0x42800000, v195
	v_cvt_pk_fp8_f32 v202, v1, v0
	v_cvt_pk_fp8_f32 v219, v3, v2
	v_cvt_pk_fp8_f32 v220, v5, v4
	v_cvt_pk_fp8_f32 v221, v7, v6
	s_add_i32 s61, s36, 0x200
	s_mov_b32 s33, 0
	s_mov_b32 s79, s66
	s_mov_b32 s90, s68
	s_branch .LBB0_926

.LBB0_926:
	v_mov_b32_e32 v40, v202
	v_mov_b32_e32 v41, v219
	v_mov_b32_e32 v42, v220
	v_mov_b32_e32 v43, v221
	s_add_i32 s4, s94, s33
	s_mov_b32 s64, s90
	s_add_i32 s90, s90, 1
	s_add_i32 s3, s4, 0x200
	s_add_i32 s5, s61, s33
	ds_read_b128 v[24:27], v217 offset:0
	ds_read_b128 v[28:31], v217 offset:0x400
	ds_read_b128 v[16:19], v217 offset:0x800
	ds_read_b128 v[20:23], v217 offset:0xc00
	ds_read_b128 v[46:49], v216 offset:0
	ds_read_b128 v[50:53], v216 offset:0x400
	ds_read_b128 v[54:57], v216 offset:0x800
	ds_read_b128 v[58:61], v216 offset:0xc00
	ds_read_b128 v[192:195], v216 offset:0x1000
	ds_read_b128 v[196:199], v216 offset:0x1400
	ds_read_b128 v[220:223], v216 offset:0x1800
	ds_read_b128 v[224:227], v216 offset:0x1c00
	ds_read_b128 v[8:11], v217 offset:0x4000
	ds_read_b128 v[12:15], v217 offset:0x4400
	ds_read_b128 v[0:3], v217 offset:0x4800
	ds_read_b128 v[4:7], v217 offset:0x4c00
	s_cmpk_eq_i32 s33, 0xe00
	s_cselect_b32 s65, s60, s3
	s_cselect_b32 s16, s95, s5
	s_add_i32 s3, s65, 0x80
	s_mov_b32 m0, s86
	s_add_i32 s5, s4, 0x80180
	buffer_load_dwordx4 v214, s[12:15], s5 offen lds
	s_add_i32 s4, s4, 0xc0180
	s_mov_b32 m0, s89
	s_add_i32 s17, s16, 0x80
	buffer_load_dwordx4 v214, s[12:15], s4 offen lds
	s_lshr_b32 s4, s90, 2
	s_mul_i32 s5, s4, s34
	s_add_i32 s36, s5, s2
	s_cmp_lt_i32 s4, s47
	s_cselect_b64 s[4:5], -1, 0
	s_and_b64 s[62:63], s[4:5], exec
	s_cselect_b32 s67, s36, 0
	s_ashr_i32 s62, s67, 7
	s_bfe_u32 s36, s90, 0x10001
	s_ashr_i32 s63, s62, 31
	s_or_b32 s78, s36, s87
	s_bfe_u32 s36, s67, 0x20005
	s_lshl_b64 vcc, s[62:63], 23
	s_add_u32 vcc_lo, s28, vcc_lo
	s_addc_u32 vcc_hi, s29, vcc_hi
	s_lshl_b32 s38, s36, 21
	s_add_u32 s38, vcc_lo, s38
	s_addc_u32 s39, vcc_hi, 0
	s_lshl_b32 s67, s67, 7
	s_and_b32 s67, s67, 0xf80
	s_lshl_b32 vcc_lo, s67, 2
	s_add_u32 vcc_lo, s38, vcc_lo
	v_and_or_b32 v202, s79, 2, v200
	s_addc_u32 vcc_hi, s39, 0
	v_lshl_or_b32 v44, s78, 5, v218
	v_lshlrev_b64 v[32:33], 14, v[202:203]
	v_lshl_add_u64 v[32:33], vcc, 0, v[32:33]
	v_lshlrev_b32_e32 v202, 2, v44
	v_lshl_add_u64 v[32:33], v[32:33], 0, v[202:203]
	s_movk_i32 s38, 0x4000
	v_add_co_u32_e32 v36, vcc, s38, v32
	s_nop 1
	v_addc_co_u32_e32 v37, vcc, 0, v33, vcc
	global_load_dwordx4 v[32:35], v[32:33], off nt
	s_nop 0
	global_load_dwordx4 v[36:39], v[36:37], off nt
	s_waitcnt vmcnt(10)
	s_waitcnt lgkmcnt(4)
	s_barrier
	s_setprio 1
	v_mfma_scale_f32_16x16x128_f8f6f4 v[188:191], v[24:31], v[46:53], v[188:191], v213, v213 op_sel_hi:[0,0,0]
	v_mfma_scale_f32_16x16x128_f8f6f4 v[184:187], v[16:23], v[46:53], v[184:187], v213, v213 op_sel_hi:[0,0,0]
	v_mfma_scale_f32_16x16x128_f8f6f4 v[180:183], v[24:31], v[54:61], v[180:183], v213, v213 op_sel_hi:[0,0,0]
	v_mfma_scale_f32_16x16x128_f8f6f4 v[176:179], v[16:23], v[54:61], v[176:179], v213, v213 op_sel_hi:[0,0,0]
	v_mfma_scale_f32_16x16x128_f8f6f4 v[172:175], v[24:31], v[192:199], v[172:175], v213, v213 op_sel_hi:[0,0,0]
	v_mfma_scale_f32_16x16x128_f8f6f4 v[168:171], v[16:23], v[192:199], v[168:171], v213, v213 op_sel_hi:[0,0,0]
	v_mfma_scale_f32_16x16x128_f8f6f4 v[164:167], v[24:31], v[220:227], v[164:167], v213, v213 op_sel_hi:[0,0,0]
	v_mfma_scale_f32_16x16x128_f8f6f4 v[160:163], v[16:23], v[220:227], v[160:163], v213, v213 op_sel_hi:[0,0,0]
	s_waitcnt lgkmcnt(2)
	v_mfma_scale_f32_16x16x128_f8f6f4 v[156:159], v[8:15], v[46:53], v[156:159], v213, v213 op_sel_hi:[0,0,0]
	s_waitcnt lgkmcnt(0)
	v_mfma_scale_f32_16x16x128_f8f6f4 v[152:155], v[0:7], v[46:53], v[152:155], v213, v213 op_sel_hi:[0,0,0]
	v_mfma_scale_f32_16x16x128_f8f6f4 v[148:151], v[8:15], v[54:61], v[148:151], v213, v213 op_sel_hi:[0,0,0]
	v_mfma_scale_f32_16x16x128_f8f6f4 v[144:147], v[0:7], v[54:61], v[144:147], v213, v213 op_sel_hi:[0,0,0]
	v_mfma_scale_f32_16x16x128_f8f6f4 v[140:143], v[8:15], v[192:199], v[140:143], v213, v213 op_sel_hi:[0,0,0]
	v_mfma_scale_f32_16x16x128_f8f6f4 v[136:139], v[0:7], v[192:199], v[136:139], v213, v213 op_sel_hi:[0,0,0]
	v_mfma_scale_f32_16x16x128_f8f6f4 v[132:135], v[8:15], v[220:227], v[132:135], v213, v213 op_sel_hi:[0,0,0]
	v_mfma_scale_f32_16x16x128_f8f6f4 v[128:131], v[0:7], v[220:227], v[128:131], v213, v213 op_sel_hi:[0,0,0]
	s_setprio 0
	s_barrier
	ds_read_b128 v[46:49], v216 offset:0x4000
	ds_read_b128 v[50:53], v216 offset:0x4400
	ds_read_b128 v[54:57], v216 offset:0x4800
	ds_read_b128 v[58:61], v216 offset:0x4c00
	ds_read_b128 v[192:195], v216 offset:0x5000
	ds_read_b128 v[196:199], v216 offset:0x5400
	ds_read_b128 v[220:223], v216 offset:0x5800
	ds_read_b128 v[224:227], v216 offset:0x5c00
	s_mov_b32 m0, s71
	s_nop 0
	buffer_load_dwordx4 v215, s[8:11], s16 offen lds
	s_add_i32 s38, s16, 0x80000
	s_mov_b32 m0, s72
	s_nop 0
	buffer_load_dwordx4 v215, s[8:11], s38 offen lds
	s_add_i32 s38, s16, 0x8000
	s_mov_b32 m0, s73
	s_nop 0
	buffer_load_dwordx4 v215, s[8:11], s38 offen lds
	s_add_i32 s38, s16, 0x88000
	s_mov_b32 m0, s74
	s_nop 0
	buffer_load_dwordx4 v215, s[8:11], s38 offen lds
	s_mov_b32 m0, s70
	s_add_i32 s38, s65, 0x40000
	buffer_load_dwordx4 v214, s[12:15], s65 offen lds
	s_mov_b32 m0, s75
	s_nop 0
	buffer_load_dwordx4 v214, s[12:15], s38 offen lds
	s_waitcnt vmcnt(10)
	s_waitcnt lgkmcnt(0)
	s_barrier
	s_setprio 1
	v_mfma_scale_f32_16x16x128_f8f6f4 v[124:127], v[24:31], v[46:53], v[124:127], v213, v213 op_sel_hi:[0,0,0]
	v_mfma_scale_f32_16x16x128_f8f6f4 v[120:123], v[16:23], v[46:53], v[120:123], v213, v213 op_sel_hi:[0,0,0]
	v_mfma_scale_f32_16x16x128_f8f6f4 v[116:119], v[24:31], v[54:61], v[116:119], v213, v213 op_sel_hi:[0,0,0]
	v_mfma_scale_f32_16x16x128_f8f6f4 v[112:115], v[16:23], v[54:61], v[112:115], v213, v213 op_sel_hi:[0,0,0]
	v_mfma_scale_f32_16x16x128_f8f6f4 v[108:111], v[24:31], v[192:199], v[108:111], v213, v213 op_sel_hi:[0,0,0]
	v_mfma_scale_f32_16x16x128_f8f6f4 v[104:107], v[16:23], v[192:199], v[104:107], v213, v213 op_sel_hi:[0,0,0]
	v_mfma_scale_f32_16x16x128_f8f6f4 v[100:103], v[24:31], v[220:227], v[100:103], v213, v213 op_sel_hi:[0,0,0]
	v_mfma_scale_f32_16x16x128_f8f6f4 v[96:99], v[16:23], v[220:227], v[96:99], v213, v213 op_sel_hi:[0,0,0]
	v_mfma_scale_f32_16x16x128_f8f6f4 v[92:95], v[8:15], v[46:53], v[92:95], v213, v213 op_sel_hi:[0,0,0]
	v_mfma_scale_f32_16x16x128_f8f6f4 v[88:91], v[0:7], v[46:53], v[88:91], v213, v213 op_sel_hi:[0,0,0]
	v_mfma_scale_f32_16x16x128_f8f6f4 v[84:87], v[8:15], v[54:61], v[84:87], v213, v213 op_sel_hi:[0,0,0]
	v_mfma_scale_f32_16x16x128_f8f6f4 v[80:83], v[0:7], v[54:61], v[80:83], v213, v213 op_sel_hi:[0,0,0]
	v_mfma_scale_f32_16x16x128_f8f6f4 v[76:79], v[8:15], v[192:199], v[76:79], v213, v213 op_sel_hi:[0,0,0]
	v_mfma_scale_f32_16x16x128_f8f6f4 v[72:75], v[0:7], v[192:199], v[72:75], v213, v213 op_sel_hi:[0,0,0]
	v_mfma_scale_f32_16x16x128_f8f6f4 v[68:71], v[8:15], v[220:227], v[68:71], v213, v213 op_sel_hi:[0,0,0]
	v_mfma_scale_f32_16x16x128_f8f6f4 v[64:67], v[0:7], v[220:227], v[64:67], v213, v213 op_sel_hi:[0,0,0]
	s_setprio 0
	s_barrier
	ds_read_b128 v[16:19], v217 offset:0x8000
	ds_read_b128 v[20:23], v217 offset:0x8400
	ds_read_b128 v[24:27], v217 offset:0x8800
	ds_read_b128 v[28:31], v217 offset:0x8c00
	ds_read_b128 v[46:49], v216 offset:0x8000
	ds_read_b128 v[50:53], v216 offset:0x8400
	ds_read_b128 v[54:57], v216 offset:0x8800
	ds_read_b128 v[58:61], v216 offset:0x8c00
	ds_read_b128 v[192:195], v216 offset:0x9000
	ds_read_b128 v[196:199], v216 offset:0x9400
	ds_read_b128 v[220:223], v216 offset:0x9800
	ds_read_b128 v[224:227], v216 offset:0x9c00
	ds_read_b128 v[8:11], v217 offset:0xc000
	ds_read_b128 v[12:15], v217 offset:0xc400
	ds_read_b128 v[0:3], v217 offset:0xc800
	ds_read_b128 v[4:7], v217 offset:0xcc00
	s_mov_b32 m0, s76
	s_add_i32 s38, s65, 0x80000
	buffer_load_dwordx4 v214, s[12:15], s38 offen lds
	s_add_i32 s38, s65, 0xc0000
	s_mov_b32 m0, s77
	s_nop 0
	buffer_load_dwordx4 v214, s[12:15], s38 offen lds
	s_waitcnt vmcnt(10)
	s_waitcnt lgkmcnt(4)
	s_barrier
	s_setprio 1
	v_mfma_scale_f32_16x16x128_f8f6f4 v[188:191], v[16:23], v[46:53], v[188:191], v213, v213 op_sel_hi:[0,0,0]
	v_mfma_scale_f32_16x16x128_f8f6f4 v[184:187], v[24:31], v[46:53], v[184:187], v213, v213 op_sel_hi:[0,0,0]
	v_mfma_scale_f32_16x16x128_f8f6f4 v[180:183], v[16:23], v[54:61], v[180:183], v213, v213 op_sel_hi:[0,0,0]
	v_mfma_scale_f32_16x16x128_f8f6f4 v[176:179], v[24:31], v[54:61], v[176:179], v213, v213 op_sel_hi:[0,0,0]
	v_mfma_scale_f32_16x16x128_f8f6f4 v[172:175], v[16:23], v[192:199], v[172:175], v213, v213 op_sel_hi:[0,0,0]
	v_mfma_scale_f32_16x16x128_f8f6f4 v[168:171], v[24:31], v[192:199], v[168:171], v213, v213 op_sel_hi:[0,0,0]
	v_mfma_scale_f32_16x16x128_f8f6f4 v[164:167], v[16:23], v[220:227], v[164:167], v213, v213 op_sel_hi:[0,0,0]
	v_mfma_scale_f32_16x16x128_f8f6f4 v[160:163], v[24:31], v[220:227], v[160:163], v213, v213 op_sel_hi:[0,0,0]
	s_waitcnt lgkmcnt(2)
	v_mfma_scale_f32_16x16x128_f8f6f4 v[156:159], v[8:15], v[46:53], v[156:159], v213, v213 op_sel_hi:[0,0,0]
	s_waitcnt lgkmcnt(0)
	v_mfma_scale_f32_16x16x128_f8f6f4 v[152:155], v[0:7], v[46:53], v[152:155], v213, v213 op_sel_hi:[0,0,0]
	v_mfma_scale_f32_16x16x128_f8f6f4 v[148:151], v[8:15], v[54:61], v[148:151], v213, v213 op_sel_hi:[0,0,0]
	v_mfma_scale_f32_16x16x128_f8f6f4 v[144:147], v[0:7], v[54:61], v[144:147], v213, v213 op_sel_hi:[0,0,0]
	v_mfma_scale_f32_16x16x128_f8f6f4 v[140:143], v[8:15], v[192:199], v[140:143], v213, v213 op_sel_hi:[0,0,0]
	v_mfma_scale_f32_16x16x128_f8f6f4 v[136:139], v[0:7], v[192:199], v[136:139], v213, v213 op_sel_hi:[0,0,0]
	v_mfma_scale_f32_16x16x128_f8f6f4 v[132:135], v[8:15], v[220:227], v[132:135], v213, v213 op_sel_hi:[0,0,0]
	v_mfma_scale_f32_16x16x128_f8f6f4 v[128:131], v[0:7], v[220:227], v[128:131], v213, v213 op_sel_hi:[0,0,0]
	s_setprio 0
	s_barrier
	ds_read_b128 v[46:49], v216 offset:0xc000
	ds_read_b128 v[50:53], v216 offset:0xc400
	ds_read_b128 v[54:57], v216 offset:0xc800
	ds_read_b128 v[58:61], v216 offset:0xcc00
	ds_read_b128 v[192:195], v216 offset:0xd000
	ds_read_b128 v[196:199], v216 offset:0xd400
	ds_read_b128 v[220:223], v216 offset:0xd800
	ds_read_b128 v[224:227], v216 offset:0xdc00
	s_mov_b32 m0, s80
	s_nop 0
	buffer_load_dwordx4 v215, s[8:11], s17 offen lds
	s_add_i32 s17, s16, 0x80080
	s_mov_b32 m0, s81
	s_add_i32 s65, s65, 0x40080
	buffer_load_dwordx4 v215, s[8:11], s17 offen lds
	s_add_i32 s17, s16, 0x8080
	s_mov_b32 m0, s84
	s_add_i32 s16, s16, 0x88080
	buffer_load_dwordx4 v215, s[8:11], s17 offen lds
	s_mov_b32 m0, s85
	s_nop 0
	buffer_load_dwordx4 v215, s[8:11], s16 offen lds
	s_mov_b32 m0, s82
	s_nop 0
	buffer_load_dwordx4 v214, s[12:15], s3 offen lds
	s_mov_b32 m0, s83
	s_nop 0
	buffer_load_dwordx4 v214, s[12:15], s65 offen lds
	s_waitcnt vmcnt(8)
	s_waitcnt lgkmcnt(0)
	s_barrier
	s_setprio 1
	v_mfma_scale_f32_16x16x128_f8f6f4 v[124:127], v[16:23], v[46:53], v[124:127], v213, v213 op_sel_hi:[0,0,0]
	v_mfma_scale_f32_16x16x128_f8f6f4 v[120:123], v[24:31], v[46:53], v[120:123], v213, v213 op_sel_hi:[0,0,0]
	v_mfma_scale_f32_16x16x128_f8f6f4 v[116:119], v[16:23], v[54:61], v[116:119], v213, v213 op_sel_hi:[0,0,0]
	v_mfma_scale_f32_16x16x128_f8f6f4 v[112:115], v[24:31], v[54:61], v[112:115], v213, v213 op_sel_hi:[0,0,0]
	v_mfma_scale_f32_16x16x128_f8f6f4 v[108:111], v[16:23], v[192:199], v[108:111], v213, v213 op_sel_hi:[0,0,0]
	v_mfma_scale_f32_16x16x128_f8f6f4 v[104:107], v[24:31], v[192:199], v[104:107], v213, v213 op_sel_hi:[0,0,0]
	v_mfma_scale_f32_16x16x128_f8f6f4 v[100:103], v[16:23], v[220:227], v[100:103], v213, v213 op_sel_hi:[0,0,0]
	v_mfma_scale_f32_16x16x128_f8f6f4 v[96:99], v[24:31], v[220:227], v[96:99], v213, v213 op_sel_hi:[0,0,0]
	v_mfma_scale_f32_16x16x128_f8f6f4 v[92:95], v[8:15], v[46:53], v[92:95], v213, v213 op_sel_hi:[0,0,0]
	v_mfma_scale_f32_16x16x128_f8f6f4 v[88:91], v[0:7], v[46:53], v[88:91], v213, v213 op_sel_hi:[0,0,0]
	v_mfma_scale_f32_16x16x128_f8f6f4 v[84:87], v[8:15], v[54:61], v[84:87], v213, v213 op_sel_hi:[0,0,0]
	v_mfma_scale_f32_16x16x128_f8f6f4 v[80:83], v[0:7], v[54:61], v[80:83], v213, v213 op_sel_hi:[0,0,0]
	v_mfma_scale_f32_16x16x128_f8f6f4 v[76:79], v[8:15], v[192:199], v[76:79], v213, v213 op_sel_hi:[0,0,0]
	v_mfma_scale_f32_16x16x128_f8f6f4 v[72:75], v[0:7], v[192:199], v[72:75], v213, v213 op_sel_hi:[0,0,0]
	v_mfma_scale_f32_16x16x128_f8f6f4 v[68:71], v[8:15], v[220:227], v[68:71], v213, v213 op_sel_hi:[0,0,0]
	v_mfma_scale_f32_16x16x128_f8f6f4 v[64:67], v[0:7], v[220:227], v[64:67], v213, v213 op_sel_hi:[0,0,0]
	s_setprio 0
	s_barrier
	s_bitcmp0_b32 s64, 0
	s_waitcnt vmcnt(15)
	v_mul_f32_e32 v0, 0x42800000, v32
	s_waitcnt vmcnt(14)
	v_mul_f32_e32 v4, 0x42800000, v36
	v_mul_f32_e32 v1, 0x42800000, v33
	v_mul_f32_e32 v5, 0x42800000, v37
	v_mul_f32_e32 v2, 0x42800000, v34
	v_mul_f32_e32 v6, 0x42800000, v38
	v_mul_f32_e32 v3, 0x42800000, v35
	v_mul_f32_e32 v7, 0x42800000, v39
	s_mov_b64 s[64:65], -1
	s_cbranch_scc0 .LBB0_929
	s_andn2_b64 vcc, exec, s[64:65]
	s_cbranch_vccnz .LBB0_925
	s_branch .LBB0_930

.LBB0_1225:
	s_add_i32 s33, s61, 0x100
	s_add_i32 s66, s60, 0x100
	s_waitcnt lgkmcnt(0)
	s_barrier
	s_setprio 1
	v_mfma_scale_f32_16x16x128_f8f6f4 v[192:195], v[24:31], v[56:63], 0, v201, v201 op_sel_hi:[0,0,0]
	v_mfma_scale_f32_16x16x128_f8f6f4 v[188:191], v[16:23], v[56:63], 0, v201, v201 op_sel_hi:[0,0,0]
	v_mfma_scale_f32_16x16x128_f8f6f4 v[184:187], v[24:31], v[48:55], 0, v201, v201 op_sel_hi:[0,0,0]
	v_mfma_scale_f32_16x16x128_f8f6f4 v[180:183], v[16:23], v[48:55], 0, v201, v201 op_sel_hi:[0,0,0]
	v_mfma_scale_f32_16x16x128_f8f6f4 v[176:179], v[24:31], v[40:47], 0, v201, v201 op_sel_hi:[0,0,0]
	v_mfma_scale_f32_16x16x128_f8f6f4 v[172:175], v[16:23], v[40:47], 0, v201, v201 op_sel_hi:[0,0,0]
	v_mfma_scale_f32_16x16x128_f8f6f4 v[168:171], v[24:31], v[32:39], 0, v201, v201 op_sel_hi:[0,0,0]
	v_mfma_scale_f32_16x16x128_f8f6f4 v[164:167], v[16:23], v[32:39], 0, v201, v201 op_sel_hi:[0,0,0]
	v_mfma_scale_f32_16x16x128_f8f6f4 v[160:163], v[8:15], v[56:63], 0, v201, v201 op_sel_hi:[0,0,0]
	v_mfma_scale_f32_16x16x128_f8f6f4 v[156:159], v[0:7], v[56:63], 0, v201, v201 op_sel_hi:[0,0,0]
	v_mfma_scale_f32_16x16x128_f8f6f4 v[152:155], v[8:15], v[48:55], 0, v201, v201 op_sel_hi:[0,0,0]
	v_mfma_scale_f32_16x16x128_f8f6f4 v[148:151], v[0:7], v[48:55], 0, v201, v201 op_sel_hi:[0,0,0]
	v_mfma_scale_f32_16x16x128_f8f6f4 v[144:147], v[8:15], v[40:47], 0, v201, v201 op_sel_hi:[0,0,0]
	v_mfma_scale_f32_16x16x128_f8f6f4 v[140:143], v[0:7], v[40:47], 0, v201, v201 op_sel_hi:[0,0,0]
	v_mfma_scale_f32_16x16x128_f8f6f4 v[136:139], v[8:15], v[32:39], 0, v201, v201 op_sel_hi:[0,0,0]
	v_mfma_scale_f32_16x16x128_f8f6f4 v[132:135], v[0:7], v[32:39], 0, v201, v201 op_sel_hi:[0,0,0]
	s_setprio 0
	s_barrier
	s_mov_b32 m0, s39
	s_mov_b32 s10, s6
	s_mov_b32 s11, s7
	ds_read_b128 v[56:59], v204 offset:0x4000
	ds_read_b128 v[60:63], v204 offset:0x4400
	ds_read_b128 v[48:51], v204 offset:0x4800
	ds_read_b128 v[52:55], v204 offset:0x4c00
	ds_read_b128 v[40:43], v204 offset:0x5000
	ds_read_b128 v[44:47], v204 offset:0x5400
	ds_read_b128 v[32:35], v204 offset:0x5800
	ds_read_b128 v[36:39], v204 offset:0x5c00
	buffer_load_dwordx4 v203, s[8:11], s66 offen lds
	s_add_i32 s66, s60, 0x80100
	s_mov_b32 m0, s40
	s_and_b64 vcc, exec, s[28:29]
	buffer_load_dwordx4 v203, s[8:11], s66 offen lds
	s_add_i32 s66, s60, 0x8100
	s_mov_b32 m0, s41
	s_nop 0
	buffer_load_dwordx4 v203, s[8:11], s66 offen lds
	s_add_i32 s66, s60, 0x88100
	s_mov_b32 m0, s42
	s_nop 0
	buffer_load_dwordx4 v203, s[8:11], s66 offen lds
	s_mov_b32 m0, s38
	s_nop 0
	buffer_load_dwordx4 v214, s[4:7], s33 offen lds
	s_mov_b32 m0, s43
	s_nop 0
	buffer_load_dwordx4 v217, s[4:7], s33 offen lds
	s_cbranch_vccz .LBB0_1236
	s_waitcnt vmcnt(32)
	s_cbranch_execnz .LBB0_1228

.LBB0_1228:
	s_add_i32 s28, s61, 0x180
	s_add_i32 s29, s60, 0x180
	s_waitcnt lgkmcnt(0)
	s_barrier
	s_setprio 1
	v_mfma_scale_f32_16x16x128_f8f6f4 v[128:131], v[24:31], v[56:63], 0, v201, v201 op_sel_hi:[0,0,0]
	v_mfma_scale_f32_16x16x128_f8f6f4 v[124:127], v[16:23], v[56:63], 0, v201, v201 op_sel_hi:[0,0,0]
	v_mfma_scale_f32_16x16x128_f8f6f4 v[120:123], v[24:31], v[48:55], 0, v201, v201 op_sel_hi:[0,0,0]
	v_mfma_scale_f32_16x16x128_f8f6f4 v[116:119], v[16:23], v[48:55], 0, v201, v201 op_sel_hi:[0,0,0]
	v_mfma_scale_f32_16x16x128_f8f6f4 v[112:115], v[24:31], v[40:47], 0, v201, v201 op_sel_hi:[0,0,0]
	v_mfma_scale_f32_16x16x128_f8f6f4 v[108:111], v[16:23], v[40:47], 0, v201, v201 op_sel_hi:[0,0,0]
	v_mfma_scale_f32_16x16x128_f8f6f4 v[104:107], v[24:31], v[32:39], 0, v201, v201 op_sel_hi:[0,0,0]
	v_mfma_scale_f32_16x16x128_f8f6f4 v[100:103], v[16:23], v[32:39], 0, v201, v201 op_sel_hi:[0,0,0]
	v_mfma_scale_f32_16x16x128_f8f6f4 v[96:99], v[8:15], v[56:63], 0, v201, v201 op_sel_hi:[0,0,0]
	v_mfma_scale_f32_16x16x128_f8f6f4 v[92:95], v[0:7], v[56:63], 0, v201, v201 op_sel_hi:[0,0,0]
	v_mfma_scale_f32_16x16x128_f8f6f4 v[88:91], v[8:15], v[48:55], 0, v201, v201 op_sel_hi:[0,0,0]
	v_mfma_scale_f32_16x16x128_f8f6f4 v[84:87], v[0:7], v[48:55], 0, v201, v201 op_sel_hi:[0,0,0]
	v_mfma_scale_f32_16x16x128_f8f6f4 v[80:83], v[8:15], v[40:47], 0, v201, v201 op_sel_hi:[0,0,0]
	v_mfma_scale_f32_16x16x128_f8f6f4 v[76:79], v[0:7], v[40:47], 0, v201, v201 op_sel_hi:[0,0,0]
	v_mfma_scale_f32_16x16x128_f8f6f4 v[72:75], v[8:15], v[32:39], 0, v201, v201 op_sel_hi:[0,0,0]
	v_mfma_scale_f32_16x16x128_f8f6f4 v[68:71], v[0:7], v[32:39], 0, v201, v201 op_sel_hi:[0,0,0]
	s_setprio 0
	s_barrier
	ds_read_b128 v[24:27], v205 offset:0x8000
	ds_read_b128 v[28:31], v205 offset:0x8400
	ds_read_b128 v[16:19], v205 offset:0x8800
	ds_read_b128 v[20:23], v205 offset:0x8c00
	ds_read_b128 v[32:35], v204 offset:0x8000
	ds_read_b128 v[36:39], v204 offset:0x8400
	ds_read_b128 v[40:43], v204 offset:0x8800
	ds_read_b128 v[44:47], v204 offset:0x8c00
	ds_read_b128 v[48:51], v204 offset:0x9000
	ds_read_b128 v[52:55], v204 offset:0x9400
	ds_read_b128 v[56:59], v204 offset:0x9800
	ds_read_b128 v[60:63], v204 offset:0x9c00
	ds_read_b128 v[8:11], v205 offset:0xc000
	ds_read_b128 v[12:15], v205 offset:0xc400
	ds_read_b128 v[0:3], v205 offset:0xc800
	ds_read_b128 v[4:7], v205 offset:0xcc00
	s_mov_b32 m0, s44
	s_nop 0
	buffer_load_dwordx4 v216, s[4:7], s33 offen lds
	s_mov_b32 m0, s45
	s_nop 0
	buffer_load_dwordx4 v215, s[4:7], s33 offen lds
	s_waitcnt vmcnt(8)
	s_waitcnt lgkmcnt(4)
	s_barrier
	s_setprio 1
	v_mfma_scale_f32_16x16x128_f8f6f4 v[192:195], v[24:31], v[32:39], v[192:195], v201, v201 op_sel_hi:[0,0,0]
	v_mfma_scale_f32_16x16x128_f8f6f4 v[188:191], v[16:23], v[32:39], v[188:191], v201, v201 op_sel_hi:[0,0,0]
	v_mfma_scale_f32_16x16x128_f8f6f4 v[184:187], v[24:31], v[40:47], v[184:187], v201, v201 op_sel_hi:[0,0,0]
	v_mfma_scale_f32_16x16x128_f8f6f4 v[180:183], v[16:23], v[40:47], v[180:183], v201, v201 op_sel_hi:[0,0,0]
	v_mfma_scale_f32_16x16x128_f8f6f4 v[176:179], v[24:31], v[48:55], v[176:179], v201, v201 op_sel_hi:[0,0,0]
	v_mfma_scale_f32_16x16x128_f8f6f4 v[172:175], v[16:23], v[48:55], v[172:175], v201, v201 op_sel_hi:[0,0,0]
	v_mfma_scale_f32_16x16x128_f8f6f4 v[168:171], v[24:31], v[56:63], v[168:171], v201, v201 op_sel_hi:[0,0,0]
	v_mfma_scale_f32_16x16x128_f8f6f4 v[164:167], v[16:23], v[56:63], v[164:167], v201, v201 op_sel_hi:[0,0,0]
	s_waitcnt lgkmcnt(2)
	v_mfma_scale_f32_16x16x128_f8f6f4 v[160:163], v[8:15], v[32:39], v[160:163], v201, v201 op_sel_hi:[0,0,0]
	s_waitcnt lgkmcnt(0)
	v_mfma_scale_f32_16x16x128_f8f6f4 v[156:159], v[0:7], v[32:39], v[156:159], v201, v201 op_sel_hi:[0,0,0]
	v_mfma_scale_f32_16x16x128_f8f6f4 v[152:155], v[8:15], v[40:47], v[152:155], v201, v201 op_sel_hi:[0,0,0]
	v_mfma_scale_f32_16x16x128_f8f6f4 v[148:151], v[0:7], v[40:47], v[148:151], v201, v201 op_sel_hi:[0,0,0]
	v_mfma_scale_f32_16x16x128_f8f6f4 v[144:147], v[8:15], v[48:55], v[144:147], v201, v201 op_sel_hi:[0,0,0]
	v_mfma_scale_f32_16x16x128_f8f6f4 v[140:143], v[0:7], v[48:55], v[140:143], v201, v201 op_sel_hi:[0,0,0]
	v_mfma_scale_f32_16x16x128_f8f6f4 v[136:139], v[8:15], v[56:63], v[136:139], v201, v201 op_sel_hi:[0,0,0]
	v_mfma_scale_f32_16x16x128_f8f6f4 v[132:135], v[0:7], v[56:63], v[132:135], v201, v201 op_sel_hi:[0,0,0]
	s_setprio 0
	s_barrier
	ds_read_b128 v[32:35], v204 offset:0xc000
	ds_read_b128 v[36:39], v204 offset:0xc400
	ds_read_b128 v[40:43], v204 offset:0xc800
	ds_read_b128 v[44:47], v204 offset:0xcc00
	ds_read_b128 v[48:51], v204 offset:0xd000
	ds_read_b128 v[52:55], v204 offset:0xd400
	ds_read_b128 v[56:59], v204 offset:0xd800
	ds_read_b128 v[60:63], v204 offset:0xdc00
	s_mov_b32 m0, s48
	s_mov_b32 s10, s6
	s_mov_b32 s11, s7
	buffer_load_dwordx4 v203, s[8:11], s29 offen lds
	s_add_i32 s29, s60, 0x80180
	s_mov_b32 m0, s49
	s_nop 0
	buffer_load_dwordx4 v203, s[8:11], s29 offen lds
	s_add_i32 s29, s60, 0x8180
	s_mov_b32 m0, s62
	s_nop 0
	buffer_load_dwordx4 v203, s[8:11], s29 offen lds
	s_add_i32 s29, s60, 0x88180
	s_mov_b32 m0, s63
	s_nop 0
	buffer_load_dwordx4 v203, s[8:11], s29 offen lds
	s_mov_b32 m0, s50
	s_nop 0
	buffer_load_dwordx4 v214, s[4:7], s28 offen lds
	s_mov_b32 m0, s51
	s_nop 0
	buffer_load_dwordx4 v217, s[4:7], s28 offen lds
	s_waitcnt vmcnt(8)
	s_waitcnt lgkmcnt(0)
	s_barrier
	s_setprio 1
	v_mfma_scale_f32_16x16x128_f8f6f4 v[128:131], v[24:31], v[32:39], v[128:131], v201, v201 op_sel_hi:[0,0,0]
	v_mfma_scale_f32_16x16x128_f8f6f4 v[124:127], v[16:23], v[32:39], v[124:127], v201, v201 op_sel_hi:[0,0,0]
	v_mfma_scale_f32_16x16x128_f8f6f4 v[120:123], v[24:31], v[40:47], v[120:123], v201, v201 op_sel_hi:[0,0,0]
	v_mfma_scale_f32_16x16x128_f8f6f4 v[116:119], v[16:23], v[40:47], v[116:119], v201, v201 op_sel_hi:[0,0,0]
	v_mfma_scale_f32_16x16x128_f8f6f4 v[112:115], v[24:31], v[48:55], v[112:115], v201, v201 op_sel_hi:[0,0,0]
	v_mfma_scale_f32_16x16x128_f8f6f4 v[108:111], v[16:23], v[48:55], v[108:111], v201, v201 op_sel_hi:[0,0,0]
	v_mfma_scale_f32_16x16x128_f8f6f4 v[104:107], v[24:31], v[56:63], v[104:107], v201, v201 op_sel_hi:[0,0,0]
	v_mfma_scale_f32_16x16x128_f8f6f4 v[100:103], v[16:23], v[56:63], v[100:103], v201, v201 op_sel_hi:[0,0,0]
	v_mfma_scale_f32_16x16x128_f8f6f4 v[96:99], v[8:15], v[32:39], v[96:99], v201, v201 op_sel_hi:[0,0,0]
	v_mfma_scale_f32_16x16x128_f8f6f4 v[92:95], v[0:7], v[32:39], v[92:95], v201, v201 op_sel_hi:[0,0,0]
	v_mfma_scale_f32_16x16x128_f8f6f4 v[88:91], v[8:15], v[40:47], v[88:91], v201, v201 op_sel_hi:[0,0,0]
	v_mfma_scale_f32_16x16x128_f8f6f4 v[84:87], v[0:7], v[40:47], v[84:87], v201, v201 op_sel_hi:[0,0,0]
	v_mfma_scale_f32_16x16x128_f8f6f4 v[80:83], v[8:15], v[48:55], v[80:83], v201, v201 op_sel_hi:[0,0,0]
	v_mfma_scale_f32_16x16x128_f8f6f4 v[76:79], v[0:7], v[48:55], v[76:79], v201, v201 op_sel_hi:[0,0,0]
	v_mfma_scale_f32_16x16x128_f8f6f4 v[72:75], v[8:15], v[56:63], v[72:75], v201, v201 op_sel_hi:[0,0,0]
	v_mfma_scale_f32_16x16x128_f8f6f4 v[68:71], v[0:7], v[56:63], v[68:71], v201, v201 op_sel_hi:[0,0,0]
	s_setprio 0
	s_barrier
	s_waitcnt vmcnt(16)
	v_mbcnt_lo_u32_b32 v0, -1, 0
	v_mbcnt_hi_u32_b32 v0, -1, v0
	s_add_i32 s29, s60, 0x200
	v_lshl_add_u32 v0, v0, 4, s37
	v_ashrrev_i32_e32 v1, 31, v0
	v_lshrrev_b32_e32 v1, 22, v1
	v_add_u32_e32 v1, v0, v1
	v_ashrrev_i32_e32 v1, 10, v1
	v_mul_i32_i24_e32 v2, 0x400, v1
	v_sub_u32_e32 v2, v0, v2
	v_lshrrev_b32_e32 v3, 4, v2
	v_bitop3_b32 v3, v3, v2, 32 bitop3:0x6c
	v_ashrrev_i32_e32 v2, 31, v2
	v_lshrrev_b32_e32 v2, 26, v2
	v_add_u32_e32 v2, v3, v2
	v_and_b32_e32 v2, 0xc0, v2
	v_add_u32_e32 v0, 0x2000, v0
	v_sub_u32_e32 v2, v3, v2
	v_ashrrev_i32_e32 v3, 31, v0
	v_lshrrev_b32_e32 v3, 22, v3
	v_add_u32_e32 v3, v0, v3
	v_ashrrev_i32_e32 v3, 10, v3
	v_mul_i32_i24_e32 v4, 0x400, v3
	v_sub_u32_e32 v0, v0, v4
	v_lshrrev_b32_e32 v4, 4, v0
	v_bitop3_b32 v4, v4, v0, 32 bitop3:0x6c
	v_ashrrev_i32_e32 v0, 31, v0
	v_lshrrev_b32_e32 v0, 26, v0
	v_add_u32_e32 v0, v4, v0
	v_and_b32_e32 v0, 0xffc0, v0
	v_sub_u32_e32 v0, v4, v0
	v_lshrrev_b16_e32 v4, 7, v0
	v_and_b32_e32 v4, 1, v4
	v_add_u16_e32 v0, v0, v4
	v_lshlrev_b32_e32 v1, 5, v1
	v_ashrrev_i16_sdwa v2, v202, sext(v2) dst_sel:DWORD dst_unused:UNUSED_PAD src0_sel:DWORD src1_sel:BYTE_0
	v_lshlrev_b32_e32 v3, 5, v3
	v_ashrrev_i16_sdwa v0, v202, sext(v0) dst_sel:DWORD dst_unused:UNUSED_PAD src0_sel:DWORD src1_sel:BYTE_0
	v_and_b32_e32 v1, 32, v1
	v_bfe_i32 v2, v2, 0, 16
	v_and_b32_e32 v3, 32, v3
	v_bfe_i32 v0, v0, 0, 16
	v_add_lshl_u32 v1, v1, v2, 1
	v_add_lshl_u32 v0, v3, v0, 1
	v_lshl_add_u32 v32, v231, 12, v1
	v_lshl_add_u32 v33, v228, 12, v0
	v_lshl_add_u32 v34, v229, 12, v1
	v_lshl_add_u32 v35, v230, 12, v0
	s_mov_b32 s33, 0
.LBB0_1229:
	s_add_i32 s66, s28, 0x80
	s_cmp_eq_u32 s33, 28
	s_cselect_b64 vcc, -1, 0
	ds_read_b128 v[16:19], v205 offset:0
	ds_read_b128 v[20:23], v205 offset:0x400
	ds_read_b128 v[24:27], v205 offset:0x800
	ds_read_b128 v[28:31], v205 offset:0xc00
	ds_read_b128 v[36:39], v204 offset:0
	ds_read_b128 v[40:43], v204 offset:0x400
	ds_read_b128 v[44:47], v204 offset:0x800
	ds_read_b128 v[48:51], v204 offset:0xc00
	ds_read_b128 v[52:55], v204 offset:0x1000
	ds_read_b128 v[56:59], v204 offset:0x1400
	ds_read_b128 v[228:231], v204 offset:0x1800
	ds_read_b128 v[232:235], v204 offset:0x1c00
	ds_read_b128 v[8:11], v205 offset:0x4000
	ds_read_b128 v[12:15], v205 offset:0x4400
	ds_read_b128 v[0:3], v205 offset:0x4800
	ds_read_b128 v[4:7], v205 offset:0x4c00
	s_and_b64 s[60:61], vcc, exec
	s_cselect_b32 s66, s72, s66
	s_cselect_b32 s61, s73, s29
	s_add_i32 s60, s66, 0x80
	s_mov_b32 m0, s65
	s_nop 0
	buffer_load_dwordx4 v216, s[4:7], s28 offen lds
	s_mov_b32 m0, s68
	s_nop 0
	buffer_load_dwordx4 v215, s[4:7], s28 offen lds
	s_waitcnt vmcnt(8)
	s_waitcnt lgkmcnt(4)
	s_barrier
	s_setprio 1
	v_mfma_scale_f32_16x16x128_f8f6f4 v[192:195], v[16:23], v[36:43], v[192:195], v201, v201 op_sel_hi:[0,0,0]
	v_mfma_scale_f32_16x16x128_f8f6f4 v[188:191], v[24:31], v[36:43], v[188:191], v201, v201 op_sel_hi:[0,0,0]
	v_mfma_scale_f32_16x16x128_f8f6f4 v[184:187], v[16:23], v[44:51], v[184:187], v201, v201 op_sel_hi:[0,0,0]
	v_mfma_scale_f32_16x16x128_f8f6f4 v[180:183], v[24:31], v[44:51], v[180:183], v201, v201 op_sel_hi:[0,0,0]
	v_mfma_scale_f32_16x16x128_f8f6f4 v[176:179], v[16:23], v[52:59], v[176:179], v201, v201 op_sel_hi:[0,0,0]
	v_mfma_scale_f32_16x16x128_f8f6f4 v[172:175], v[24:31], v[52:59], v[172:175], v201, v201 op_sel_hi:[0,0,0]
	v_mfma_scale_f32_16x16x128_f8f6f4 v[168:171], v[16:23], v[228:235], v[168:171], v201, v201 op_sel_hi:[0,0,0]
	v_mfma_scale_f32_16x16x128_f8f6f4 v[164:167], v[24:31], v[228:235], v[164:167], v201, v201 op_sel_hi:[0,0,0]
	s_waitcnt lgkmcnt(2)
	v_mfma_scale_f32_16x16x128_f8f6f4 v[160:163], v[8:15], v[36:43], v[160:163], v201, v201 op_sel_hi:[0,0,0]
	s_waitcnt lgkmcnt(0)
	v_mfma_scale_f32_16x16x128_f8f6f4 v[156:159], v[0:7], v[36:43], v[156:159], v201, v201 op_sel_hi:[0,0,0]
	v_mfma_scale_f32_16x16x128_f8f6f4 v[152:155], v[8:15], v[44:51], v[152:155], v201, v201 op_sel_hi:[0,0,0]
	v_mfma_scale_f32_16x16x128_f8f6f4 v[148:151], v[0:7], v[44:51], v[148:151], v201, v201 op_sel_hi:[0,0,0]
	v_mfma_scale_f32_16x16x128_f8f6f4 v[144:147], v[8:15], v[52:59], v[144:147], v201, v201 op_sel_hi:[0,0,0]
	v_mfma_scale_f32_16x16x128_f8f6f4 v[140:143], v[0:7], v[52:59], v[140:143], v201, v201 op_sel_hi:[0,0,0]
	v_mfma_scale_f32_16x16x128_f8f6f4 v[136:139], v[8:15], v[228:235], v[136:139], v201, v201 op_sel_hi:[0,0,0]
	v_mfma_scale_f32_16x16x128_f8f6f4 v[132:135], v[0:7], v[228:235], v[132:135], v201, v201 op_sel_hi:[0,0,0]
	s_setprio 0
	s_barrier
	ds_read_b128 v[36:39], v204 offset:0x4000
	ds_read_b128 v[40:43], v204 offset:0x4400
	ds_read_b128 v[44:47], v204 offset:0x4800
	ds_read_b128 v[48:51], v204 offset:0x4c00
	ds_read_b128 v[52:55], v204 offset:0x5000
	ds_read_b128 v[56:59], v204 offset:0x5400
	ds_read_b128 v[228:231], v204 offset:0x5800
	ds_read_b128 v[232:235], v204 offset:0x5c00
	s_mov_b32 m0, s39
	s_nop 0
	buffer_load_dwordx4 v203, s[8:11], s61 offen lds
	s_add_i32 s67, s61, 0x80000
	s_mov_b32 m0, s40
	v_cndmask_b32_e32 v60, v214, v32, vcc
	buffer_load_dwordx4 v203, s[8:11], s67 offen lds
	s_add_i32 s67, s61, 0x8000
	s_mov_b32 m0, s41
	v_cndmask_b32_e32 v61, v217, v33, vcc
	buffer_load_dwordx4 v203, s[8:11], s67 offen lds
	s_add_i32 s67, s61, 0x88000
	s_mov_b32 m0, s42
	s_nop 0
	buffer_load_dwordx4 v203, s[8:11], s67 offen lds
	s_mov_b32 m0, s38
	s_nop 0
	buffer_load_dwordx4 v60, s[4:7], s66 offen lds
	s_mov_b32 m0, s43
	s_nop 0
	buffer_load_dwordx4 v61, s[4:7], s66 offen lds
	s_waitcnt vmcnt(8)
	s_waitcnt lgkmcnt(0)
	s_barrier
	s_setprio 1
	v_mfma_scale_f32_16x16x128_f8f6f4 v[128:131], v[16:23], v[36:43], v[128:131], v201, v201 op_sel_hi:[0,0,0]
	v_mfma_scale_f32_16x16x128_f8f6f4 v[124:127], v[24:31], v[36:43], v[124:127], v201, v201 op_sel_hi:[0,0,0]
	v_mfma_scale_f32_16x16x128_f8f6f4 v[120:123], v[16:23], v[44:51], v[120:123], v201, v201 op_sel_hi:[0,0,0]
	v_mfma_scale_f32_16x16x128_f8f6f4 v[116:119], v[24:31], v[44:51], v[116:119], v201, v201 op_sel_hi:[0,0,0]
	v_mfma_scale_f32_16x16x128_f8f6f4 v[112:115], v[16:23], v[52:59], v[112:115], v201, v201 op_sel_hi:[0,0,0]
	v_mfma_scale_f32_16x16x128_f8f6f4 v[108:111], v[24:31], v[52:59], v[108:111], v201, v201 op_sel_hi:[0,0,0]
	v_mfma_scale_f32_16x16x128_f8f6f4 v[104:107], v[16:23], v[228:235], v[104:107], v201, v201 op_sel_hi:[0,0,0]
	v_mfma_scale_f32_16x16x128_f8f6f4 v[100:103], v[24:31], v[228:235], v[100:103], v201, v201 op_sel_hi:[0,0,0]
	v_mfma_scale_f32_16x16x128_f8f6f4 v[96:99], v[8:15], v[36:43], v[96:99], v201, v201 op_sel_hi:[0,0,0]
	v_mfma_scale_f32_16x16x128_f8f6f4 v[92:95], v[0:7], v[36:43], v[92:95], v201, v201 op_sel_hi:[0,0,0]
	v_mfma_scale_f32_16x16x128_f8f6f4 v[88:91], v[8:15], v[44:51], v[88:91], v201, v201 op_sel_hi:[0,0,0]
	v_mfma_scale_f32_16x16x128_f8f6f4 v[84:87], v[0:7], v[44:51], v[84:87], v201, v201 op_sel_hi:[0,0,0]
	v_mfma_scale_f32_16x16x128_f8f6f4 v[80:83], v[8:15], v[52:59], v[80:83], v201, v201 op_sel_hi:[0,0,0]
	v_mfma_scale_f32_16x16x128_f8f6f4 v[76:79], v[0:7], v[52:59], v[76:79], v201, v201 op_sel_hi:[0,0,0]
	v_mfma_scale_f32_16x16x128_f8f6f4 v[72:75], v[8:15], v[228:235], v[72:75], v201, v201 op_sel_hi:[0,0,0]
	v_mfma_scale_f32_16x16x128_f8f6f4 v[68:71], v[0:7], v[228:235], v[68:71], v201, v201 op_sel_hi:[0,0,0]
	s_setprio 0
	s_barrier
	ds_read_b128 v[24:27], v205 offset:0x8000
	ds_read_b128 v[28:31], v205 offset:0x8400
	ds_read_b128 v[16:19], v205 offset:0x8800
	ds_read_b128 v[20:23], v205 offset:0x8c00
	ds_read_b128 v[36:39], v204 offset:0x8000
	ds_read_b128 v[40:43], v204 offset:0x8400
	ds_read_b128 v[44:47], v204 offset:0x8800
	ds_read_b128 v[48:51], v204 offset:0x8c00
	ds_read_b128 v[52:55], v204 offset:0x9000
	ds_read_b128 v[56:59], v204 offset:0x9400
	ds_read_b128 v[228:231], v204 offset:0x9800
	ds_read_b128 v[232:235], v204 offset:0x9c00
	ds_read_b128 v[8:11], v205 offset:0xc000
	ds_read_b128 v[12:15], v205 offset:0xc400
	ds_read_b128 v[0:3], v205 offset:0xc800
	ds_read_b128 v[4:7], v205 offset:0xcc00
	s_mov_b32 m0, s44
	v_cndmask_b32_e32 v62, v216, v34, vcc
	buffer_load_dwordx4 v62, s[4:7], s66 offen lds
	v_cndmask_b32_e32 v62, v215, v35, vcc
	s_mov_b32 m0, s45
	s_nop 0
	buffer_load_dwordx4 v62, s[4:7], s66 offen lds
	s_waitcnt vmcnt(8)
	s_waitcnt lgkmcnt(4)
	s_barrier
	s_setprio 1
	v_mfma_scale_f32_16x16x128_f8f6f4 v[192:195], v[24:31], v[36:43], v[192:195], v201, v201 op_sel_hi:[0,0,0]
	v_mfma_scale_f32_16x16x128_f8f6f4 v[188:191], v[16:23], v[36:43], v[188:191], v201, v201 op_sel_hi:[0,0,0]
	v_mfma_scale_f32_16x16x128_f8f6f4 v[184:187], v[24:31], v[44:51], v[184:187], v201, v201 op_sel_hi:[0,0,0]
	v_mfma_scale_f32_16x16x128_f8f6f4 v[180:183], v[16:23], v[44:51], v[180:183], v201, v201 op_sel_hi:[0,0,0]
	v_mfma_scale_f32_16x16x128_f8f6f4 v[176:179], v[24:31], v[52:59], v[176:179], v201, v201 op_sel_hi:[0,0,0]
	v_mfma_scale_f32_16x16x128_f8f6f4 v[172:175], v[16:23], v[52:59], v[172:175], v201, v201 op_sel_hi:[0,0,0]
	v_mfma_scale_f32_16x16x128_f8f6f4 v[168:171], v[24:31], v[228:235], v[168:171], v201, v201 op_sel_hi:[0,0,0]
	v_mfma_scale_f32_16x16x128_f8f6f4 v[164:167], v[16:23], v[228:235], v[164:167], v201, v201 op_sel_hi:[0,0,0]
	s_waitcnt lgkmcnt(2)
	v_mfma_scale_f32_16x16x128_f8f6f4 v[160:163], v[8:15], v[36:43], v[160:163], v201, v201 op_sel_hi:[0,0,0]
	s_waitcnt lgkmcnt(0)
	v_mfma_scale_f32_16x16x128_f8f6f4 v[156:159], v[0:7], v[36:43], v[156:159], v201, v201 op_sel_hi:[0,0,0]
	v_mfma_scale_f32_16x16x128_f8f6f4 v[152:155], v[8:15], v[44:51], v[152:155], v201, v201 op_sel_hi:[0,0,0]
	v_mfma_scale_f32_16x16x128_f8f6f4 v[148:151], v[0:7], v[44:51], v[148:151], v201, v201 op_sel_hi:[0,0,0]
	v_mfma_scale_f32_16x16x128_f8f6f4 v[144:147], v[8:15], v[52:59], v[144:147], v201, v201 op_sel_hi:[0,0,0]
	v_mfma_scale_f32_16x16x128_f8f6f4 v[140:143], v[0:7], v[52:59], v[140:143], v201, v201 op_sel_hi:[0,0,0]
	v_mfma_scale_f32_16x16x128_f8f6f4 v[136:139], v[8:15], v[228:235], v[136:139], v201, v201 op_sel_hi:[0,0,0]
	v_mfma_scale_f32_16x16x128_f8f6f4 v[132:135], v[0:7], v[228:235], v[132:135], v201, v201 op_sel_hi:[0,0,0]
	s_setprio 0
	s_barrier
	ds_read_b128 v[36:39], v204 offset:0xc000
	ds_read_b128 v[40:43], v204 offset:0xc400
	ds_read_b128 v[44:47], v204 offset:0xc800
	ds_read_b128 v[48:51], v204 offset:0xcc00
	ds_read_b128 v[52:55], v204 offset:0xd000
	ds_read_b128 v[56:59], v204 offset:0xd400
	ds_read_b128 v[228:231], v204 offset:0xd800
	ds_read_b128 v[232:235], v204 offset:0xdc00
	s_mov_b32 m0, s48
	s_add_i32 s66, s61, 0x80
	buffer_load_dwordx4 v203, s[8:11], s66 offen lds
	s_add_i32 s66, s61, 0x80080
	s_mov_b32 m0, s49
	s_nop 0
	buffer_load_dwordx4 v203, s[8:11], s66 offen lds
	s_add_i32 s66, s61, 0x8080
	s_mov_b32 m0, s62
	s_add_i32 s61, s61, 0x88080
	buffer_load_dwordx4 v203, s[8:11], s66 offen lds
	s_mov_b32 m0, s63
	s_nop 0
	buffer_load_dwordx4 v203, s[8:11], s61 offen lds
	s_mov_b32 m0, s50
	s_nop 0
	buffer_load_dwordx4 v60, s[4:7], s60 offen lds
	s_mov_b32 m0, s51
	s_nop 0
	buffer_load_dwordx4 v61, s[4:7], s60 offen lds
	s_waitcnt vmcnt(8)
	s_waitcnt lgkmcnt(0)
	s_barrier
	s_setprio 1
	v_mfma_scale_f32_16x16x128_f8f6f4 v[128:131], v[24:31], v[36:43], v[128:131], v201, v201 op_sel_hi:[0,0,0]
	v_mfma_scale_f32_16x16x128_f8f6f4 v[124:127], v[16:23], v[36:43], v[124:127], v201, v201 op_sel_hi:[0,0,0]
	v_mfma_scale_f32_16x16x128_f8f6f4 v[120:123], v[24:31], v[44:51], v[120:123], v201, v201 op_sel_hi:[0,0,0]
	v_mfma_scale_f32_16x16x128_f8f6f4 v[116:119], v[16:23], v[44:51], v[116:119], v201, v201 op_sel_hi:[0,0,0]
	v_mfma_scale_f32_16x16x128_f8f6f4 v[112:115], v[24:31], v[52:59], v[112:115], v201, v201 op_sel_hi:[0,0,0]
	v_mfma_scale_f32_16x16x128_f8f6f4 v[108:111], v[16:23], v[52:59], v[108:111], v201, v201 op_sel_hi:[0,0,0]
	v_mfma_scale_f32_16x16x128_f8f6f4 v[104:107], v[24:31], v[228:235], v[104:107], v201, v201 op_sel_hi:[0,0,0]
	v_mfma_scale_f32_16x16x128_f8f6f4 v[100:103], v[16:23], v[228:235], v[100:103], v201, v201 op_sel_hi:[0,0,0]
	v_mfma_scale_f32_16x16x128_f8f6f4 v[96:99], v[8:15], v[36:43], v[96:99], v201, v201 op_sel_hi:[0,0,0]
	v_mfma_scale_f32_16x16x128_f8f6f4 v[92:95], v[0:7], v[36:43], v[92:95], v201, v201 op_sel_hi:[0,0,0]
	v_mfma_scale_f32_16x16x128_f8f6f4 v[88:91], v[8:15], v[44:51], v[88:91], v201, v201 op_sel_hi:[0,0,0]
	v_mfma_scale_f32_16x16x128_f8f6f4 v[84:87], v[0:7], v[44:51], v[84:87], v201, v201 op_sel_hi:[0,0,0]
	v_mfma_scale_f32_16x16x128_f8f6f4 v[80:83], v[8:15], v[52:59], v[80:83], v201, v201 op_sel_hi:[0,0,0]
	v_mfma_scale_f32_16x16x128_f8f6f4 v[76:79], v[0:7], v[52:59], v[76:79], v201, v201 op_sel_hi:[0,0,0]
	v_mfma_scale_f32_16x16x128_f8f6f4 v[72:75], v[8:15], v[228:235], v[72:75], v201, v201 op_sel_hi:[0,0,0]
	v_mfma_scale_f32_16x16x128_f8f6f4 v[68:71], v[0:7], v[228:235], v[68:71], v201, v201 op_sel_hi:[0,0,0]
	s_setprio 0
	s_barrier
	s_add_i32 s33, s33, 2
	s_addk_i32 s28, 0x100
	s_addk_i32 s29, 0x100
	s_cmp_gt_u32 s33, 29
	s_cbranch_scc0 .LBB0_1229
	s_and_b64 vcc, exec, s[18:19]
	s_cbranch_vccz .LBB0_1232
	s_barrier

.LBB0_1326:
	s_add_i32 s33, s89, 0x100
	s_add_i32 s66, s61, 0x100
	s_waitcnt lgkmcnt(0)
	s_barrier
	s_setprio 1
	v_mfma_scale_f32_16x16x128_f8f6f4 v[192:195], v[24:31], v[56:63], 0, v198, v198 op_sel_hi:[0,0,0]
	v_mfma_scale_f32_16x16x128_f8f6f4 v[188:191], v[16:23], v[56:63], 0, v198, v198 op_sel_hi:[0,0,0]
	v_mfma_scale_f32_16x16x128_f8f6f4 v[184:187], v[24:31], v[48:55], 0, v198, v198 op_sel_hi:[0,0,0]
	v_mfma_scale_f32_16x16x128_f8f6f4 v[180:183], v[16:23], v[48:55], 0, v198, v198 op_sel_hi:[0,0,0]
	v_mfma_scale_f32_16x16x128_f8f6f4 v[176:179], v[24:31], v[40:47], 0, v198, v198 op_sel_hi:[0,0,0]
	v_mfma_scale_f32_16x16x128_f8f6f4 v[172:175], v[16:23], v[40:47], 0, v198, v198 op_sel_hi:[0,0,0]
	v_mfma_scale_f32_16x16x128_f8f6f4 v[168:171], v[24:31], v[32:39], 0, v198, v198 op_sel_hi:[0,0,0]
	v_mfma_scale_f32_16x16x128_f8f6f4 v[164:167], v[16:23], v[32:39], 0, v198, v198 op_sel_hi:[0,0,0]
	v_mfma_scale_f32_16x16x128_f8f6f4 v[160:163], v[8:15], v[56:63], 0, v198, v198 op_sel_hi:[0,0,0]
	v_mfma_scale_f32_16x16x128_f8f6f4 v[156:159], v[0:7], v[56:63], 0, v198, v198 op_sel_hi:[0,0,0]
	v_mfma_scale_f32_16x16x128_f8f6f4 v[152:155], v[8:15], v[48:55], 0, v198, v198 op_sel_hi:[0,0,0]
	v_mfma_scale_f32_16x16x128_f8f6f4 v[148:151], v[0:7], v[48:55], 0, v198, v198 op_sel_hi:[0,0,0]
	v_mfma_scale_f32_16x16x128_f8f6f4 v[144:147], v[8:15], v[40:47], 0, v198, v198 op_sel_hi:[0,0,0]
	v_mfma_scale_f32_16x16x128_f8f6f4 v[140:143], v[0:7], v[40:47], 0, v198, v198 op_sel_hi:[0,0,0]
	v_mfma_scale_f32_16x16x128_f8f6f4 v[136:139], v[8:15], v[32:39], 0, v198, v198 op_sel_hi:[0,0,0]
	v_mfma_scale_f32_16x16x128_f8f6f4 v[132:135], v[0:7], v[32:39], 0, v198, v198 op_sel_hi:[0,0,0]
	s_setprio 0
	s_barrier
	s_mov_b32 m0, s45
	s_mov_b32 s10, s6
	s_mov_b32 s11, s7
	ds_read_b128 v[56:59], v201 offset:0x4000
	ds_read_b128 v[60:63], v201 offset:0x4400
	ds_read_b128 v[48:51], v201 offset:0x4800
	ds_read_b128 v[52:55], v201 offset:0x4c00
	ds_read_b128 v[40:43], v201 offset:0x5000
	ds_read_b128 v[44:47], v201 offset:0x5400
	ds_read_b128 v[32:35], v201 offset:0x5800
	ds_read_b128 v[36:39], v201 offset:0x5c00
	buffer_load_dwordx4 v200, s[8:11], s66 offen lds
	s_add_i32 s66, s61, 0x80100
	s_mov_b32 m0, s46
	s_and_b64 vcc, exec, s[36:37]
	buffer_load_dwordx4 v200, s[8:11], s66 offen lds
	s_add_i32 s66, s61, 0x8100
	s_mov_b32 m0, s47
	s_nop 0
	buffer_load_dwordx4 v200, s[8:11], s66 offen lds
	s_add_i32 s66, s61, 0x88100
	s_mov_b32 m0, s48
	s_nop 0
	buffer_load_dwordx4 v200, s[8:11], s66 offen lds
	s_mov_b32 m0, s44
	s_nop 0
	buffer_load_dwordx4 v205, s[4:7], s33 offen lds
	s_mov_b32 m0, s49
	s_nop 0
	buffer_load_dwordx4 v208, s[4:7], s33 offen lds
	s_cbranch_vccz .LBB0_1337
	s_waitcnt vmcnt(32)
	s_cbranch_execnz .LBB0_1329

.LBB0_1329:
	s_add_i32 s36, s89, 0x180
	s_add_i32 s37, s61, 0x180
	s_waitcnt lgkmcnt(0)
	s_barrier
	s_setprio 1
	v_mfma_scale_f32_16x16x128_f8f6f4 v[128:131], v[24:31], v[56:63], 0, v198, v198 op_sel_hi:[0,0,0]
	v_mfma_scale_f32_16x16x128_f8f6f4 v[124:127], v[16:23], v[56:63], 0, v198, v198 op_sel_hi:[0,0,0]
	v_mfma_scale_f32_16x16x128_f8f6f4 v[120:123], v[24:31], v[48:55], 0, v198, v198 op_sel_hi:[0,0,0]
	v_mfma_scale_f32_16x16x128_f8f6f4 v[116:119], v[16:23], v[48:55], 0, v198, v198 op_sel_hi:[0,0,0]
	v_mfma_scale_f32_16x16x128_f8f6f4 v[112:115], v[24:31], v[40:47], 0, v198, v198 op_sel_hi:[0,0,0]
	v_mfma_scale_f32_16x16x128_f8f6f4 v[108:111], v[16:23], v[40:47], 0, v198, v198 op_sel_hi:[0,0,0]
	v_mfma_scale_f32_16x16x128_f8f6f4 v[104:107], v[24:31], v[32:39], 0, v198, v198 op_sel_hi:[0,0,0]
	v_mfma_scale_f32_16x16x128_f8f6f4 v[100:103], v[16:23], v[32:39], 0, v198, v198 op_sel_hi:[0,0,0]
	v_mfma_scale_f32_16x16x128_f8f6f4 v[96:99], v[8:15], v[56:63], 0, v198, v198 op_sel_hi:[0,0,0]
	v_mfma_scale_f32_16x16x128_f8f6f4 v[92:95], v[0:7], v[56:63], 0, v198, v198 op_sel_hi:[0,0,0]
	v_mfma_scale_f32_16x16x128_f8f6f4 v[88:91], v[8:15], v[48:55], 0, v198, v198 op_sel_hi:[0,0,0]
	v_mfma_scale_f32_16x16x128_f8f6f4 v[84:87], v[0:7], v[48:55], 0, v198, v198 op_sel_hi:[0,0,0]
	v_mfma_scale_f32_16x16x128_f8f6f4 v[80:83], v[8:15], v[40:47], 0, v198, v198 op_sel_hi:[0,0,0]
	v_mfma_scale_f32_16x16x128_f8f6f4 v[76:79], v[0:7], v[40:47], 0, v198, v198 op_sel_hi:[0,0,0]
	v_mfma_scale_f32_16x16x128_f8f6f4 v[72:75], v[8:15], v[32:39], 0, v198, v198 op_sel_hi:[0,0,0]
	v_mfma_scale_f32_16x16x128_f8f6f4 v[68:71], v[0:7], v[32:39], 0, v198, v198 op_sel_hi:[0,0,0]
	s_setprio 0
	s_barrier
	ds_read_b128 v[24:27], v202 offset:0x8000
	ds_read_b128 v[28:31], v202 offset:0x8400
	ds_read_b128 v[16:19], v202 offset:0x8800
	ds_read_b128 v[20:23], v202 offset:0x8c00
	ds_read_b128 v[32:35], v201 offset:0x8000
	ds_read_b128 v[36:39], v201 offset:0x8400
	ds_read_b128 v[40:43], v201 offset:0x8800
	ds_read_b128 v[44:47], v201 offset:0x8c00
	ds_read_b128 v[48:51], v201 offset:0x9000
	ds_read_b128 v[52:55], v201 offset:0x9400
	ds_read_b128 v[56:59], v201 offset:0x9800
	ds_read_b128 v[60:63], v201 offset:0x9c00
	ds_read_b128 v[8:11], v202 offset:0xc000
	ds_read_b128 v[12:15], v202 offset:0xc400
	ds_read_b128 v[0:3], v202 offset:0xc800
	ds_read_b128 v[4:7], v202 offset:0xcc00
	s_mov_b32 m0, s50
	s_nop 0
	buffer_load_dwordx4 v207, s[4:7], s33 offen lds
	s_mov_b32 m0, s51
	s_nop 0
	buffer_load_dwordx4 v206, s[4:7], s33 offen lds
	s_waitcnt vmcnt(8)
	s_waitcnt lgkmcnt(4)
	s_barrier
	s_setprio 1
	v_mfma_scale_f32_16x16x128_f8f6f4 v[192:195], v[24:31], v[32:39], v[192:195], v198, v198 op_sel_hi:[0,0,0]
	v_mfma_scale_f32_16x16x128_f8f6f4 v[188:191], v[16:23], v[32:39], v[188:191], v198, v198 op_sel_hi:[0,0,0]
	v_mfma_scale_f32_16x16x128_f8f6f4 v[184:187], v[24:31], v[40:47], v[184:187], v198, v198 op_sel_hi:[0,0,0]
	v_mfma_scale_f32_16x16x128_f8f6f4 v[180:183], v[16:23], v[40:47], v[180:183], v198, v198 op_sel_hi:[0,0,0]
	v_mfma_scale_f32_16x16x128_f8f6f4 v[176:179], v[24:31], v[48:55], v[176:179], v198, v198 op_sel_hi:[0,0,0]
	v_mfma_scale_f32_16x16x128_f8f6f4 v[172:175], v[16:23], v[48:55], v[172:175], v198, v198 op_sel_hi:[0,0,0]
	v_mfma_scale_f32_16x16x128_f8f6f4 v[168:171], v[24:31], v[56:63], v[168:171], v198, v198 op_sel_hi:[0,0,0]
	v_mfma_scale_f32_16x16x128_f8f6f4 v[164:167], v[16:23], v[56:63], v[164:167], v198, v198 op_sel_hi:[0,0,0]
	s_waitcnt lgkmcnt(2)
	v_mfma_scale_f32_16x16x128_f8f6f4 v[160:163], v[8:15], v[32:39], v[160:163], v198, v198 op_sel_hi:[0,0,0]
	s_waitcnt lgkmcnt(0)
	v_mfma_scale_f32_16x16x128_f8f6f4 v[156:159], v[0:7], v[32:39], v[156:159], v198, v198 op_sel_hi:[0,0,0]
	v_mfma_scale_f32_16x16x128_f8f6f4 v[152:155], v[8:15], v[40:47], v[152:155], v198, v198 op_sel_hi:[0,0,0]
	v_mfma_scale_f32_16x16x128_f8f6f4 v[148:151], v[0:7], v[40:47], v[148:151], v198, v198 op_sel_hi:[0,0,0]
	v_mfma_scale_f32_16x16x128_f8f6f4 v[144:147], v[8:15], v[48:55], v[144:147], v198, v198 op_sel_hi:[0,0,0]
	v_mfma_scale_f32_16x16x128_f8f6f4 v[140:143], v[0:7], v[48:55], v[140:143], v198, v198 op_sel_hi:[0,0,0]
	v_mfma_scale_f32_16x16x128_f8f6f4 v[136:139], v[8:15], v[56:63], v[136:139], v198, v198 op_sel_hi:[0,0,0]
	v_mfma_scale_f32_16x16x128_f8f6f4 v[132:135], v[0:7], v[56:63], v[132:135], v198, v198 op_sel_hi:[0,0,0]
	s_setprio 0
	s_barrier
	ds_read_b128 v[32:35], v201 offset:0xc000
	ds_read_b128 v[36:39], v201 offset:0xc400
	ds_read_b128 v[40:43], v201 offset:0xc800
	ds_read_b128 v[44:47], v201 offset:0xcc00
	ds_read_b128 v[48:51], v201 offset:0xd000
	ds_read_b128 v[52:55], v201 offset:0xd400
	ds_read_b128 v[56:59], v201 offset:0xd800
	ds_read_b128 v[60:63], v201 offset:0xdc00
	s_mov_b32 m0, s64
	s_mov_b32 s10, s6
	s_mov_b32 s11, s7
	buffer_load_dwordx4 v200, s[8:11], s37 offen lds
	s_add_i32 s33, s61, 0x80180
	s_mov_b32 m0, s65
	s_nop 0
	buffer_load_dwordx4 v200, s[8:11], s33 offen lds
	s_add_i32 s33, s61, 0x8180
	s_mov_b32 m0, s70
	s_nop 0
	buffer_load_dwordx4 v200, s[8:11], s33 offen lds
	s_add_i32 s33, s61, 0x88180
	s_mov_b32 m0, s71
	s_nop 0
	buffer_load_dwordx4 v200, s[8:11], s33 offen lds
	s_mov_b32 m0, s68
	s_nop 0
	buffer_load_dwordx4 v205, s[4:7], s36 offen lds
	s_mov_b32 m0, s69
	s_nop 0
	buffer_load_dwordx4 v208, s[4:7], s36 offen lds
	s_waitcnt vmcnt(8)
	s_waitcnt lgkmcnt(0)
	s_barrier
	s_setprio 1
	v_mfma_scale_f32_16x16x128_f8f6f4 v[128:131], v[24:31], v[32:39], v[128:131], v198, v198 op_sel_hi:[0,0,0]
	v_mfma_scale_f32_16x16x128_f8f6f4 v[124:127], v[16:23], v[32:39], v[124:127], v198, v198 op_sel_hi:[0,0,0]
	v_mfma_scale_f32_16x16x128_f8f6f4 v[120:123], v[24:31], v[40:47], v[120:123], v198, v198 op_sel_hi:[0,0,0]
	v_mfma_scale_f32_16x16x128_f8f6f4 v[116:119], v[16:23], v[40:47], v[116:119], v198, v198 op_sel_hi:[0,0,0]
	v_mfma_scale_f32_16x16x128_f8f6f4 v[112:115], v[24:31], v[48:55], v[112:115], v198, v198 op_sel_hi:[0,0,0]
	v_mfma_scale_f32_16x16x128_f8f6f4 v[108:111], v[16:23], v[48:55], v[108:111], v198, v198 op_sel_hi:[0,0,0]
	v_mfma_scale_f32_16x16x128_f8f6f4 v[104:107], v[24:31], v[56:63], v[104:107], v198, v198 op_sel_hi:[0,0,0]
	v_mfma_scale_f32_16x16x128_f8f6f4 v[100:103], v[16:23], v[56:63], v[100:103], v198, v198 op_sel_hi:[0,0,0]
	v_mfma_scale_f32_16x16x128_f8f6f4 v[96:99], v[8:15], v[32:39], v[96:99], v198, v198 op_sel_hi:[0,0,0]
	v_mfma_scale_f32_16x16x128_f8f6f4 v[92:95], v[0:7], v[32:39], v[92:95], v198, v198 op_sel_hi:[0,0,0]
	v_mfma_scale_f32_16x16x128_f8f6f4 v[88:91], v[8:15], v[40:47], v[88:91], v198, v198 op_sel_hi:[0,0,0]
	v_mfma_scale_f32_16x16x128_f8f6f4 v[84:87], v[0:7], v[40:47], v[84:87], v198, v198 op_sel_hi:[0,0,0]
	v_mfma_scale_f32_16x16x128_f8f6f4 v[80:83], v[8:15], v[48:55], v[80:83], v198, v198 op_sel_hi:[0,0,0]
	v_mfma_scale_f32_16x16x128_f8f6f4 v[76:79], v[0:7], v[48:55], v[76:79], v198, v198 op_sel_hi:[0,0,0]
	v_mfma_scale_f32_16x16x128_f8f6f4 v[72:75], v[8:15], v[56:63], v[72:75], v198, v198 op_sel_hi:[0,0,0]
	v_mfma_scale_f32_16x16x128_f8f6f4 v[68:71], v[0:7], v[56:63], v[68:71], v198, v198 op_sel_hi:[0,0,0]
	s_setprio 0
	s_barrier
	s_waitcnt vmcnt(16)
	v_mbcnt_lo_u32_b32 v0, -1, 0
	v_mbcnt_hi_u32_b32 v0, -1, v0
	s_add_i32 s33, s61, 0x200
	v_lshl_add_u32 v0, v0, 4, s40
	v_ashrrev_i32_e32 v1, 31, v0
	v_lshrrev_b32_e32 v1, 22, v1
	v_add_u32_e32 v1, v0, v1
	v_ashrrev_i32_e32 v1, 10, v1
	v_mul_i32_i24_e32 v2, 0x400, v1
	v_sub_u32_e32 v2, v0, v2
	v_lshrrev_b32_e32 v3, 4, v2
	v_bitop3_b32 v3, v3, v2, 32 bitop3:0x6c
	v_ashrrev_i32_e32 v2, 31, v2
	v_lshrrev_b32_e32 v2, 26, v2
	v_add_u32_e32 v2, v3, v2
	v_and_b32_e32 v2, 0xc0, v2
	v_add_u32_e32 v0, 0x2000, v0
	v_sub_u32_e32 v2, v3, v2
	v_ashrrev_i32_e32 v3, 31, v0
	v_lshrrev_b32_e32 v3, 22, v3
	v_add_u32_e32 v3, v0, v3
	v_ashrrev_i32_e32 v3, 10, v3
	v_mul_i32_i24_e32 v4, 0x400, v3
	v_sub_u32_e32 v0, v0, v4
	v_lshrrev_b32_e32 v4, 4, v0
	v_bitop3_b32 v4, v4, v0, 32 bitop3:0x6c
	v_ashrrev_i32_e32 v0, 31, v0
	v_lshrrev_b32_e32 v0, 26, v0
	v_add_u32_e32 v0, v4, v0
	v_and_b32_e32 v0, 0xffc0, v0
	v_sub_u32_e32 v0, v4, v0
	v_lshrrev_b16_e32 v4, 7, v0
	v_and_b32_e32 v4, 1, v4
	v_add_u16_e32 v0, v0, v4
	v_lshlrev_b32_e32 v1, 5, v1
	v_ashrrev_i16_sdwa v2, v199, sext(v2) dst_sel:DWORD dst_unused:UNUSED_PAD src0_sel:DWORD src1_sel:BYTE_0
	v_lshlrev_b32_e32 v3, 5, v3
	v_ashrrev_i16_sdwa v0, v199, sext(v0) dst_sel:DWORD dst_unused:UNUSED_PAD src0_sel:DWORD src1_sel:BYTE_0
	v_and_b32_e32 v1, 32, v1
	v_bfe_i32 v2, v2, 0, 16
	v_and_b32_e32 v3, 32, v3
	v_bfe_i32 v0, v0, 0, 16
	v_add_lshl_u32 v1, v1, v2, 1
	v_add_lshl_u32 v0, v3, v0, 1
	v_lshl_add_u32 v32, v220, 12, v1
	v_lshl_add_u32 v33, v217, 12, v0
	v_lshl_add_u32 v34, v218, 12, v1
	v_lshl_add_u32 v35, v219, 12, v0
	s_mov_b32 s37, 0
.LBB0_1330:
	s_add_i32 s61, s36, 0x80
	s_cmp_eq_u32 s37, 28
	s_cselect_b64 vcc, -1, 0
	ds_read_b128 v[16:19], v202 offset:0
	ds_read_b128 v[20:23], v202 offset:0x400
	ds_read_b128 v[24:27], v202 offset:0x800
	ds_read_b128 v[28:31], v202 offset:0xc00
	ds_read_b128 v[36:39], v201 offset:0
	ds_read_b128 v[40:43], v201 offset:0x400
	ds_read_b128 v[44:47], v201 offset:0x800
	ds_read_b128 v[48:51], v201 offset:0xc00
	ds_read_b128 v[52:55], v201 offset:0x1000
	ds_read_b128 v[56:59], v201 offset:0x1400
	ds_read_b128 v[218:221], v201 offset:0x1800
	ds_read_b128 v[222:225], v201 offset:0x1c00
	ds_read_b128 v[8:11], v202 offset:0x4000
	ds_read_b128 v[12:15], v202 offset:0x4400
	ds_read_b128 v[0:3], v202 offset:0x4800
	ds_read_b128 v[4:7], v202 offset:0x4c00
	s_and_b64 s[66:67], vcc, exec
	s_cselect_b32 s67, s85, s61
	s_cselect_b32 s66, s86, s33
	s_add_i32 s61, s67, 0x80
	s_mov_b32 m0, s73
	s_nop 0
	buffer_load_dwordx4 v207, s[4:7], s36 offen lds
	s_mov_b32 m0, s74
	s_nop 0
	buffer_load_dwordx4 v206, s[4:7], s36 offen lds
	s_waitcnt vmcnt(8)
	s_waitcnt lgkmcnt(4)
	s_barrier
	s_setprio 1
	v_mfma_scale_f32_16x16x128_f8f6f4 v[192:195], v[16:23], v[36:43], v[192:195], v198, v198 op_sel_hi:[0,0,0]
	v_mfma_scale_f32_16x16x128_f8f6f4 v[188:191], v[24:31], v[36:43], v[188:191], v198, v198 op_sel_hi:[0,0,0]
	v_mfma_scale_f32_16x16x128_f8f6f4 v[184:187], v[16:23], v[44:51], v[184:187], v198, v198 op_sel_hi:[0,0,0]
	v_mfma_scale_f32_16x16x128_f8f6f4 v[180:183], v[24:31], v[44:51], v[180:183], v198, v198 op_sel_hi:[0,0,0]
	v_mfma_scale_f32_16x16x128_f8f6f4 v[176:179], v[16:23], v[52:59], v[176:179], v198, v198 op_sel_hi:[0,0,0]
	v_mfma_scale_f32_16x16x128_f8f6f4 v[172:175], v[24:31], v[52:59], v[172:175], v198, v198 op_sel_hi:[0,0,0]
	v_mfma_scale_f32_16x16x128_f8f6f4 v[168:171], v[16:23], v[218:225], v[168:171], v198, v198 op_sel_hi:[0,0,0]
	v_mfma_scale_f32_16x16x128_f8f6f4 v[164:167], v[24:31], v[218:225], v[164:167], v198, v198 op_sel_hi:[0,0,0]
	s_waitcnt lgkmcnt(2)
	v_mfma_scale_f32_16x16x128_f8f6f4 v[160:163], v[8:15], v[36:43], v[160:163], v198, v198 op_sel_hi:[0,0,0]
	s_waitcnt lgkmcnt(0)
	v_mfma_scale_f32_16x16x128_f8f6f4 v[156:159], v[0:7], v[36:43], v[156:159], v198, v198 op_sel_hi:[0,0,0]
	v_mfma_scale_f32_16x16x128_f8f6f4 v[152:155], v[8:15], v[44:51], v[152:155], v198, v198 op_sel_hi:[0,0,0]
	v_mfma_scale_f32_16x16x128_f8f6f4 v[148:151], v[0:7], v[44:51], v[148:151], v198, v198 op_sel_hi:[0,0,0]
	v_mfma_scale_f32_16x16x128_f8f6f4 v[144:147], v[8:15], v[52:59], v[144:147], v198, v198 op_sel_hi:[0,0,0]
	v_mfma_scale_f32_16x16x128_f8f6f4 v[140:143], v[0:7], v[52:59], v[140:143], v198, v198 op_sel_hi:[0,0,0]
	v_mfma_scale_f32_16x16x128_f8f6f4 v[136:139], v[8:15], v[218:225], v[136:139], v198, v198 op_sel_hi:[0,0,0]
	v_mfma_scale_f32_16x16x128_f8f6f4 v[132:135], v[0:7], v[218:225], v[132:135], v198, v198 op_sel_hi:[0,0,0]
	s_setprio 0
	s_barrier
	ds_read_b128 v[36:39], v201 offset:0x4000
	ds_read_b128 v[40:43], v201 offset:0x4400
	ds_read_b128 v[44:47], v201 offset:0x4800
	ds_read_b128 v[48:51], v201 offset:0x4c00
	ds_read_b128 v[52:55], v201 offset:0x5000
	ds_read_b128 v[56:59], v201 offset:0x5400
	ds_read_b128 v[218:221], v201 offset:0x5800
	ds_read_b128 v[222:225], v201 offset:0x5c00
	s_mov_b32 m0, s45
	s_nop 0
	buffer_load_dwordx4 v200, s[8:11], s66 offen lds
	s_add_i32 s89, s66, 0x80000
	s_mov_b32 m0, s46
	v_cndmask_b32_e32 v60, v205, v32, vcc
	buffer_load_dwordx4 v200, s[8:11], s89 offen lds
	s_add_i32 s89, s66, 0x8000
	s_mov_b32 m0, s47
	v_cndmask_b32_e32 v61, v208, v33, vcc
	buffer_load_dwordx4 v200, s[8:11], s89 offen lds
	s_add_i32 s89, s66, 0x88000
	s_mov_b32 m0, s48
	s_nop 0
	buffer_load_dwordx4 v200, s[8:11], s89 offen lds
	s_mov_b32 m0, s44
	s_nop 0
	buffer_load_dwordx4 v60, s[4:7], s67 offen lds
	s_mov_b32 m0, s49
	s_nop 0
	buffer_load_dwordx4 v61, s[4:7], s67 offen lds
	s_waitcnt vmcnt(8)
	s_waitcnt lgkmcnt(0)
	s_barrier
	s_setprio 1
	v_mfma_scale_f32_16x16x128_f8f6f4 v[128:131], v[16:23], v[36:43], v[128:131], v198, v198 op_sel_hi:[0,0,0]
	v_mfma_scale_f32_16x16x128_f8f6f4 v[124:127], v[24:31], v[36:43], v[124:127], v198, v198 op_sel_hi:[0,0,0]
	v_mfma_scale_f32_16x16x128_f8f6f4 v[120:123], v[16:23], v[44:51], v[120:123], v198, v198 op_sel_hi:[0,0,0]
	v_mfma_scale_f32_16x16x128_f8f6f4 v[116:119], v[24:31], v[44:51], v[116:119], v198, v198 op_sel_hi:[0,0,0]
	v_mfma_scale_f32_16x16x128_f8f6f4 v[112:115], v[16:23], v[52:59], v[112:115], v198, v198 op_sel_hi:[0,0,0]
	v_mfma_scale_f32_16x16x128_f8f6f4 v[108:111], v[24:31], v[52:59], v[108:111], v198, v198 op_sel_hi:[0,0,0]
	v_mfma_scale_f32_16x16x128_f8f6f4 v[104:107], v[16:23], v[218:225], v[104:107], v198, v198 op_sel_hi:[0,0,0]
	v_mfma_scale_f32_16x16x128_f8f6f4 v[100:103], v[24:31], v[218:225], v[100:103], v198, v198 op_sel_hi:[0,0,0]
	v_mfma_scale_f32_16x16x128_f8f6f4 v[96:99], v[8:15], v[36:43], v[96:99], v198, v198 op_sel_hi:[0,0,0]
	v_mfma_scale_f32_16x16x128_f8f6f4 v[92:95], v[0:7], v[36:43], v[92:95], v198, v198 op_sel_hi:[0,0,0]
	v_mfma_scale_f32_16x16x128_f8f6f4 v[88:91], v[8:15], v[44:51], v[88:91], v198, v198 op_sel_hi:[0,0,0]
	v_mfma_scale_f32_16x16x128_f8f6f4 v[84:87], v[0:7], v[44:51], v[84:87], v198, v198 op_sel_hi:[0,0,0]
	v_mfma_scale_f32_16x16x128_f8f6f4 v[80:83], v[8:15], v[52:59], v[80:83], v198, v198 op_sel_hi:[0,0,0]
	v_mfma_scale_f32_16x16x128_f8f6f4 v[76:79], v[0:7], v[52:59], v[76:79], v198, v198 op_sel_hi:[0,0,0]
	v_mfma_scale_f32_16x16x128_f8f6f4 v[72:75], v[8:15], v[218:225], v[72:75], v198, v198 op_sel_hi:[0,0,0]
	v_mfma_scale_f32_16x16x128_f8f6f4 v[68:71], v[0:7], v[218:225], v[68:71], v198, v198 op_sel_hi:[0,0,0]
	s_setprio 0
	s_barrier
	ds_read_b128 v[24:27], v202 offset:0x8000
	ds_read_b128 v[28:31], v202 offset:0x8400
	ds_read_b128 v[16:19], v202 offset:0x8800
	ds_read_b128 v[20:23], v202 offset:0x8c00
	ds_read_b128 v[36:39], v201 offset:0x8000
	ds_read_b128 v[40:43], v201 offset:0x8400
	ds_read_b128 v[44:47], v201 offset:0x8800
	ds_read_b128 v[48:51], v201 offset:0x8c00
	ds_read_b128 v[52:55], v201 offset:0x9000
	ds_read_b128 v[56:59], v201 offset:0x9400
	ds_read_b128 v[218:221], v201 offset:0x9800
	ds_read_b128 v[222:225], v201 offset:0x9c00
	ds_read_b128 v[8:11], v202 offset:0xc000
	ds_read_b128 v[12:15], v202 offset:0xc400
	ds_read_b128 v[0:3], v202 offset:0xc800
	ds_read_b128 v[4:7], v202 offset:0xcc00
	s_mov_b32 m0, s50
	v_cndmask_b32_e32 v62, v207, v34, vcc
	buffer_load_dwordx4 v62, s[4:7], s67 offen lds
	v_cndmask_b32_e32 v62, v206, v35, vcc
	s_mov_b32 m0, s51
	s_nop 0
	buffer_load_dwordx4 v62, s[4:7], s67 offen lds
	s_waitcnt vmcnt(8)
	s_waitcnt lgkmcnt(4)
	s_barrier
	s_setprio 1
	v_mfma_scale_f32_16x16x128_f8f6f4 v[192:195], v[24:31], v[36:43], v[192:195], v198, v198 op_sel_hi:[0,0,0]
	v_mfma_scale_f32_16x16x128_f8f6f4 v[188:191], v[16:23], v[36:43], v[188:191], v198, v198 op_sel_hi:[0,0,0]
	v_mfma_scale_f32_16x16x128_f8f6f4 v[184:187], v[24:31], v[44:51], v[184:187], v198, v198 op_sel_hi:[0,0,0]
	v_mfma_scale_f32_16x16x128_f8f6f4 v[180:183], v[16:23], v[44:51], v[180:183], v198, v198 op_sel_hi:[0,0,0]
	v_mfma_scale_f32_16x16x128_f8f6f4 v[176:179], v[24:31], v[52:59], v[176:179], v198, v198 op_sel_hi:[0,0,0]
	v_mfma_scale_f32_16x16x128_f8f6f4 v[172:175], v[16:23], v[52:59], v[172:175], v198, v198 op_sel_hi:[0,0,0]
	v_mfma_scale_f32_16x16x128_f8f6f4 v[168:171], v[24:31], v[218:225], v[168:171], v198, v198 op_sel_hi:[0,0,0]
	v_mfma_scale_f32_16x16x128_f8f6f4 v[164:167], v[16:23], v[218:225], v[164:167], v198, v198 op_sel_hi:[0,0,0]
	s_waitcnt lgkmcnt(2)
	v_mfma_scale_f32_16x16x128_f8f6f4 v[160:163], v[8:15], v[36:43], v[160:163], v198, v198 op_sel_hi:[0,0,0]
	s_waitcnt lgkmcnt(0)
	v_mfma_scale_f32_16x16x128_f8f6f4 v[156:159], v[0:7], v[36:43], v[156:159], v198, v198 op_sel_hi:[0,0,0]
	v_mfma_scale_f32_16x16x128_f8f6f4 v[152:155], v[8:15], v[44:51], v[152:155], v198, v198 op_sel_hi:[0,0,0]
	v_mfma_scale_f32_16x16x128_f8f6f4 v[148:151], v[0:7], v[44:51], v[148:151], v198, v198 op_sel_hi:[0,0,0]
	v_mfma_scale_f32_16x16x128_f8f6f4 v[144:147], v[8:15], v[52:59], v[144:147], v198, v198 op_sel_hi:[0,0,0]
	v_mfma_scale_f32_16x16x128_f8f6f4 v[140:143], v[0:7], v[52:59], v[140:143], v198, v198 op_sel_hi:[0,0,0]
	v_mfma_scale_f32_16x16x128_f8f6f4 v[136:139], v[8:15], v[218:225], v[136:139], v198, v198 op_sel_hi:[0,0,0]
	v_mfma_scale_f32_16x16x128_f8f6f4 v[132:135], v[0:7], v[218:225], v[132:135], v198, v198 op_sel_hi:[0,0,0]
	s_setprio 0
	s_barrier
	ds_read_b128 v[36:39], v201 offset:0xc000
	ds_read_b128 v[40:43], v201 offset:0xc400
	ds_read_b128 v[44:47], v201 offset:0xc800
	ds_read_b128 v[48:51], v201 offset:0xcc00
	ds_read_b128 v[52:55], v201 offset:0xd000
	ds_read_b128 v[56:59], v201 offset:0xd400
	ds_read_b128 v[218:221], v201 offset:0xd800
	ds_read_b128 v[222:225], v201 offset:0xdc00
	s_mov_b32 m0, s64
	s_add_i32 s67, s66, 0x80
	buffer_load_dwordx4 v200, s[8:11], s67 offen lds
	s_add_i32 s67, s66, 0x80080
	s_mov_b32 m0, s65
	s_nop 0
	buffer_load_dwordx4 v200, s[8:11], s67 offen lds
	s_add_i32 s67, s66, 0x8080
	s_mov_b32 m0, s70
	s_add_i32 s66, s66, 0x88080
	buffer_load_dwordx4 v200, s[8:11], s67 offen lds
	s_mov_b32 m0, s71
	s_nop 0
	buffer_load_dwordx4 v200, s[8:11], s66 offen lds
	s_mov_b32 m0, s68
	s_nop 0
	buffer_load_dwordx4 v60, s[4:7], s61 offen lds
	s_mov_b32 m0, s69
	s_nop 0
	buffer_load_dwordx4 v61, s[4:7], s61 offen lds
	s_waitcnt vmcnt(8)
	s_waitcnt lgkmcnt(0)
	s_barrier
	s_setprio 1
	v_mfma_scale_f32_16x16x128_f8f6f4 v[128:131], v[24:31], v[36:43], v[128:131], v198, v198 op_sel_hi:[0,0,0]
	v_mfma_scale_f32_16x16x128_f8f6f4 v[124:127], v[16:23], v[36:43], v[124:127], v198, v198 op_sel_hi:[0,0,0]
	v_mfma_scale_f32_16x16x128_f8f6f4 v[120:123], v[24:31], v[44:51], v[120:123], v198, v198 op_sel_hi:[0,0,0]
	v_mfma_scale_f32_16x16x128_f8f6f4 v[116:119], v[16:23], v[44:51], v[116:119], v198, v198 op_sel_hi:[0,0,0]
	v_mfma_scale_f32_16x16x128_f8f6f4 v[112:115], v[24:31], v[52:59], v[112:115], v198, v198 op_sel_hi:[0,0,0]
	v_mfma_scale_f32_16x16x128_f8f6f4 v[108:111], v[16:23], v[52:59], v[108:111], v198, v198 op_sel_hi:[0,0,0]
	v_mfma_scale_f32_16x16x128_f8f6f4 v[104:107], v[24:31], v[218:225], v[104:107], v198, v198 op_sel_hi:[0,0,0]
	v_mfma_scale_f32_16x16x128_f8f6f4 v[100:103], v[16:23], v[218:225], v[100:103], v198, v198 op_sel_hi:[0,0,0]
	v_mfma_scale_f32_16x16x128_f8f6f4 v[96:99], v[8:15], v[36:43], v[96:99], v198, v198 op_sel_hi:[0,0,0]
	v_mfma_scale_f32_16x16x128_f8f6f4 v[92:95], v[0:7], v[36:43], v[92:95], v198, v198 op_sel_hi:[0,0,0]
	v_mfma_scale_f32_16x16x128_f8f6f4 v[88:91], v[8:15], v[44:51], v[88:91], v198, v198 op_sel_hi:[0,0,0]
	v_mfma_scale_f32_16x16x128_f8f6f4 v[84:87], v[0:7], v[44:51], v[84:87], v198, v198 op_sel_hi:[0,0,0]
	v_mfma_scale_f32_16x16x128_f8f6f4 v[80:83], v[8:15], v[52:59], v[80:83], v198, v198 op_sel_hi:[0,0,0]
	v_mfma_scale_f32_16x16x128_f8f6f4 v[76:79], v[0:7], v[52:59], v[76:79], v198, v198 op_sel_hi:[0,0,0]
	v_mfma_scale_f32_16x16x128_f8f6f4 v[72:75], v[8:15], v[218:225], v[72:75], v198, v198 op_sel_hi:[0,0,0]
	v_mfma_scale_f32_16x16x128_f8f6f4 v[68:71], v[0:7], v[218:225], v[68:71], v198, v198 op_sel_hi:[0,0,0]
	s_setprio 0
	s_barrier
	s_add_i32 s37, s37, 2
	s_addk_i32 s36, 0x100
	s_addk_i32 s33, 0x100
	s_cmp_gt_u32 s37, 29
	s_cbranch_scc0 .LBB0_1330
	s_and_b64 vcc, exec, s[28:29]
	s_cbranch_vccz .LBB0_1333
	s_barrier

.LBB0_1366:
	s_add_i32 s33, s88, 0x100
	s_add_i32 s66, s89, 0x100
	s_waitcnt lgkmcnt(0)
	s_barrier
	s_setprio 1
	v_mfma_scale_f32_16x16x128_f8f6f4 v[192:195], v[24:31], v[56:63], 0, v235, v235 op_sel_hi:[0,0,0]
	v_mfma_scale_f32_16x16x128_f8f6f4 v[188:191], v[16:23], v[56:63], 0, v235, v235 op_sel_hi:[0,0,0]
	v_mfma_scale_f32_16x16x128_f8f6f4 v[184:187], v[24:31], v[48:55], 0, v235, v235 op_sel_hi:[0,0,0]
	v_mfma_scale_f32_16x16x128_f8f6f4 v[180:183], v[16:23], v[48:55], 0, v235, v235 op_sel_hi:[0,0,0]
	v_mfma_scale_f32_16x16x128_f8f6f4 v[176:179], v[24:31], v[40:47], 0, v235, v235 op_sel_hi:[0,0,0]
	v_mfma_scale_f32_16x16x128_f8f6f4 v[172:175], v[16:23], v[40:47], 0, v235, v235 op_sel_hi:[0,0,0]
	v_mfma_scale_f32_16x16x128_f8f6f4 v[168:171], v[24:31], v[32:39], 0, v235, v235 op_sel_hi:[0,0,0]
	v_mfma_scale_f32_16x16x128_f8f6f4 v[164:167], v[16:23], v[32:39], 0, v235, v235 op_sel_hi:[0,0,0]
	v_mfma_scale_f32_16x16x128_f8f6f4 v[160:163], v[8:15], v[56:63], 0, v235, v235 op_sel_hi:[0,0,0]
	v_mfma_scale_f32_16x16x128_f8f6f4 v[156:159], v[0:7], v[56:63], 0, v235, v235 op_sel_hi:[0,0,0]
	v_mfma_scale_f32_16x16x128_f8f6f4 v[152:155], v[8:15], v[48:55], 0, v235, v235 op_sel_hi:[0,0,0]
	v_mfma_scale_f32_16x16x128_f8f6f4 v[148:151], v[0:7], v[48:55], 0, v235, v235 op_sel_hi:[0,0,0]
	v_mfma_scale_f32_16x16x128_f8f6f4 v[144:147], v[8:15], v[40:47], 0, v235, v235 op_sel_hi:[0,0,0]
	v_mfma_scale_f32_16x16x128_f8f6f4 v[140:143], v[0:7], v[40:47], 0, v235, v235 op_sel_hi:[0,0,0]
	v_mfma_scale_f32_16x16x128_f8f6f4 v[136:139], v[8:15], v[32:39], 0, v235, v235 op_sel_hi:[0,0,0]
	v_mfma_scale_f32_16x16x128_f8f6f4 v[132:135], v[0:7], v[32:39], 0, v235, v235 op_sel_hi:[0,0,0]
	s_setprio 0
	s_barrier
	s_mov_b32 m0, s46
	s_mov_b32 s10, s6
	s_mov_b32 s11, s7
	ds_read_b128 v[56:59], v232 offset:0x4000
	ds_read_b128 v[60:63], v232 offset:0x4400
	ds_read_b128 v[48:51], v232 offset:0x4800
	ds_read_b128 v[52:55], v232 offset:0x4c00
	ds_read_b128 v[40:43], v232 offset:0x5000
	ds_read_b128 v[44:47], v232 offset:0x5400
	ds_read_b128 v[32:35], v232 offset:0x5800
	ds_read_b128 v[36:39], v232 offset:0x5c00
	buffer_load_dwordx4 v231, s[8:11], s66 offen lds
	s_add_i32 s66, s89, 0x10100
	s_mov_b32 m0, s47
	s_and_b64 vcc, exec, s[40:41]
	buffer_load_dwordx4 v231, s[8:11], s66 offen lds
	s_add_i32 s66, s89, 0x1100
	s_mov_b32 m0, s49
	s_nop 0
	buffer_load_dwordx4 v231, s[8:11], s66 offen lds
	s_add_i32 s66, s89, 0x11100
	s_mov_b32 m0, s50
	s_nop 0
	buffer_load_dwordx4 v231, s[8:11], s66 offen lds
	s_mov_b32 m0, s48
	s_add_i32 s10, s88, 0x8100
	buffer_load_dwordx4 v230, s[4:7], s33 offen lds
	s_mov_b32 m0, s51
	s_nop 0
	buffer_load_dwordx4 v230, s[4:7], s10 offen lds
	s_cbranch_vccz .LBB0_1375
	s_waitcnt vmcnt(37)
	s_cbranch_execnz .LBB0_1369

.LBB0_1369:
	s_add_i32 s33, s88, 0x180
	s_add_i32 s40, s89, 0x180
	s_waitcnt lgkmcnt(0)
	s_barrier
	s_setprio 1
	v_mfma_scale_f32_16x16x128_f8f6f4 v[128:131], v[24:31], v[56:63], 0, v235, v235 op_sel_hi:[0,0,0]
	v_mfma_scale_f32_16x16x128_f8f6f4 v[124:127], v[16:23], v[56:63], 0, v235, v235 op_sel_hi:[0,0,0]
	v_mfma_scale_f32_16x16x128_f8f6f4 v[120:123], v[24:31], v[48:55], 0, v235, v235 op_sel_hi:[0,0,0]
	v_mfma_scale_f32_16x16x128_f8f6f4 v[116:119], v[16:23], v[48:55], 0, v235, v235 op_sel_hi:[0,0,0]
	v_mfma_scale_f32_16x16x128_f8f6f4 v[112:115], v[24:31], v[40:47], 0, v235, v235 op_sel_hi:[0,0,0]
	v_mfma_scale_f32_16x16x128_f8f6f4 v[108:111], v[16:23], v[40:47], 0, v235, v235 op_sel_hi:[0,0,0]
	v_mfma_scale_f32_16x16x128_f8f6f4 v[104:107], v[24:31], v[32:39], 0, v235, v235 op_sel_hi:[0,0,0]
	v_mfma_scale_f32_16x16x128_f8f6f4 v[100:103], v[16:23], v[32:39], 0, v235, v235 op_sel_hi:[0,0,0]
	v_mfma_scale_f32_16x16x128_f8f6f4 v[96:99], v[8:15], v[56:63], 0, v235, v235 op_sel_hi:[0,0,0]
	v_mfma_scale_f32_16x16x128_f8f6f4 v[92:95], v[0:7], v[56:63], 0, v235, v235 op_sel_hi:[0,0,0]
	v_mfma_scale_f32_16x16x128_f8f6f4 v[88:91], v[8:15], v[48:55], 0, v235, v235 op_sel_hi:[0,0,0]
	v_mfma_scale_f32_16x16x128_f8f6f4 v[84:87], v[0:7], v[48:55], 0, v235, v235 op_sel_hi:[0,0,0]
	v_mfma_scale_f32_16x16x128_f8f6f4 v[80:83], v[8:15], v[40:47], 0, v235, v235 op_sel_hi:[0,0,0]
	v_mfma_scale_f32_16x16x128_f8f6f4 v[76:79], v[0:7], v[40:47], 0, v235, v235 op_sel_hi:[0,0,0]
	v_mfma_scale_f32_16x16x128_f8f6f4 v[72:75], v[8:15], v[32:39], 0, v235, v235 op_sel_hi:[0,0,0]
	v_mfma_scale_f32_16x16x128_f8f6f4 v[68:71], v[0:7], v[32:39], 0, v235, v235 op_sel_hi:[0,0,0]
	s_setprio 0
	s_barrier
	ds_read_b128 v[16:19], v233 offset:0x8000
	ds_read_b128 v[20:23], v233 offset:0x8400
	ds_read_b128 v[24:27], v233 offset:0x8800
	ds_read_b128 v[28:31], v233 offset:0x8c00
	ds_read_b128 v[32:35], v232 offset:0x8000
	ds_read_b128 v[36:39], v232 offset:0x8400
	ds_read_b128 v[40:43], v232 offset:0x8800
	ds_read_b128 v[44:47], v232 offset:0x8c00
	ds_read_b128 v[48:51], v232 offset:0x9000
	ds_read_b128 v[52:55], v232 offset:0x9400
	ds_read_b128 v[56:59], v232 offset:0x9800
	ds_read_b128 v[60:63], v232 offset:0x9c00
	ds_read_b128 v[8:11], v233 offset:0xc000
	ds_read_b128 v[12:15], v233 offset:0xc400
	ds_read_b128 v[0:3], v233 offset:0xc800
	ds_read_b128 v[4:7], v233 offset:0xcc00
	s_mov_b32 m0, s62
	s_add_i32 s10, s88, 0x10100
	buffer_load_dwordx4 v230, s[4:7], s10 offen lds
	s_add_i32 s10, s88, 0x18100
	s_mov_b32 m0, s63
	s_nop 0
	buffer_load_dwordx4 v230, s[4:7], s10 offen lds
	s_waitcnt vmcnt(8)
	s_waitcnt lgkmcnt(4)
	s_barrier
	s_setprio 1
	v_mfma_scale_f32_16x16x128_f8f6f4 v[192:195], v[16:23], v[32:39], v[192:195], v235, v235 op_sel_hi:[0,0,0]
	v_mfma_scale_f32_16x16x128_f8f6f4 v[188:191], v[24:31], v[32:39], v[188:191], v235, v235 op_sel_hi:[0,0,0]
	v_mfma_scale_f32_16x16x128_f8f6f4 v[184:187], v[16:23], v[40:47], v[184:187], v235, v235 op_sel_hi:[0,0,0]
	v_mfma_scale_f32_16x16x128_f8f6f4 v[180:183], v[24:31], v[40:47], v[180:183], v235, v235 op_sel_hi:[0,0,0]
	v_mfma_scale_f32_16x16x128_f8f6f4 v[176:179], v[16:23], v[48:55], v[176:179], v235, v235 op_sel_hi:[0,0,0]
	v_mfma_scale_f32_16x16x128_f8f6f4 v[172:175], v[24:31], v[48:55], v[172:175], v235, v235 op_sel_hi:[0,0,0]
	v_mfma_scale_f32_16x16x128_f8f6f4 v[168:171], v[16:23], v[56:63], v[168:171], v235, v235 op_sel_hi:[0,0,0]
	v_mfma_scale_f32_16x16x128_f8f6f4 v[164:167], v[24:31], v[56:63], v[164:167], v235, v235 op_sel_hi:[0,0,0]
	s_waitcnt lgkmcnt(2)
	v_mfma_scale_f32_16x16x128_f8f6f4 v[160:163], v[8:15], v[32:39], v[160:163], v235, v235 op_sel_hi:[0,0,0]
	s_waitcnt lgkmcnt(0)
	v_mfma_scale_f32_16x16x128_f8f6f4 v[156:159], v[0:7], v[32:39], v[156:159], v235, v235 op_sel_hi:[0,0,0]
	v_mfma_scale_f32_16x16x128_f8f6f4 v[152:155], v[8:15], v[40:47], v[152:155], v235, v235 op_sel_hi:[0,0,0]
	v_mfma_scale_f32_16x16x128_f8f6f4 v[148:151], v[0:7], v[40:47], v[148:151], v235, v235 op_sel_hi:[0,0,0]
	v_mfma_scale_f32_16x16x128_f8f6f4 v[144:147], v[8:15], v[48:55], v[144:147], v235, v235 op_sel_hi:[0,0,0]
	v_mfma_scale_f32_16x16x128_f8f6f4 v[140:143], v[0:7], v[48:55], v[140:143], v235, v235 op_sel_hi:[0,0,0]
	v_mfma_scale_f32_16x16x128_f8f6f4 v[136:139], v[8:15], v[56:63], v[136:139], v235, v235 op_sel_hi:[0,0,0]
	v_mfma_scale_f32_16x16x128_f8f6f4 v[132:135], v[0:7], v[56:63], v[132:135], v235, v235 op_sel_hi:[0,0,0]
	s_setprio 0
	s_barrier
	ds_read_b128 v[32:35], v232 offset:0xc000
	ds_read_b128 v[36:39], v232 offset:0xc400
	ds_read_b128 v[40:43], v232 offset:0xc800
	ds_read_b128 v[44:47], v232 offset:0xcc00
	ds_read_b128 v[48:51], v232 offset:0xd000
	ds_read_b128 v[52:55], v232 offset:0xd400
	ds_read_b128 v[56:59], v232 offset:0xd800
	ds_read_b128 v[60:63], v232 offset:0xdc00
	s_mov_b32 m0, s64
	s_mov_b32 s10, s6
	s_mov_b32 s11, s7
	buffer_load_dwordx4 v231, s[8:11], s40 offen lds
	s_add_i32 s40, s89, 0x10180
	s_mov_b32 m0, s65
	s_nop 0
	buffer_load_dwordx4 v231, s[8:11], s40 offen lds
	s_add_i32 s40, s89, 0x1180
	s_mov_b32 m0, s70
	s_nop 0
	buffer_load_dwordx4 v231, s[8:11], s40 offen lds
	s_add_i32 s40, s89, 0x11180
	s_mov_b32 m0, s71
	s_nop 0
	buffer_load_dwordx4 v231, s[8:11], s40 offen lds
	s_mov_b32 m0, s68
	s_nop 0
	buffer_load_dwordx4 v230, s[4:7], s33 offen lds
	s_add_i32 s33, s88, 0x8180
	s_mov_b32 m0, s69
	s_nop 0
	buffer_load_dwordx4 v230, s[4:7], s33 offen lds
	s_waitcnt vmcnt(8)
	s_waitcnt lgkmcnt(0)
	s_barrier
	s_setprio 1
	v_mfma_scale_f32_16x16x128_f8f6f4 v[128:131], v[16:23], v[32:39], v[128:131], v235, v235 op_sel_hi:[0,0,0]
	v_mfma_scale_f32_16x16x128_f8f6f4 v[124:127], v[24:31], v[32:39], v[124:127], v235, v235 op_sel_hi:[0,0,0]
	v_mfma_scale_f32_16x16x128_f8f6f4 v[120:123], v[16:23], v[40:47], v[120:123], v235, v235 op_sel_hi:[0,0,0]
	v_mfma_scale_f32_16x16x128_f8f6f4 v[116:119], v[24:31], v[40:47], v[116:119], v235, v235 op_sel_hi:[0,0,0]
	v_mfma_scale_f32_16x16x128_f8f6f4 v[112:115], v[16:23], v[48:55], v[112:115], v235, v235 op_sel_hi:[0,0,0]
	v_mfma_scale_f32_16x16x128_f8f6f4 v[108:111], v[24:31], v[48:55], v[108:111], v235, v235 op_sel_hi:[0,0,0]
	v_mfma_scale_f32_16x16x128_f8f6f4 v[104:107], v[16:23], v[56:63], v[104:107], v235, v235 op_sel_hi:[0,0,0]
	v_mfma_scale_f32_16x16x128_f8f6f4 v[100:103], v[24:31], v[56:63], v[100:103], v235, v235 op_sel_hi:[0,0,0]
	v_mfma_scale_f32_16x16x128_f8f6f4 v[96:99], v[8:15], v[32:39], v[96:99], v235, v235 op_sel_hi:[0,0,0]
	v_mfma_scale_f32_16x16x128_f8f6f4 v[92:95], v[0:7], v[32:39], v[92:95], v235, v235 op_sel_hi:[0,0,0]
	v_mfma_scale_f32_16x16x128_f8f6f4 v[88:91], v[8:15], v[40:47], v[88:91], v235, v235 op_sel_hi:[0,0,0]
	v_mfma_scale_f32_16x16x128_f8f6f4 v[84:87], v[0:7], v[40:47], v[84:87], v235, v235 op_sel_hi:[0,0,0]
	v_mfma_scale_f32_16x16x128_f8f6f4 v[80:83], v[8:15], v[48:55], v[80:83], v235, v235 op_sel_hi:[0,0,0]
	v_mfma_scale_f32_16x16x128_f8f6f4 v[76:79], v[0:7], v[48:55], v[76:79], v235, v235 op_sel_hi:[0,0,0]
	v_mfma_scale_f32_16x16x128_f8f6f4 v[72:75], v[8:15], v[56:63], v[72:75], v235, v235 op_sel_hi:[0,0,0]
	v_mfma_scale_f32_16x16x128_f8f6f4 v[68:71], v[0:7], v[56:63], v[68:71], v235, v235 op_sel_hi:[0,0,0]
	s_setprio 0
	s_barrier
	ds_read_b128 v[16:19], v233 offset:0
	ds_read_b128 v[20:23], v233 offset:0x400
	ds_read_b128 v[24:27], v233 offset:0x800
	ds_read_b128 v[28:31], v233 offset:0xc00
	ds_read_b128 v[32:35], v232 offset:0
	ds_read_b128 v[36:39], v232 offset:0x400
	ds_read_b128 v[40:43], v232 offset:0x800
	ds_read_b128 v[44:47], v232 offset:0xc00
	ds_read_b128 v[48:51], v232 offset:0x1000
	ds_read_b128 v[52:55], v232 offset:0x1400
	ds_read_b128 v[56:59], v232 offset:0x1800
	ds_read_b128 v[60:63], v232 offset:0x1c00
	ds_read_b128 v[8:11], v233 offset:0x4000
	ds_read_b128 v[12:15], v233 offset:0x4400
	ds_read_b128 v[0:3], v233 offset:0x4800
	ds_read_b128 v[4:7], v233 offset:0x4c00
	s_add_i32 s33, s85, 0x80
	s_mov_b32 m0, s74
	s_add_i32 s40, s88, 0x10180
	buffer_load_dwordx4 v230, s[4:7], s40 offen lds
	s_add_i32 s40, s88, 0x18180
	s_mov_b32 m0, s76
	s_nop 0
	buffer_load_dwordx4 v230, s[4:7], s40 offen lds
	s_waitcnt vmcnt(8)
	s_waitcnt lgkmcnt(4)
	s_barrier
	s_setprio 1
	v_mfma_scale_f32_16x16x128_f8f6f4 v[192:195], v[16:23], v[32:39], v[192:195], v235, v235 op_sel_hi:[0,0,0]
	v_mfma_scale_f32_16x16x128_f8f6f4 v[188:191], v[24:31], v[32:39], v[188:191], v235, v235 op_sel_hi:[0,0,0]
	v_mfma_scale_f32_16x16x128_f8f6f4 v[184:187], v[16:23], v[40:47], v[184:187], v235, v235 op_sel_hi:[0,0,0]
	v_mfma_scale_f32_16x16x128_f8f6f4 v[180:183], v[24:31], v[40:47], v[180:183], v235, v235 op_sel_hi:[0,0,0]
	v_mfma_scale_f32_16x16x128_f8f6f4 v[176:179], v[16:23], v[48:55], v[176:179], v235, v235 op_sel_hi:[0,0,0]
	v_mfma_scale_f32_16x16x128_f8f6f4 v[172:175], v[24:31], v[48:55], v[172:175], v235, v235 op_sel_hi:[0,0,0]
	v_mfma_scale_f32_16x16x128_f8f6f4 v[168:171], v[16:23], v[56:63], v[168:171], v235, v235 op_sel_hi:[0,0,0]
	v_mfma_scale_f32_16x16x128_f8f6f4 v[164:167], v[24:31], v[56:63], v[164:167], v235, v235 op_sel_hi:[0,0,0]
	s_waitcnt lgkmcnt(2)
	v_mfma_scale_f32_16x16x128_f8f6f4 v[160:163], v[8:15], v[32:39], v[160:163], v235, v235 op_sel_hi:[0,0,0]
	s_waitcnt lgkmcnt(0)
	v_mfma_scale_f32_16x16x128_f8f6f4 v[156:159], v[0:7], v[32:39], v[156:159], v235, v235 op_sel_hi:[0,0,0]
	v_mfma_scale_f32_16x16x128_f8f6f4 v[152:155], v[8:15], v[40:47], v[152:155], v235, v235 op_sel_hi:[0,0,0]
	v_mfma_scale_f32_16x16x128_f8f6f4 v[148:151], v[0:7], v[40:47], v[148:151], v235, v235 op_sel_hi:[0,0,0]
	v_mfma_scale_f32_16x16x128_f8f6f4 v[144:147], v[8:15], v[48:55], v[144:147], v235, v235 op_sel_hi:[0,0,0]
	v_mfma_scale_f32_16x16x128_f8f6f4 v[140:143], v[0:7], v[48:55], v[140:143], v235, v235 op_sel_hi:[0,0,0]
	v_mfma_scale_f32_16x16x128_f8f6f4 v[136:139], v[8:15], v[56:63], v[136:139], v235, v235 op_sel_hi:[0,0,0]
	v_mfma_scale_f32_16x16x128_f8f6f4 v[132:135], v[0:7], v[56:63], v[132:135], v235, v235 op_sel_hi:[0,0,0]
	s_setprio 0
	s_barrier
	ds_read_b128 v[32:35], v232 offset:0x4000
	ds_read_b128 v[36:39], v232 offset:0x4400
	ds_read_b128 v[40:43], v232 offset:0x4800
	ds_read_b128 v[44:47], v232 offset:0x4c00
	ds_read_b128 v[48:51], v232 offset:0x5000
	ds_read_b128 v[52:55], v232 offset:0x5400
	ds_read_b128 v[56:59], v232 offset:0x5800
	ds_read_b128 v[60:63], v232 offset:0x5c00
	s_mov_b32 m0, s46
	s_nop 0
	buffer_load_dwordx4 v231, s[8:11], s86 offen lds
	s_add_i32 s40, s86, 0x10000
	s_mov_b32 m0, s47
	s_nop 0
	buffer_load_dwordx4 v231, s[8:11], s40 offen lds
	s_add_i32 s40, s86, 0x1000
	s_mov_b32 m0, s49
	s_nop 0
	buffer_load_dwordx4 v231, s[8:11], s40 offen lds
	s_add_i32 s40, s86, 0x11000
	s_mov_b32 m0, s50
	s_nop 0
	buffer_load_dwordx4 v231, s[8:11], s40 offen lds
	s_mov_b32 m0, s48
	s_add_i32 s40, s85, 0x8000
	buffer_load_dwordx4 v230, s[4:7], s85 offen lds
	s_mov_b32 m0, s51
	s_nop 0
	buffer_load_dwordx4 v230, s[4:7], s40 offen lds
	s_waitcnt vmcnt(8)
	s_waitcnt lgkmcnt(0)
	s_barrier
	s_setprio 1
	v_mfma_scale_f32_16x16x128_f8f6f4 v[128:131], v[16:23], v[32:39], v[128:131], v235, v235 op_sel_hi:[0,0,0]
	v_mfma_scale_f32_16x16x128_f8f6f4 v[124:127], v[24:31], v[32:39], v[124:127], v235, v235 op_sel_hi:[0,0,0]
	v_mfma_scale_f32_16x16x128_f8f6f4 v[120:123], v[16:23], v[40:47], v[120:123], v235, v235 op_sel_hi:[0,0,0]
	v_mfma_scale_f32_16x16x128_f8f6f4 v[116:119], v[24:31], v[40:47], v[116:119], v235, v235 op_sel_hi:[0,0,0]
	v_mfma_scale_f32_16x16x128_f8f6f4 v[112:115], v[16:23], v[48:55], v[112:115], v235, v235 op_sel_hi:[0,0,0]
	v_mfma_scale_f32_16x16x128_f8f6f4 v[108:111], v[24:31], v[48:55], v[108:111], v235, v235 op_sel_hi:[0,0,0]
	v_mfma_scale_f32_16x16x128_f8f6f4 v[104:107], v[16:23], v[56:63], v[104:107], v235, v235 op_sel_hi:[0,0,0]
	v_mfma_scale_f32_16x16x128_f8f6f4 v[100:103], v[24:31], v[56:63], v[100:103], v235, v235 op_sel_hi:[0,0,0]
	v_mfma_scale_f32_16x16x128_f8f6f4 v[96:99], v[8:15], v[32:39], v[96:99], v235, v235 op_sel_hi:[0,0,0]
	v_mfma_scale_f32_16x16x128_f8f6f4 v[92:95], v[0:7], v[32:39], v[92:95], v235, v235 op_sel_hi:[0,0,0]
	v_mfma_scale_f32_16x16x128_f8f6f4 v[88:91], v[8:15], v[40:47], v[88:91], v235, v235 op_sel_hi:[0,0,0]
	v_mfma_scale_f32_16x16x128_f8f6f4 v[84:87], v[0:7], v[40:47], v[84:87], v235, v235 op_sel_hi:[0,0,0]
	v_mfma_scale_f32_16x16x128_f8f6f4 v[80:83], v[8:15], v[48:55], v[80:83], v235, v235 op_sel_hi:[0,0,0]
	v_mfma_scale_f32_16x16x128_f8f6f4 v[76:79], v[0:7], v[48:55], v[76:79], v235, v235 op_sel_hi:[0,0,0]
	v_mfma_scale_f32_16x16x128_f8f6f4 v[72:75], v[8:15], v[56:63], v[72:75], v235, v235 op_sel_hi:[0,0,0]
	v_mfma_scale_f32_16x16x128_f8f6f4 v[68:71], v[0:7], v[56:63], v[68:71], v235, v235 op_sel_hi:[0,0,0]
	s_setprio 0
	s_barrier
	ds_read_b128 v[16:19], v233 offset:0x8000
	ds_read_b128 v[20:23], v233 offset:0x8400
	ds_read_b128 v[24:27], v233 offset:0x8800
	ds_read_b128 v[28:31], v233 offset:0x8c00
	ds_read_b128 v[32:35], v232 offset:0x8000
	ds_read_b128 v[36:39], v232 offset:0x8400
	ds_read_b128 v[40:43], v232 offset:0x8800
	ds_read_b128 v[44:47], v232 offset:0x8c00
	ds_read_b128 v[48:51], v232 offset:0x9000
	ds_read_b128 v[52:55], v232 offset:0x9400
	ds_read_b128 v[56:59], v232 offset:0x9800
	ds_read_b128 v[60:63], v232 offset:0x9c00
	ds_read_b128 v[8:11], v233 offset:0xc000
	ds_read_b128 v[12:15], v233 offset:0xc400
	ds_read_b128 v[0:3], v233 offset:0xc800
	ds_read_b128 v[4:7], v233 offset:0xcc00
	s_mov_b32 m0, s62
	s_add_i32 s40, s85, 0x10000
	buffer_load_dwordx4 v230, s[4:7], s40 offen lds
	s_add_i32 s40, s85, 0x18000
	s_mov_b32 m0, s63
	s_nop 0
	buffer_load_dwordx4 v230, s[4:7], s40 offen lds
	s_waitcnt vmcnt(8)
	s_waitcnt lgkmcnt(4)
	s_barrier
	s_setprio 1
	v_mfma_scale_f32_16x16x128_f8f6f4 v[192:195], v[16:23], v[32:39], v[192:195], v235, v235 op_sel_hi:[0,0,0]
	v_mfma_scale_f32_16x16x128_f8f6f4 v[188:191], v[24:31], v[32:39], v[188:191], v235, v235 op_sel_hi:[0,0,0]
	v_mfma_scale_f32_16x16x128_f8f6f4 v[184:187], v[16:23], v[40:47], v[184:187], v235, v235 op_sel_hi:[0,0,0]
	v_mfma_scale_f32_16x16x128_f8f6f4 v[180:183], v[24:31], v[40:47], v[180:183], v235, v235 op_sel_hi:[0,0,0]
	v_mfma_scale_f32_16x16x128_f8f6f4 v[176:179], v[16:23], v[48:55], v[176:179], v235, v235 op_sel_hi:[0,0,0]
	v_mfma_scale_f32_16x16x128_f8f6f4 v[172:175], v[24:31], v[48:55], v[172:175], v235, v235 op_sel_hi:[0,0,0]
	v_mfma_scale_f32_16x16x128_f8f6f4 v[168:171], v[16:23], v[56:63], v[168:171], v235, v235 op_sel_hi:[0,0,0]
	v_mfma_scale_f32_16x16x128_f8f6f4 v[164:167], v[24:31], v[56:63], v[164:167], v235, v235 op_sel_hi:[0,0,0]
	s_waitcnt lgkmcnt(2)
	v_mfma_scale_f32_16x16x128_f8f6f4 v[160:163], v[8:15], v[32:39], v[160:163], v235, v235 op_sel_hi:[0,0,0]
	s_waitcnt lgkmcnt(0)
	v_mfma_scale_f32_16x16x128_f8f6f4 v[156:159], v[0:7], v[32:39], v[156:159], v235, v235 op_sel_hi:[0,0,0]
	v_mfma_scale_f32_16x16x128_f8f6f4 v[152:155], v[8:15], v[40:47], v[152:155], v235, v235 op_sel_hi:[0,0,0]
	v_mfma_scale_f32_16x16x128_f8f6f4 v[148:151], v[0:7], v[40:47], v[148:151], v235, v235 op_sel_hi:[0,0,0]
	v_mfma_scale_f32_16x16x128_f8f6f4 v[144:147], v[8:15], v[48:55], v[144:147], v235, v235 op_sel_hi:[0,0,0]
	v_mfma_scale_f32_16x16x128_f8f6f4 v[140:143], v[0:7], v[48:55], v[140:143], v235, v235 op_sel_hi:[0,0,0]
	v_mfma_scale_f32_16x16x128_f8f6f4 v[136:139], v[8:15], v[56:63], v[136:139], v235, v235 op_sel_hi:[0,0,0]
	v_mfma_scale_f32_16x16x128_f8f6f4 v[132:135], v[0:7], v[56:63], v[132:135], v235, v235 op_sel_hi:[0,0,0]
	s_setprio 0
	s_barrier
	ds_read_b128 v[32:35], v232 offset:0xc000
	ds_read_b128 v[36:39], v232 offset:0xc400
	ds_read_b128 v[40:43], v232 offset:0xc800
	ds_read_b128 v[44:47], v232 offset:0xcc00
	ds_read_b128 v[48:51], v232 offset:0xd000
	ds_read_b128 v[52:55], v232 offset:0xd400
	ds_read_b128 v[56:59], v232 offset:0xd800
	ds_read_b128 v[60:63], v232 offset:0xdc00
	s_mov_b32 m0, s64
	s_add_i32 s40, s86, 0x80
	buffer_load_dwordx4 v231, s[8:11], s40 offen lds
	s_add_i32 s40, s86, 0x10080
	s_mov_b32 m0, s65
	s_nop 0
	buffer_load_dwordx4 v231, s[8:11], s40 offen lds
	s_add_i32 s40, s86, 0x1080
	s_mov_b32 m0, s70
	s_nop 0
	buffer_load_dwordx4 v231, s[8:11], s40 offen lds
	s_add_i32 s40, s86, 0x11080
	s_mov_b32 m0, s71
	s_nop 0
	buffer_load_dwordx4 v231, s[8:11], s40 offen lds
	s_mov_b32 m0, s68
	s_add_i32 s10, s85, 0x8080
	buffer_load_dwordx4 v230, s[4:7], s33 offen lds
	s_mov_b32 m0, s69
	s_nop 0
	buffer_load_dwordx4 v230, s[4:7], s10 offen lds
	s_waitcnt vmcnt(8)
	s_waitcnt lgkmcnt(0)
	s_barrier
	s_setprio 1
	v_mfma_scale_f32_16x16x128_f8f6f4 v[128:131], v[16:23], v[32:39], v[128:131], v235, v235 op_sel_hi:[0,0,0]
	v_mfma_scale_f32_16x16x128_f8f6f4 v[124:127], v[24:31], v[32:39], v[124:127], v235, v235 op_sel_hi:[0,0,0]
	v_mfma_scale_f32_16x16x128_f8f6f4 v[120:123], v[16:23], v[40:47], v[120:123], v235, v235 op_sel_hi:[0,0,0]
	v_mfma_scale_f32_16x16x128_f8f6f4 v[116:119], v[24:31], v[40:47], v[116:119], v235, v235 op_sel_hi:[0,0,0]
	v_mfma_scale_f32_16x16x128_f8f6f4 v[112:115], v[16:23], v[48:55], v[112:115], v235, v235 op_sel_hi:[0,0,0]
	v_mfma_scale_f32_16x16x128_f8f6f4 v[108:111], v[24:31], v[48:55], v[108:111], v235, v235 op_sel_hi:[0,0,0]
	v_mfma_scale_f32_16x16x128_f8f6f4 v[104:107], v[16:23], v[56:63], v[104:107], v235, v235 op_sel_hi:[0,0,0]
	v_mfma_scale_f32_16x16x128_f8f6f4 v[100:103], v[24:31], v[56:63], v[100:103], v235, v235 op_sel_hi:[0,0,0]
	v_mfma_scale_f32_16x16x128_f8f6f4 v[96:99], v[8:15], v[32:39], v[96:99], v235, v235 op_sel_hi:[0,0,0]
	v_mfma_scale_f32_16x16x128_f8f6f4 v[92:95], v[0:7], v[32:39], v[92:95], v235, v235 op_sel_hi:[0,0,0]
	v_mfma_scale_f32_16x16x128_f8f6f4 v[88:91], v[8:15], v[40:47], v[88:91], v235, v235 op_sel_hi:[0,0,0]
	v_mfma_scale_f32_16x16x128_f8f6f4 v[84:87], v[0:7], v[40:47], v[84:87], v235, v235 op_sel_hi:[0,0,0]
	v_mfma_scale_f32_16x16x128_f8f6f4 v[80:83], v[8:15], v[48:55], v[80:83], v235, v235 op_sel_hi:[0,0,0]
	v_mfma_scale_f32_16x16x128_f8f6f4 v[76:79], v[0:7], v[48:55], v[76:79], v235, v235 op_sel_hi:[0,0,0]
	v_mfma_scale_f32_16x16x128_f8f6f4 v[72:75], v[8:15], v[56:63], v[72:75], v235, v235 op_sel_hi:[0,0,0]
	v_mfma_scale_f32_16x16x128_f8f6f4 v[68:71], v[0:7], v[56:63], v[68:71], v235, v235 op_sel_hi:[0,0,0]
	s_setprio 0
	s_barrier
	s_andn2_b64 vcc, exec, s[20:21]
	s_cbranch_vccnz .LBB0_1371
	s_barrier

.LBB0_1449:
	s_add_i32 s33, s80, 0x100
	s_add_i32 s66, s81, 0x100
	s_waitcnt lgkmcnt(0)
	s_barrier
	s_setprio 1
	v_mfma_scale_f32_16x16x128_f8f6f4 v[192:195], v[24:31], v[56:63], 0, v235, v235 op_sel_hi:[0,0,0]
	v_mfma_scale_f32_16x16x128_f8f6f4 v[188:191], v[16:23], v[56:63], 0, v235, v235 op_sel_hi:[0,0,0]
	v_mfma_scale_f32_16x16x128_f8f6f4 v[184:187], v[24:31], v[48:55], 0, v235, v235 op_sel_hi:[0,0,0]
	v_mfma_scale_f32_16x16x128_f8f6f4 v[180:183], v[16:23], v[48:55], 0, v235, v235 op_sel_hi:[0,0,0]
	v_mfma_scale_f32_16x16x128_f8f6f4 v[176:179], v[24:31], v[40:47], 0, v235, v235 op_sel_hi:[0,0,0]
	v_mfma_scale_f32_16x16x128_f8f6f4 v[172:175], v[16:23], v[40:47], 0, v235, v235 op_sel_hi:[0,0,0]
	v_mfma_scale_f32_16x16x128_f8f6f4 v[168:171], v[24:31], v[32:39], 0, v235, v235 op_sel_hi:[0,0,0]
	v_mfma_scale_f32_16x16x128_f8f6f4 v[164:167], v[16:23], v[32:39], 0, v235, v235 op_sel_hi:[0,0,0]
	v_mfma_scale_f32_16x16x128_f8f6f4 v[160:163], v[8:15], v[56:63], 0, v235, v235 op_sel_hi:[0,0,0]
	v_mfma_scale_f32_16x16x128_f8f6f4 v[156:159], v[0:7], v[56:63], 0, v235, v235 op_sel_hi:[0,0,0]
	v_mfma_scale_f32_16x16x128_f8f6f4 v[152:155], v[8:15], v[48:55], 0, v235, v235 op_sel_hi:[0,0,0]
	v_mfma_scale_f32_16x16x128_f8f6f4 v[148:151], v[0:7], v[48:55], 0, v235, v235 op_sel_hi:[0,0,0]
	v_mfma_scale_f32_16x16x128_f8f6f4 v[144:147], v[8:15], v[40:47], 0, v235, v235 op_sel_hi:[0,0,0]
	v_mfma_scale_f32_16x16x128_f8f6f4 v[140:143], v[0:7], v[40:47], 0, v235, v235 op_sel_hi:[0,0,0]
	v_mfma_scale_f32_16x16x128_f8f6f4 v[136:139], v[8:15], v[32:39], 0, v235, v235 op_sel_hi:[0,0,0]
	v_mfma_scale_f32_16x16x128_f8f6f4 v[132:135], v[0:7], v[32:39], 0, v235, v235 op_sel_hi:[0,0,0]
	s_setprio 0
	s_barrier
	s_mov_b32 m0, s46
	s_mov_b32 s10, s6
	s_mov_b32 s11, s7
	ds_read_b128 v[56:59], v232 offset:0x4000
	ds_read_b128 v[60:63], v232 offset:0x4400
	ds_read_b128 v[48:51], v232 offset:0x4800
	ds_read_b128 v[52:55], v232 offset:0x4c00
	ds_read_b128 v[40:43], v232 offset:0x5000
	ds_read_b128 v[44:47], v232 offset:0x5400
	ds_read_b128 v[32:35], v232 offset:0x5800
	ds_read_b128 v[36:39], v232 offset:0x5c00
	buffer_load_dwordx4 v231, s[8:11], s66 offen lds
	s_add_i32 s66, s81, 0x10100
	s_mov_b32 m0, s47
	s_and_b64 vcc, exec, s[36:37]
	buffer_load_dwordx4 v231, s[8:11], s66 offen lds
	s_add_i32 s66, s81, 0x1100
	s_mov_b32 m0, s49
	s_nop 0
	buffer_load_dwordx4 v231, s[8:11], s66 offen lds
	s_add_i32 s66, s81, 0x11100
	s_mov_b32 m0, s50
	s_nop 0
	buffer_load_dwordx4 v231, s[8:11], s66 offen lds
	s_mov_b32 m0, s48
	s_add_i32 s10, s80, 0x8100
	buffer_load_dwordx4 v230, s[4:7], s33 offen lds
	s_mov_b32 m0, s51
	s_nop 0
	buffer_load_dwordx4 v230, s[4:7], s10 offen lds
	s_cbranch_vccz .LBB0_1458
	s_waitcnt vmcnt(37)
	s_cbranch_execnz .LBB0_1452

.LBB0_1452:
	s_add_i32 s33, s80, 0x180
	s_add_i32 s36, s81, 0x180
	s_waitcnt lgkmcnt(0)
	s_barrier
	s_setprio 1
	v_mfma_scale_f32_16x16x128_f8f6f4 v[128:131], v[24:31], v[56:63], 0, v235, v235 op_sel_hi:[0,0,0]
	v_mfma_scale_f32_16x16x128_f8f6f4 v[124:127], v[16:23], v[56:63], 0, v235, v235 op_sel_hi:[0,0,0]
	v_mfma_scale_f32_16x16x128_f8f6f4 v[120:123], v[24:31], v[48:55], 0, v235, v235 op_sel_hi:[0,0,0]
	v_mfma_scale_f32_16x16x128_f8f6f4 v[116:119], v[16:23], v[48:55], 0, v235, v235 op_sel_hi:[0,0,0]
	v_mfma_scale_f32_16x16x128_f8f6f4 v[112:115], v[24:31], v[40:47], 0, v235, v235 op_sel_hi:[0,0,0]
	v_mfma_scale_f32_16x16x128_f8f6f4 v[108:111], v[16:23], v[40:47], 0, v235, v235 op_sel_hi:[0,0,0]
	v_mfma_scale_f32_16x16x128_f8f6f4 v[104:107], v[24:31], v[32:39], 0, v235, v235 op_sel_hi:[0,0,0]
	v_mfma_scale_f32_16x16x128_f8f6f4 v[100:103], v[16:23], v[32:39], 0, v235, v235 op_sel_hi:[0,0,0]
	v_mfma_scale_f32_16x16x128_f8f6f4 v[96:99], v[8:15], v[56:63], 0, v235, v235 op_sel_hi:[0,0,0]
	v_mfma_scale_f32_16x16x128_f8f6f4 v[92:95], v[0:7], v[56:63], 0, v235, v235 op_sel_hi:[0,0,0]
	v_mfma_scale_f32_16x16x128_f8f6f4 v[88:91], v[8:15], v[48:55], 0, v235, v235 op_sel_hi:[0,0,0]
	v_mfma_scale_f32_16x16x128_f8f6f4 v[84:87], v[0:7], v[48:55], 0, v235, v235 op_sel_hi:[0,0,0]
	v_mfma_scale_f32_16x16x128_f8f6f4 v[80:83], v[8:15], v[40:47], 0, v235, v235 op_sel_hi:[0,0,0]
	v_mfma_scale_f32_16x16x128_f8f6f4 v[76:79], v[0:7], v[40:47], 0, v235, v235 op_sel_hi:[0,0,0]
	v_mfma_scale_f32_16x16x128_f8f6f4 v[72:75], v[8:15], v[32:39], 0, v235, v235 op_sel_hi:[0,0,0]
	v_mfma_scale_f32_16x16x128_f8f6f4 v[68:71], v[0:7], v[32:39], 0, v235, v235 op_sel_hi:[0,0,0]
	s_setprio 0
	s_barrier
	ds_read_b128 v[16:19], v233 offset:0x8000
	ds_read_b128 v[20:23], v233 offset:0x8400
	ds_read_b128 v[24:27], v233 offset:0x8800
	ds_read_b128 v[28:31], v233 offset:0x8c00
	ds_read_b128 v[32:35], v232 offset:0x8000
	ds_read_b128 v[36:39], v232 offset:0x8400
	ds_read_b128 v[40:43], v232 offset:0x8800
	ds_read_b128 v[44:47], v232 offset:0x8c00
	ds_read_b128 v[48:51], v232 offset:0x9000
	ds_read_b128 v[52:55], v232 offset:0x9400
	ds_read_b128 v[56:59], v232 offset:0x9800
	ds_read_b128 v[60:63], v232 offset:0x9c00
	ds_read_b128 v[8:11], v233 offset:0xc000
	ds_read_b128 v[12:15], v233 offset:0xc400
	ds_read_b128 v[0:3], v233 offset:0xc800
	ds_read_b128 v[4:7], v233 offset:0xcc00
	s_mov_b32 m0, s62
	s_add_i32 s10, s80, 0x10100
	buffer_load_dwordx4 v230, s[4:7], s10 offen lds
	s_add_i32 s10, s80, 0x18100
	s_mov_b32 m0, s63
	s_nop 0
	buffer_load_dwordx4 v230, s[4:7], s10 offen lds
	s_waitcnt vmcnt(8)
	s_waitcnt lgkmcnt(4)
	s_barrier
	s_setprio 1
	v_mfma_scale_f32_16x16x128_f8f6f4 v[192:195], v[16:23], v[32:39], v[192:195], v235, v235 op_sel_hi:[0,0,0]
	v_mfma_scale_f32_16x16x128_f8f6f4 v[188:191], v[24:31], v[32:39], v[188:191], v235, v235 op_sel_hi:[0,0,0]
	v_mfma_scale_f32_16x16x128_f8f6f4 v[184:187], v[16:23], v[40:47], v[184:187], v235, v235 op_sel_hi:[0,0,0]
	v_mfma_scale_f32_16x16x128_f8f6f4 v[180:183], v[24:31], v[40:47], v[180:183], v235, v235 op_sel_hi:[0,0,0]
	v_mfma_scale_f32_16x16x128_f8f6f4 v[176:179], v[16:23], v[48:55], v[176:179], v235, v235 op_sel_hi:[0,0,0]
	v_mfma_scale_f32_16x16x128_f8f6f4 v[172:175], v[24:31], v[48:55], v[172:175], v235, v235 op_sel_hi:[0,0,0]
	v_mfma_scale_f32_16x16x128_f8f6f4 v[168:171], v[16:23], v[56:63], v[168:171], v235, v235 op_sel_hi:[0,0,0]
	v_mfma_scale_f32_16x16x128_f8f6f4 v[164:167], v[24:31], v[56:63], v[164:167], v235, v235 op_sel_hi:[0,0,0]
	s_waitcnt lgkmcnt(2)
	v_mfma_scale_f32_16x16x128_f8f6f4 v[160:163], v[8:15], v[32:39], v[160:163], v235, v235 op_sel_hi:[0,0,0]
	s_waitcnt lgkmcnt(0)
	v_mfma_scale_f32_16x16x128_f8f6f4 v[156:159], v[0:7], v[32:39], v[156:159], v235, v235 op_sel_hi:[0,0,0]
	v_mfma_scale_f32_16x16x128_f8f6f4 v[152:155], v[8:15], v[40:47], v[152:155], v235, v235 op_sel_hi:[0,0,0]
	v_mfma_scale_f32_16x16x128_f8f6f4 v[148:151], v[0:7], v[40:47], v[148:151], v235, v235 op_sel_hi:[0,0,0]
	v_mfma_scale_f32_16x16x128_f8f6f4 v[144:147], v[8:15], v[48:55], v[144:147], v235, v235 op_sel_hi:[0,0,0]
	v_mfma_scale_f32_16x16x128_f8f6f4 v[140:143], v[0:7], v[48:55], v[140:143], v235, v235 op_sel_hi:[0,0,0]
	v_mfma_scale_f32_16x16x128_f8f6f4 v[136:139], v[8:15], v[56:63], v[136:139], v235, v235 op_sel_hi:[0,0,0]
	v_mfma_scale_f32_16x16x128_f8f6f4 v[132:135], v[0:7], v[56:63], v[132:135], v235, v235 op_sel_hi:[0,0,0]
	s_setprio 0
	s_barrier
	ds_read_b128 v[32:35], v232 offset:0xc000
	ds_read_b128 v[36:39], v232 offset:0xc400
	ds_read_b128 v[40:43], v232 offset:0xc800
	ds_read_b128 v[44:47], v232 offset:0xcc00
	ds_read_b128 v[48:51], v232 offset:0xd000
	ds_read_b128 v[52:55], v232 offset:0xd400
	ds_read_b128 v[56:59], v232 offset:0xd800
	ds_read_b128 v[60:63], v232 offset:0xdc00
	s_mov_b32 m0, s64
	s_mov_b32 s10, s6
	s_mov_b32 s11, s7
	buffer_load_dwordx4 v231, s[8:11], s36 offen lds
	s_add_i32 s36, s81, 0x10180
	s_mov_b32 m0, s65
	s_nop 0
	buffer_load_dwordx4 v231, s[8:11], s36 offen lds
	s_add_i32 s36, s81, 0x1180
	s_mov_b32 m0, s70
	s_nop 0
	buffer_load_dwordx4 v231, s[8:11], s36 offen lds
	s_add_i32 s36, s81, 0x11180
	s_mov_b32 m0, s71
	s_nop 0
	buffer_load_dwordx4 v231, s[8:11], s36 offen lds
	s_mov_b32 m0, s68
	s_nop 0
	buffer_load_dwordx4 v230, s[4:7], s33 offen lds
	s_add_i32 s33, s80, 0x8180
	s_mov_b32 m0, s69
	s_nop 0
	buffer_load_dwordx4 v230, s[4:7], s33 offen lds
	s_waitcnt vmcnt(8)
	s_waitcnt lgkmcnt(0)
	s_barrier
	s_setprio 1
	v_mfma_scale_f32_16x16x128_f8f6f4 v[128:131], v[16:23], v[32:39], v[128:131], v235, v235 op_sel_hi:[0,0,0]
	v_mfma_scale_f32_16x16x128_f8f6f4 v[124:127], v[24:31], v[32:39], v[124:127], v235, v235 op_sel_hi:[0,0,0]
	v_mfma_scale_f32_16x16x128_f8f6f4 v[120:123], v[16:23], v[40:47], v[120:123], v235, v235 op_sel_hi:[0,0,0]
	v_mfma_scale_f32_16x16x128_f8f6f4 v[116:119], v[24:31], v[40:47], v[116:119], v235, v235 op_sel_hi:[0,0,0]
	v_mfma_scale_f32_16x16x128_f8f6f4 v[112:115], v[16:23], v[48:55], v[112:115], v235, v235 op_sel_hi:[0,0,0]
	v_mfma_scale_f32_16x16x128_f8f6f4 v[108:111], v[24:31], v[48:55], v[108:111], v235, v235 op_sel_hi:[0,0,0]
	v_mfma_scale_f32_16x16x128_f8f6f4 v[104:107], v[16:23], v[56:63], v[104:107], v235, v235 op_sel_hi:[0,0,0]
	v_mfma_scale_f32_16x16x128_f8f6f4 v[100:103], v[24:31], v[56:63], v[100:103], v235, v235 op_sel_hi:[0,0,0]
	v_mfma_scale_f32_16x16x128_f8f6f4 v[96:99], v[8:15], v[32:39], v[96:99], v235, v235 op_sel_hi:[0,0,0]
	v_mfma_scale_f32_16x16x128_f8f6f4 v[92:95], v[0:7], v[32:39], v[92:95], v235, v235 op_sel_hi:[0,0,0]
	v_mfma_scale_f32_16x16x128_f8f6f4 v[88:91], v[8:15], v[40:47], v[88:91], v235, v235 op_sel_hi:[0,0,0]
	v_mfma_scale_f32_16x16x128_f8f6f4 v[84:87], v[0:7], v[40:47], v[84:87], v235, v235 op_sel_hi:[0,0,0]
	v_mfma_scale_f32_16x16x128_f8f6f4 v[80:83], v[8:15], v[48:55], v[80:83], v235, v235 op_sel_hi:[0,0,0]
	v_mfma_scale_f32_16x16x128_f8f6f4 v[76:79], v[0:7], v[48:55], v[76:79], v235, v235 op_sel_hi:[0,0,0]
	v_mfma_scale_f32_16x16x128_f8f6f4 v[72:75], v[8:15], v[56:63], v[72:75], v235, v235 op_sel_hi:[0,0,0]
	v_mfma_scale_f32_16x16x128_f8f6f4 v[68:71], v[0:7], v[56:63], v[68:71], v235, v235 op_sel_hi:[0,0,0]
	s_setprio 0
	s_barrier
	ds_read_b128 v[16:19], v233 offset:0
	ds_read_b128 v[20:23], v233 offset:0x400
	ds_read_b128 v[24:27], v233 offset:0x800
	ds_read_b128 v[28:31], v233 offset:0xc00
	ds_read_b128 v[32:35], v232 offset:0
	ds_read_b128 v[36:39], v232 offset:0x400
	ds_read_b128 v[40:43], v232 offset:0x800
	ds_read_b128 v[44:47], v232 offset:0xc00
	ds_read_b128 v[48:51], v232 offset:0x1000
	ds_read_b128 v[52:55], v232 offset:0x1400
	ds_read_b128 v[56:59], v232 offset:0x1800
	ds_read_b128 v[60:63], v232 offset:0x1c00
	ds_read_b128 v[8:11], v233 offset:0x4000
	ds_read_b128 v[12:15], v233 offset:0x4400
	ds_read_b128 v[0:3], v233 offset:0x4800
	ds_read_b128 v[4:7], v233 offset:0x4c00
	s_add_i32 s33, s43, 0x80
	s_mov_b32 m0, s74
	s_add_i32 s36, s80, 0x10180
	buffer_load_dwordx4 v230, s[4:7], s36 offen lds
	s_add_i32 s36, s80, 0x18180
	s_mov_b32 m0, s76
	s_nop 0
	buffer_load_dwordx4 v230, s[4:7], s36 offen lds
	s_waitcnt vmcnt(8)
	s_waitcnt lgkmcnt(4)
	s_barrier
	s_setprio 1
	v_mfma_scale_f32_16x16x128_f8f6f4 v[192:195], v[16:23], v[32:39], v[192:195], v235, v235 op_sel_hi:[0,0,0]
	v_mfma_scale_f32_16x16x128_f8f6f4 v[188:191], v[24:31], v[32:39], v[188:191], v235, v235 op_sel_hi:[0,0,0]
	v_mfma_scale_f32_16x16x128_f8f6f4 v[184:187], v[16:23], v[40:47], v[184:187], v235, v235 op_sel_hi:[0,0,0]
	v_mfma_scale_f32_16x16x128_f8f6f4 v[180:183], v[24:31], v[40:47], v[180:183], v235, v235 op_sel_hi:[0,0,0]
	v_mfma_scale_f32_16x16x128_f8f6f4 v[176:179], v[16:23], v[48:55], v[176:179], v235, v235 op_sel_hi:[0,0,0]
	v_mfma_scale_f32_16x16x128_f8f6f4 v[172:175], v[24:31], v[48:55], v[172:175], v235, v235 op_sel_hi:[0,0,0]
	v_mfma_scale_f32_16x16x128_f8f6f4 v[168:171], v[16:23], v[56:63], v[168:171], v235, v235 op_sel_hi:[0,0,0]
	v_mfma_scale_f32_16x16x128_f8f6f4 v[164:167], v[24:31], v[56:63], v[164:167], v235, v235 op_sel_hi:[0,0,0]
	s_waitcnt lgkmcnt(2)
	v_mfma_scale_f32_16x16x128_f8f6f4 v[160:163], v[8:15], v[32:39], v[160:163], v235, v235 op_sel_hi:[0,0,0]
	s_waitcnt lgkmcnt(0)
	v_mfma_scale_f32_16x16x128_f8f6f4 v[156:159], v[0:7], v[32:39], v[156:159], v235, v235 op_sel_hi:[0,0,0]
	v_mfma_scale_f32_16x16x128_f8f6f4 v[152:155], v[8:15], v[40:47], v[152:155], v235, v235 op_sel_hi:[0,0,0]
	v_mfma_scale_f32_16x16x128_f8f6f4 v[148:151], v[0:7], v[40:47], v[148:151], v235, v235 op_sel_hi:[0,0,0]
	v_mfma_scale_f32_16x16x128_f8f6f4 v[144:147], v[8:15], v[48:55], v[144:147], v235, v235 op_sel_hi:[0,0,0]
	v_mfma_scale_f32_16x16x128_f8f6f4 v[140:143], v[0:7], v[48:55], v[140:143], v235, v235 op_sel_hi:[0,0,0]
	v_mfma_scale_f32_16x16x128_f8f6f4 v[136:139], v[8:15], v[56:63], v[136:139], v235, v235 op_sel_hi:[0,0,0]
	v_mfma_scale_f32_16x16x128_f8f6f4 v[132:135], v[0:7], v[56:63], v[132:135], v235, v235 op_sel_hi:[0,0,0]
	s_setprio 0
	s_barrier
	ds_read_b128 v[32:35], v232 offset:0x4000
	ds_read_b128 v[36:39], v232 offset:0x4400
	ds_read_b128 v[40:43], v232 offset:0x4800
	ds_read_b128 v[44:47], v232 offset:0x4c00
	ds_read_b128 v[48:51], v232 offset:0x5000
	ds_read_b128 v[52:55], v232 offset:0x5400
	ds_read_b128 v[56:59], v232 offset:0x5800
	ds_read_b128 v[60:63], v232 offset:0x5c00
	s_mov_b32 m0, s46
	s_nop 0
	buffer_load_dwordx4 v231, s[8:11], s78 offen lds
	s_add_i32 s36, s78, 0x10000
	s_mov_b32 m0, s47
	s_nop 0
	buffer_load_dwordx4 v231, s[8:11], s36 offen lds
	s_add_i32 s36, s78, 0x1000
	s_mov_b32 m0, s49
	s_nop 0
	buffer_load_dwordx4 v231, s[8:11], s36 offen lds
	s_add_i32 s36, s78, 0x11000
	s_mov_b32 m0, s50
	s_nop 0
	buffer_load_dwordx4 v231, s[8:11], s36 offen lds
	s_mov_b32 m0, s48
	s_add_i32 s36, s43, 0x8000
	buffer_load_dwordx4 v230, s[4:7], s43 offen lds
	s_mov_b32 m0, s51
	s_nop 0
	buffer_load_dwordx4 v230, s[4:7], s36 offen lds
	s_waitcnt vmcnt(8)
	s_waitcnt lgkmcnt(0)
	s_barrier
	s_setprio 1
	v_mfma_scale_f32_16x16x128_f8f6f4 v[128:131], v[16:23], v[32:39], v[128:131], v235, v235 op_sel_hi:[0,0,0]
	v_mfma_scale_f32_16x16x128_f8f6f4 v[124:127], v[24:31], v[32:39], v[124:127], v235, v235 op_sel_hi:[0,0,0]
	v_mfma_scale_f32_16x16x128_f8f6f4 v[120:123], v[16:23], v[40:47], v[120:123], v235, v235 op_sel_hi:[0,0,0]
	v_mfma_scale_f32_16x16x128_f8f6f4 v[116:119], v[24:31], v[40:47], v[116:119], v235, v235 op_sel_hi:[0,0,0]
	v_mfma_scale_f32_16x16x128_f8f6f4 v[112:115], v[16:23], v[48:55], v[112:115], v235, v235 op_sel_hi:[0,0,0]
	v_mfma_scale_f32_16x16x128_f8f6f4 v[108:111], v[24:31], v[48:55], v[108:111], v235, v235 op_sel_hi:[0,0,0]
	v_mfma_scale_f32_16x16x128_f8f6f4 v[104:107], v[16:23], v[56:63], v[104:107], v235, v235 op_sel_hi:[0,0,0]
	v_mfma_scale_f32_16x16x128_f8f6f4 v[100:103], v[24:31], v[56:63], v[100:103], v235, v235 op_sel_hi:[0,0,0]
	v_mfma_scale_f32_16x16x128_f8f6f4 v[96:99], v[8:15], v[32:39], v[96:99], v235, v235 op_sel_hi:[0,0,0]
	v_mfma_scale_f32_16x16x128_f8f6f4 v[92:95], v[0:7], v[32:39], v[92:95], v235, v235 op_sel_hi:[0,0,0]
	v_mfma_scale_f32_16x16x128_f8f6f4 v[88:91], v[8:15], v[40:47], v[88:91], v235, v235 op_sel_hi:[0,0,0]
	v_mfma_scale_f32_16x16x128_f8f6f4 v[84:87], v[0:7], v[40:47], v[84:87], v235, v235 op_sel_hi:[0,0,0]
	v_mfma_scale_f32_16x16x128_f8f6f4 v[80:83], v[8:15], v[48:55], v[80:83], v235, v235 op_sel_hi:[0,0,0]
	v_mfma_scale_f32_16x16x128_f8f6f4 v[76:79], v[0:7], v[48:55], v[76:79], v235, v235 op_sel_hi:[0,0,0]
	v_mfma_scale_f32_16x16x128_f8f6f4 v[72:75], v[8:15], v[56:63], v[72:75], v235, v235 op_sel_hi:[0,0,0]
	v_mfma_scale_f32_16x16x128_f8f6f4 v[68:71], v[0:7], v[56:63], v[68:71], v235, v235 op_sel_hi:[0,0,0]
	s_setprio 0
	s_barrier
	ds_read_b128 v[16:19], v233 offset:0x8000
	ds_read_b128 v[20:23], v233 offset:0x8400
	ds_read_b128 v[24:27], v233 offset:0x8800
	ds_read_b128 v[28:31], v233 offset:0x8c00
	ds_read_b128 v[32:35], v232 offset:0x8000
	ds_read_b128 v[36:39], v232 offset:0x8400
	ds_read_b128 v[40:43], v232 offset:0x8800
	ds_read_b128 v[44:47], v232 offset:0x8c00
	ds_read_b128 v[48:51], v232 offset:0x9000
	ds_read_b128 v[52:55], v232 offset:0x9400
	ds_read_b128 v[56:59], v232 offset:0x9800
	ds_read_b128 v[60:63], v232 offset:0x9c00
	ds_read_b128 v[8:11], v233 offset:0xc000
	ds_read_b128 v[12:15], v233 offset:0xc400
	ds_read_b128 v[0:3], v233 offset:0xc800
	ds_read_b128 v[4:7], v233 offset:0xcc00
	s_mov_b32 m0, s62
	s_add_i32 s36, s43, 0x10000
	buffer_load_dwordx4 v230, s[4:7], s36 offen lds
	s_add_i32 s36, s43, 0x18000
	s_mov_b32 m0, s63
	s_nop 0
	buffer_load_dwordx4 v230, s[4:7], s36 offen lds
	s_waitcnt vmcnt(8)
	s_waitcnt lgkmcnt(4)
	s_barrier
	s_setprio 1
	v_mfma_scale_f32_16x16x128_f8f6f4 v[192:195], v[16:23], v[32:39], v[192:195], v235, v235 op_sel_hi:[0,0,0]
	v_mfma_scale_f32_16x16x128_f8f6f4 v[188:191], v[24:31], v[32:39], v[188:191], v235, v235 op_sel_hi:[0,0,0]
	v_mfma_scale_f32_16x16x128_f8f6f4 v[184:187], v[16:23], v[40:47], v[184:187], v235, v235 op_sel_hi:[0,0,0]
	v_mfma_scale_f32_16x16x128_f8f6f4 v[180:183], v[24:31], v[40:47], v[180:183], v235, v235 op_sel_hi:[0,0,0]
	v_mfma_scale_f32_16x16x128_f8f6f4 v[176:179], v[16:23], v[48:55], v[176:179], v235, v235 op_sel_hi:[0,0,0]
	v_mfma_scale_f32_16x16x128_f8f6f4 v[172:175], v[24:31], v[48:55], v[172:175], v235, v235 op_sel_hi:[0,0,0]
	v_mfma_scale_f32_16x16x128_f8f6f4 v[168:171], v[16:23], v[56:63], v[168:171], v235, v235 op_sel_hi:[0,0,0]
	v_mfma_scale_f32_16x16x128_f8f6f4 v[164:167], v[24:31], v[56:63], v[164:167], v235, v235 op_sel_hi:[0,0,0]
	s_waitcnt lgkmcnt(2)
	v_mfma_scale_f32_16x16x128_f8f6f4 v[160:163], v[8:15], v[32:39], v[160:163], v235, v235 op_sel_hi:[0,0,0]
	s_waitcnt lgkmcnt(0)
	v_mfma_scale_f32_16x16x128_f8f6f4 v[156:159], v[0:7], v[32:39], v[156:159], v235, v235 op_sel_hi:[0,0,0]
	v_mfma_scale_f32_16x16x128_f8f6f4 v[152:155], v[8:15], v[40:47], v[152:155], v235, v235 op_sel_hi:[0,0,0]
	v_mfma_scale_f32_16x16x128_f8f6f4 v[148:151], v[0:7], v[40:47], v[148:151], v235, v235 op_sel_hi:[0,0,0]
	v_mfma_scale_f32_16x16x128_f8f6f4 v[144:147], v[8:15], v[48:55], v[144:147], v235, v235 op_sel_hi:[0,0,0]
	v_mfma_scale_f32_16x16x128_f8f6f4 v[140:143], v[0:7], v[48:55], v[140:143], v235, v235 op_sel_hi:[0,0,0]
	v_mfma_scale_f32_16x16x128_f8f6f4 v[136:139], v[8:15], v[56:63], v[136:139], v235, v235 op_sel_hi:[0,0,0]
	v_mfma_scale_f32_16x16x128_f8f6f4 v[132:135], v[0:7], v[56:63], v[132:135], v235, v235 op_sel_hi:[0,0,0]
	s_setprio 0
	s_barrier
	ds_read_b128 v[32:35], v232 offset:0xc000
	ds_read_b128 v[36:39], v232 offset:0xc400
	ds_read_b128 v[40:43], v232 offset:0xc800
	ds_read_b128 v[44:47], v232 offset:0xcc00
	ds_read_b128 v[48:51], v232 offset:0xd000
	ds_read_b128 v[52:55], v232 offset:0xd400
	ds_read_b128 v[56:59], v232 offset:0xd800
	ds_read_b128 v[60:63], v232 offset:0xdc00
	s_mov_b32 m0, s64
	s_add_i32 s36, s78, 0x80
	buffer_load_dwordx4 v231, s[8:11], s36 offen lds
	s_add_i32 s36, s78, 0x10080
	s_mov_b32 m0, s65
	s_nop 0
	buffer_load_dwordx4 v231, s[8:11], s36 offen lds
	s_add_i32 s36, s78, 0x1080
	s_mov_b32 m0, s70
	s_nop 0
	buffer_load_dwordx4 v231, s[8:11], s36 offen lds
	s_add_i32 s36, s78, 0x11080
	s_mov_b32 m0, s71
	s_nop 0
	buffer_load_dwordx4 v231, s[8:11], s36 offen lds
	s_mov_b32 m0, s68
	s_add_i32 s10, s43, 0x8080
	buffer_load_dwordx4 v230, s[4:7], s33 offen lds
	s_mov_b32 m0, s69
	s_nop 0
	buffer_load_dwordx4 v230, s[4:7], s10 offen lds
	s_waitcnt vmcnt(8)
	s_waitcnt lgkmcnt(0)
	s_barrier
	s_setprio 1
	v_mfma_scale_f32_16x16x128_f8f6f4 v[128:131], v[16:23], v[32:39], v[128:131], v235, v235 op_sel_hi:[0,0,0]
	v_mfma_scale_f32_16x16x128_f8f6f4 v[124:127], v[24:31], v[32:39], v[124:127], v235, v235 op_sel_hi:[0,0,0]
	v_mfma_scale_f32_16x16x128_f8f6f4 v[120:123], v[16:23], v[40:47], v[120:123], v235, v235 op_sel_hi:[0,0,0]
	v_mfma_scale_f32_16x16x128_f8f6f4 v[116:119], v[24:31], v[40:47], v[116:119], v235, v235 op_sel_hi:[0,0,0]
	v_mfma_scale_f32_16x16x128_f8f6f4 v[112:115], v[16:23], v[48:55], v[112:115], v235, v235 op_sel_hi:[0,0,0]
	v_mfma_scale_f32_16x16x128_f8f6f4 v[108:111], v[24:31], v[48:55], v[108:111], v235, v235 op_sel_hi:[0,0,0]
	v_mfma_scale_f32_16x16x128_f8f6f4 v[104:107], v[16:23], v[56:63], v[104:107], v235, v235 op_sel_hi:[0,0,0]
	v_mfma_scale_f32_16x16x128_f8f6f4 v[100:103], v[24:31], v[56:63], v[100:103], v235, v235 op_sel_hi:[0,0,0]
	v_mfma_scale_f32_16x16x128_f8f6f4 v[96:99], v[8:15], v[32:39], v[96:99], v235, v235 op_sel_hi:[0,0,0]
	v_mfma_scale_f32_16x16x128_f8f6f4 v[92:95], v[0:7], v[32:39], v[92:95], v235, v235 op_sel_hi:[0,0,0]
	v_mfma_scale_f32_16x16x128_f8f6f4 v[88:91], v[8:15], v[40:47], v[88:91], v235, v235 op_sel_hi:[0,0,0]
	v_mfma_scale_f32_16x16x128_f8f6f4 v[84:87], v[0:7], v[40:47], v[84:87], v235, v235 op_sel_hi:[0,0,0]
	v_mfma_scale_f32_16x16x128_f8f6f4 v[80:83], v[8:15], v[48:55], v[80:83], v235, v235 op_sel_hi:[0,0,0]
	v_mfma_scale_f32_16x16x128_f8f6f4 v[76:79], v[0:7], v[48:55], v[76:79], v235, v235 op_sel_hi:[0,0,0]
	v_mfma_scale_f32_16x16x128_f8f6f4 v[72:75], v[8:15], v[56:63], v[72:75], v235, v235 op_sel_hi:[0,0,0]
	v_mfma_scale_f32_16x16x128_f8f6f4 v[68:71], v[0:7], v[56:63], v[68:71], v235, v235 op_sel_hi:[0,0,0]
	s_setprio 0
	s_barrier
	s_andn2_b64 vcc, exec, s[20:21]
	s_cbranch_vccnz .LBB0_1454
	s_barrier
